# GEMM K-loops: LDS-DMA issue balanced 4+4 per load segment (was 2+6), vmcnt recounted; plus MLA loop reschedule and wide epilogue stores
# speedup vs baseline: 1.0033x; 1.0033x over previous
.LBB0_173:
	s_mov_b32 s99, 0
	v_readlane_b32 s0, v253, 11
	v_readlane_b32 s1, v253, 12
	s_mov_b32 s3, s1
	s_cmp_lt_i32 s0, 4
	s_cselect_b64 s[0:1], -1, 0
	s_cmp_gt_i32 s3, 3
	s_cselect_b64 s[4:5], -1, 0
	s_and_b64 s[0:1], s[0:1], s[4:5]
	s_andn2_b64 vcc, exec, s[0:1]
	s_cbranch_vccnz .LBB0_260
	v_readlane_b32 s6, v253, 0
	v_readlane_b32 s7, v253, 1
	s_load_dwordx2 s[14:15], s[6:7], 0xc0
	s_load_dwordx4 s[16:19], s[6:7], 0xb0
	s_load_dwordx2 s[20:21], s[6:7], 0xd0
	s_cmpk_lt_i32 s2, 0x145
	s_cselect_b64 s[8:9], -1, 0
	v_mov_b32_e32 v10, v0
	s_and_b64 vcc, exec, s[8:9]
	v_readfirstlane_b32 s10, v10
	s_cbranch_vccz .LBB0_176
	s_ashr_i32 s0, s2, 31
	s_lshr_b32 s0, s0, 29
	s_add_i32 s0, s2, s0
	s_and_b32 s1, s0, -8
	s_sub_i32 s1, s2, s1
	s_mul_i32 s4, s1, 40
	s_or_b32 s4, s4, 5
	s_ashr_i32 s0, s0, 3
	s_mul_i32 s3, s1, 41
	s_cmp_lt_i32 s1, 5
	s_cselect_b32 s1, s3, s4
	s_add_i32 s1, s1, s0
	s_mul_hi_i32 s0, s1, 0x66666667
	s_lshr_b32 s3, s0, 31
	s_ashr_i32 s0, s0, 4
	s_add_i32 s0, s0, s3
	s_lshl_b32 s3, s0, 3
	s_sub_i32 s4, 0x41, s3
	s_mul_i32 s0, s0, 40
	s_min_u32 s4, s4, 8
	s_sub_i32 s5, s1, s0
	s_sext_i32_i8 s0, s5
	v_cvt_f32_ubyte0_e32 v2, s4
	v_cvt_f32_i32_e32 v1, s0
	v_rcp_iflag_f32_e32 v3, v2
	s_ashr_i32 s0, s0, 30
	s_or_b32 s11, s0, 1
	v_mul_f32_e32 v3, v1, v3
	v_trunc_f32_e32 v3, v3
	v_fma_f32 v1, -v3, v2, v1
	v_cvt_i32_f32_e32 v3, v3
	v_cmp_ge_f32_e64 s[0:1], |v1|, v2
	s_and_b64 s[0:1], s[0:1], exec
	s_cselect_b32 s0, s11, 0
	v_readfirstlane_b32 s1, v3
	s_add_i32 s0, s1, s0
	s_sext_i32_i8 s50, s0
	s_mul_i32 s0, s0, s4
	s_sub_i32 s0, s5, s0
	s_sext_i32_i8 s0, s0
	s_add_i32 s26, s3, s0

.LBB0_189:
	s_cmp_eq_u32 s99, 0
	s_cbranch_scc1 .Lbal_skip_189
	s_mov_b32 m0, s69
	s_nop 0
	global_load_lds_dwordx4 v[240:241], off
	s_mov_b32 m0, s70
	s_nop 0
	global_load_lds_dwordx4 v[242:243], off
.Lbal_skip_189:
	ds_read_b128 v[156:159], v165
	ds_read_b128 v[170:173], v165 offset:1024
	ds_read_b128 v[174:177], v165 offset:2048
	ds_read_b128 v[178:181], v165 offset:3072
	ds_read_b128 v[182:185], v166
	ds_read_b128 v[186:189], v166 offset:1024
	ds_read_b128 v[190:193], v166 offset:2048
	ds_read_b128 v[194:197], v166 offset:3072
	s_add_u32 s54, s52, 0xfff80080
	s_addc_u32 s55, s53, -1
	s_cmp_eq_u32 s83, 28
	s_cselect_b32 s57, s45, s55
	s_cselect_b32 s56, s51, s54
	s_cselect_b32 s55, s43, s82
	s_cselect_b32 s54, s80, s81
	v_lshl_add_u64 v[230:231], s[52:53], 0, v[148:149]
	s_add_i32 m0, s58, 0xc000
	ds_read_b128 v[198:201], v167
	ds_read_b128 v[202:205], v167 offset:1024
	ds_read_b128 v[206:209], v167 offset:2048
	ds_read_b128 v[210:213], v167 offset:3072
	ds_read_b128 v[214:217], v167 offset:4096
	ds_read_b128 v[218:221], v167 offset:5120
	ds_read_b128 v[222:225], v167 offset:6144
	ds_read_b128 v[226:229], v167 offset:7168
	global_load_lds_dwordx4 v[230:231], off
	v_lshl_add_u64 v[230:231], s[52:53], 0, v[150:151]
	s_add_i32 m0, s58, 0xe000
	s_nop 0
	global_load_lds_dwordx4 v[230:231], off
	s_waitcnt vmcnt(8)
	s_waitcnt lgkmcnt(0)
	s_barrier
	s_setprio 1
	s_waitcnt lgkmcnt(0)
	v_mfma_f32_16x16x32_bf16 v[70:73], v[156:159], v[198:201], v[70:73]
	v_mfma_f32_16x16x32_bf16 v[66:69], v[174:177], v[198:201], v[66:69]
	v_mfma_f32_16x16x32_bf16 v[54:57], v[156:159], v[206:209], v[54:57]
	v_mfma_f32_16x16x32_bf16 v[50:53], v[174:177], v[206:209], v[50:53]
	v_mfma_f32_16x16x32_bf16 v[46:49], v[156:159], v[214:217], v[46:49]
	v_mfma_f32_16x16x32_bf16 v[42:45], v[174:177], v[214:217], v[42:45]
	v_mfma_f32_16x16x32_bf16 v[38:41], v[156:159], v[222:225], v[38:41]
	v_mfma_f32_16x16x32_bf16 v[34:37], v[174:177], v[222:225], v[34:37]
	v_mfma_f32_16x16x32_bf16 v[70:73], v[170:173], v[202:205], v[70:73]
	v_mfma_f32_16x16x32_bf16 v[66:69], v[178:181], v[202:205], v[66:69]
	v_mfma_f32_16x16x32_bf16 v[54:57], v[170:173], v[210:213], v[54:57]
	v_mfma_f32_16x16x32_bf16 v[50:53], v[178:181], v[210:213], v[50:53]
	v_mfma_f32_16x16x32_bf16 v[46:49], v[170:173], v[218:221], v[46:49]
	v_mfma_f32_16x16x32_bf16 v[42:45], v[178:181], v[218:221], v[42:45]
	v_mfma_f32_16x16x32_bf16 v[38:41], v[170:173], v[226:229], v[38:41]
	v_mfma_f32_16x16x32_bf16 v[34:37], v[178:181], v[226:229], v[34:37]
	s_setprio 0
	s_setprio 1
	v_mfma_f32_16x16x32_bf16 v[126:129], v[182:185], v[198:201], v[126:129]
	v_mfma_f32_16x16x32_bf16 v[122:125], v[190:193], v[198:201], v[122:125]
	v_mfma_f32_16x16x32_bf16 v[118:121], v[182:185], v[206:209], v[118:121]
	v_mfma_f32_16x16x32_bf16 v[114:117], v[190:193], v[206:209], v[114:117]
	v_mfma_f32_16x16x32_bf16 v[110:113], v[182:185], v[214:217], v[110:113]
	v_mfma_f32_16x16x32_bf16 v[106:109], v[190:193], v[214:217], v[106:109]
	v_mfma_f32_16x16x32_bf16 v[102:105], v[182:185], v[222:225], v[102:105]
	v_mfma_f32_16x16x32_bf16 v[98:101], v[190:193], v[222:225], v[98:101]
	v_mfma_f32_16x16x32_bf16 v[126:129], v[186:189], v[202:205], v[126:129]
	v_mfma_f32_16x16x32_bf16 v[122:125], v[194:197], v[202:205], v[122:125]
	v_mfma_f32_16x16x32_bf16 v[118:121], v[186:189], v[210:213], v[118:121]
	v_mfma_f32_16x16x32_bf16 v[114:117], v[194:197], v[210:213], v[114:117]
	v_mfma_f32_16x16x32_bf16 v[110:113], v[186:189], v[218:221], v[110:113]
	v_mfma_f32_16x16x32_bf16 v[106:109], v[194:197], v[218:221], v[106:109]
	v_mfma_f32_16x16x32_bf16 v[102:105], v[186:189], v[226:229], v[102:105]
	v_mfma_f32_16x16x32_bf16 v[98:101], v[194:197], v[226:229], v[98:101]
	s_setprio 0
	s_barrier
	s_add_i32 s84, s71, s5
	v_lshl_add_u64 v[230:231], s[54:55], 0, v[132:133]
	s_mov_b32 m0, s84
	ds_read_b128 v[198:201], v167 offset:16384
	ds_read_b128 v[202:205], v167 offset:17408
	ds_read_b128 v[206:209], v167 offset:18432
	ds_read_b128 v[210:213], v167 offset:19456
	ds_read_b128 v[214:217], v167 offset:20480
	ds_read_b128 v[218:221], v167 offset:21504
	ds_read_b128 v[222:225], v167 offset:22528
	ds_read_b128 v[226:229], v167 offset:23552
	global_load_lds_dwordx4 v[230:231], off
	s_add_i32 m0, s84, 0x2000
	s_add_u32 s84, s54, 0x80000
	v_lshl_add_u64 v[232:233], s[54:55], 0, v[136:137]
	s_addc_u32 s85, s55, 0
	s_add_i32 s86, s72, s5
	global_load_lds_dwordx4 v[232:233], off
	v_lshl_add_u64 v[234:235], s[84:85], 0, v[132:133]
	s_mov_b32 m0, s86
	v_lshl_add_u64 v[236:237], s[56:57], 0, v[134:135]
	global_load_lds_dwordx4 v[234:235], off
	v_lshl_add_u64 v[234:235], s[84:85], 0, v[136:137]
	s_add_i32 m0, s86, 0x2000
	s_nop 0
	global_load_lds_dwordx4 v[234:235], off
	s_waitcnt vmcnt(6)
	s_waitcnt lgkmcnt(0)
	s_barrier
	s_setprio 1
	s_waitcnt lgkmcnt(0)
	v_mfma_f32_16x16x32_bf16 v[30:33], v[156:159], v[198:201], v[30:33]
	v_mfma_f32_16x16x32_bf16 v[26:29], v[174:177], v[198:201], v[26:29]
	v_mfma_f32_16x16x32_bf16 v[22:25], v[156:159], v[206:209], v[22:25]
	v_mfma_f32_16x16x32_bf16 v[18:21], v[174:177], v[206:209], v[18:21]
	v_mfma_f32_16x16x32_bf16 v[14:17], v[156:159], v[214:217], v[14:17]
	v_mfma_f32_16x16x32_bf16 v[10:13], v[174:177], v[214:217], v[10:13]
	v_mfma_f32_16x16x32_bf16 v[6:9], v[156:159], v[222:225], v[6:9]
	v_mfma_f32_16x16x32_bf16 v[2:5], v[174:177], v[222:225], v[2:5]
	v_mfma_f32_16x16x32_bf16 v[30:33], v[170:173], v[202:205], v[30:33]
	v_mfma_f32_16x16x32_bf16 v[26:29], v[178:181], v[202:205], v[26:29]
	v_mfma_f32_16x16x32_bf16 v[22:25], v[170:173], v[210:213], v[22:25]
	v_mfma_f32_16x16x32_bf16 v[18:21], v[178:181], v[210:213], v[18:21]
	v_mfma_f32_16x16x32_bf16 v[14:17], v[170:173], v[218:221], v[14:17]
	v_mfma_f32_16x16x32_bf16 v[10:13], v[178:181], v[218:221], v[10:13]
	v_mfma_f32_16x16x32_bf16 v[6:9], v[170:173], v[226:229], v[6:9]
	v_mfma_f32_16x16x32_bf16 v[2:5], v[178:181], v[226:229], v[2:5]
	s_setprio 0
	s_setprio 1
	v_mfma_f32_16x16x32_bf16 v[94:97], v[182:185], v[198:201], v[94:97]
	v_mfma_f32_16x16x32_bf16 v[90:93], v[190:193], v[198:201], v[90:93]
	v_mfma_f32_16x16x32_bf16 v[86:89], v[182:185], v[206:209], v[86:89]
	v_mfma_f32_16x16x32_bf16 v[82:85], v[190:193], v[206:209], v[82:85]
	v_mfma_f32_16x16x32_bf16 v[78:81], v[182:185], v[214:217], v[78:81]
	v_mfma_f32_16x16x32_bf16 v[74:77], v[190:193], v[214:217], v[74:77]
	v_mfma_f32_16x16x32_bf16 v[62:65], v[182:185], v[222:225], v[62:65]
	v_mfma_f32_16x16x32_bf16 v[58:61], v[190:193], v[222:225], v[58:61]
	v_mfma_f32_16x16x32_bf16 v[94:97], v[186:189], v[202:205], v[94:97]
	v_mfma_f32_16x16x32_bf16 v[90:93], v[194:197], v[202:205], v[90:93]
	v_mfma_f32_16x16x32_bf16 v[86:89], v[186:189], v[210:213], v[86:89]
	v_mfma_f32_16x16x32_bf16 v[82:85], v[194:197], v[210:213], v[82:85]
	v_mfma_f32_16x16x32_bf16 v[78:81], v[186:189], v[218:221], v[78:81]
	v_mfma_f32_16x16x32_bf16 v[74:77], v[194:197], v[218:221], v[74:77]
	v_mfma_f32_16x16x32_bf16 v[62:65], v[186:189], v[226:229], v[62:65]
	v_mfma_f32_16x16x32_bf16 v[58:61], v[194:197], v[226:229], v[58:61]
	s_setprio 0
	s_barrier
	v_lshl_add_u64 v[234:235], s[56:57], 0, v[130:131]
	s_mov_b32 m0, s58
	s_nop 0
	global_load_lds_dwordx4 v[234:235], off
	s_mov_b32 m0, s33
	s_nop 0
	global_load_lds_dwordx4 v[236:237], off
	s_add_i32 s84, 0, 0x18000
	v_add_u32_e32 v138, s84, v160
	s_add_i32 s85, 0, 0x1c000
	ds_read_b128 v[156:159], v138
	ds_read_b128 v[170:173], v138 offset:1024
	ds_read_b128 v[174:177], v138 offset:2048
	ds_read_b128 v[178:181], v138 offset:3072
	v_add_u32_e32 v138, s85, v160
	ds_read_b128 v[182:185], v138
	ds_read_b128 v[186:189], v138 offset:1024
	ds_read_b128 v[190:193], v138 offset:2048
	ds_read_b128 v[194:197], v138 offset:3072
	s_add_u32 s56, s56, 0x80000
	s_addc_u32 s57, s57, 0
	s_mov_b32 m0, s59
	v_lshl_add_u64 v[238:239], s[56:57], 0, v[130:131]
	ds_read_b128 v[198:201], v167 offset:32768
	ds_read_b128 v[202:205], v167 offset:33792
	ds_read_b128 v[206:209], v167 offset:34816
	ds_read_b128 v[210:213], v167 offset:35840
	ds_read_b128 v[214:217], v167 offset:36864
	ds_read_b128 v[218:221], v167 offset:37888
	ds_read_b128 v[222:225], v167 offset:38912
	ds_read_b128 v[226:229], v167 offset:39936
	global_load_lds_dwordx4 v[238:239], off
	v_lshl_add_u64 v[238:239], s[56:57], 0, v[134:135]
	s_mov_b32 m0, s61
	s_nop 0
	global_load_lds_dwordx4 v[238:239], off
	s_waitcnt vmcnt(8)
	s_waitcnt lgkmcnt(0)
	s_barrier
	s_setprio 1
	s_waitcnt lgkmcnt(0)
	v_mfma_f32_16x16x32_bf16 v[70:73], v[156:159], v[198:201], v[70:73]
	v_mfma_f32_16x16x32_bf16 v[66:69], v[174:177], v[198:201], v[66:69]
	v_mfma_f32_16x16x32_bf16 v[54:57], v[156:159], v[206:209], v[54:57]
	v_mfma_f32_16x16x32_bf16 v[50:53], v[174:177], v[206:209], v[50:53]
	v_mfma_f32_16x16x32_bf16 v[46:49], v[156:159], v[214:217], v[46:49]
	v_mfma_f32_16x16x32_bf16 v[42:45], v[174:177], v[214:217], v[42:45]
	v_mfma_f32_16x16x32_bf16 v[38:41], v[156:159], v[222:225], v[38:41]
	v_mfma_f32_16x16x32_bf16 v[34:37], v[174:177], v[222:225], v[34:37]
	v_mfma_f32_16x16x32_bf16 v[70:73], v[170:173], v[202:205], v[70:73]
	v_mfma_f32_16x16x32_bf16 v[66:69], v[178:181], v[202:205], v[66:69]
	v_mfma_f32_16x16x32_bf16 v[54:57], v[170:173], v[210:213], v[54:57]
	v_mfma_f32_16x16x32_bf16 v[50:53], v[178:181], v[210:213], v[50:53]
	v_mfma_f32_16x16x32_bf16 v[46:49], v[170:173], v[218:221], v[46:49]
	v_mfma_f32_16x16x32_bf16 v[42:45], v[178:181], v[218:221], v[42:45]
	v_mfma_f32_16x16x32_bf16 v[38:41], v[170:173], v[226:229], v[38:41]
	v_mfma_f32_16x16x32_bf16 v[34:37], v[178:181], v[226:229], v[34:37]
	s_setprio 0
	s_setprio 1
	v_mfma_f32_16x16x32_bf16 v[126:129], v[182:185], v[198:201], v[126:129]
	v_mfma_f32_16x16x32_bf16 v[122:125], v[190:193], v[198:201], v[122:125]
	v_mfma_f32_16x16x32_bf16 v[118:121], v[182:185], v[206:209], v[118:121]
	v_mfma_f32_16x16x32_bf16 v[114:117], v[190:193], v[206:209], v[114:117]
	v_mfma_f32_16x16x32_bf16 v[110:113], v[182:185], v[214:217], v[110:113]
	v_mfma_f32_16x16x32_bf16 v[106:109], v[190:193], v[214:217], v[106:109]
	v_mfma_f32_16x16x32_bf16 v[102:105], v[182:185], v[222:225], v[102:105]
	v_mfma_f32_16x16x32_bf16 v[98:101], v[190:193], v[222:225], v[98:101]
	v_mfma_f32_16x16x32_bf16 v[126:129], v[186:189], v[202:205], v[126:129]
	v_mfma_f32_16x16x32_bf16 v[122:125], v[194:197], v[202:205], v[122:125]
	v_mfma_f32_16x16x32_bf16 v[118:121], v[186:189], v[210:213], v[118:121]
	v_mfma_f32_16x16x32_bf16 v[114:117], v[194:197], v[210:213], v[114:117]
	v_mfma_f32_16x16x32_bf16 v[110:113], v[186:189], v[218:221], v[110:113]
	v_mfma_f32_16x16x32_bf16 v[106:109], v[194:197], v[218:221], v[106:109]
	v_mfma_f32_16x16x32_bf16 v[102:105], v[186:189], v[226:229], v[102:105]
	v_mfma_f32_16x16x32_bf16 v[98:101], v[194:197], v[226:229], v[98:101]
	s_setprio 0
	s_barrier
	s_add_i32 s56, s84, s5
	v_lshl_add_u64 v[230:231], v[230:231], 0, s[36:37]
	s_mov_b32 m0, s56
	ds_read_b128 v[198:201], v167 offset:49152
	ds_read_b128 v[202:205], v167 offset:50176
	ds_read_b128 v[206:209], v167 offset:51200
	ds_read_b128 v[210:213], v167 offset:52224
	ds_read_b128 v[214:217], v167 offset:53248
	ds_read_b128 v[218:221], v167 offset:54272
	ds_read_b128 v[222:225], v167 offset:55296
	ds_read_b128 v[226:229], v167 offset:56320
	global_load_lds_dwordx4 v[230:231], off
	s_add_i32 m0, s56, 0x2000
	s_add_u32 s54, s54, 0x80080
	v_lshl_add_u64 v[230:231], v[232:233], 0, s[36:37]
	s_addc_u32 s55, s55, 0
	s_add_i32 s56, s85, s5
	global_load_lds_dwordx4 v[230:231], off
	v_lshl_add_u64 v[230:231], s[54:55], 0, v[132:133]
	s_mov_b32 m0, s56
	s_nop 0
	global_load_lds_dwordx4 v[230:231], off
	v_lshl_add_u64 v[230:231], s[54:55], 0, v[136:137]
	s_add_i32 m0, s56, 0x2000
	s_nop 0
	global_load_lds_dwordx4 v[230:231], off
	v_lshl_add_u64 v[240:241], v[234:235], 0, s[36:37]
	v_lshl_add_u64 v[242:243], v[236:237], 0, s[36:37]
	s_waitcnt vmcnt(6)
	s_waitcnt lgkmcnt(0)
	s_barrier
	s_setprio 1
	s_waitcnt lgkmcnt(0)
	v_mfma_f32_16x16x32_bf16 v[30:33], v[156:159], v[198:201], v[30:33]
	v_mfma_f32_16x16x32_bf16 v[26:29], v[174:177], v[198:201], v[26:29]
	v_mfma_f32_16x16x32_bf16 v[22:25], v[156:159], v[206:209], v[22:25]
	v_mfma_f32_16x16x32_bf16 v[18:21], v[174:177], v[206:209], v[18:21]
	v_mfma_f32_16x16x32_bf16 v[14:17], v[156:159], v[214:217], v[14:17]
	v_mfma_f32_16x16x32_bf16 v[10:13], v[174:177], v[214:217], v[10:13]
	v_mfma_f32_16x16x32_bf16 v[6:9], v[156:159], v[222:225], v[6:9]
	v_mfma_f32_16x16x32_bf16 v[2:5], v[174:177], v[222:225], v[2:5]
	v_mfma_f32_16x16x32_bf16 v[30:33], v[170:173], v[202:205], v[30:33]
	v_mfma_f32_16x16x32_bf16 v[26:29], v[178:181], v[202:205], v[26:29]
	v_mfma_f32_16x16x32_bf16 v[22:25], v[170:173], v[210:213], v[22:25]
	v_mfma_f32_16x16x32_bf16 v[18:21], v[178:181], v[210:213], v[18:21]
	v_mfma_f32_16x16x32_bf16 v[14:17], v[170:173], v[218:221], v[14:17]
	v_mfma_f32_16x16x32_bf16 v[10:13], v[178:181], v[218:221], v[10:13]
	v_mfma_f32_16x16x32_bf16 v[6:9], v[170:173], v[226:229], v[6:9]
	v_mfma_f32_16x16x32_bf16 v[2:5], v[178:181], v[226:229], v[2:5]
	s_setprio 0
	s_setprio 1
	v_mfma_f32_16x16x32_bf16 v[94:97], v[182:185], v[198:201], v[94:97]
	v_mfma_f32_16x16x32_bf16 v[90:93], v[190:193], v[198:201], v[90:93]
	v_mfma_f32_16x16x32_bf16 v[86:89], v[182:185], v[206:209], v[86:89]
	v_mfma_f32_16x16x32_bf16 v[82:85], v[190:193], v[206:209], v[82:85]
	v_mfma_f32_16x16x32_bf16 v[78:81], v[182:185], v[214:217], v[78:81]
	v_mfma_f32_16x16x32_bf16 v[74:77], v[190:193], v[214:217], v[74:77]
	v_mfma_f32_16x16x32_bf16 v[62:65], v[182:185], v[222:225], v[62:65]
	v_mfma_f32_16x16x32_bf16 v[58:61], v[190:193], v[222:225], v[58:61]
	v_mfma_f32_16x16x32_bf16 v[94:97], v[186:189], v[202:205], v[94:97]
	v_mfma_f32_16x16x32_bf16 v[90:93], v[194:197], v[202:205], v[90:93]
	v_mfma_f32_16x16x32_bf16 v[86:89], v[186:189], v[210:213], v[86:89]
	v_mfma_f32_16x16x32_bf16 v[82:85], v[194:197], v[210:213], v[82:85]
	v_mfma_f32_16x16x32_bf16 v[78:81], v[186:189], v[218:221], v[78:81]
	v_mfma_f32_16x16x32_bf16 v[74:77], v[194:197], v[218:221], v[74:77]
	v_mfma_f32_16x16x32_bf16 v[62:65], v[186:189], v[226:229], v[62:65]
	v_mfma_f32_16x16x32_bf16 v[58:61], v[194:197], v[226:229], v[58:61]
	s_setprio 0
	s_barrier
	s_mov_b32 s99, 1
	s_add_i32 s83, s83, 2
	s_add_u32 s52, s52, 0x100
	s_addc_u32 s53, s53, 0
	s_add_u32 s81, s81, 0x100
	s_addc_u32 s82, s82, 0
	s_cmp_gt_u32 s83, 29
	s_cbranch_scc0 .LBB0_189
	s_and_b64 vcc, exec, s[38:39]
	s_cbranch_vccz .LBB0_192
	s_barrier

.LBB0_318:
	s_mov_b32 s99, 0
	v_readlane_b32 s0, v253, 11
	v_readlane_b32 s1, v253, 12
	s_mov_b32 s3, s1
	s_cmp_lt_i32 s0, 6
	s_cselect_b64 s[0:1], -1, 0
	s_cmp_gt_i32 s3, 5
	s_cselect_b64 s[4:5], -1, 0
	s_and_b64 s[0:1], s[0:1], s[4:5]
	s_andn2_b64 vcc, exec, s[0:1]
	s_cbranch_vccnz .LBB0_407
	v_readlane_b32 s0, v253, 0
	v_readlane_b32 s1, v253, 1
	s_load_dwordx2 s[10:11], s[0:1], 0x70
	s_load_dwordx2 s[16:17], s[0:1], 0x80
	s_load_dwordx2 s[18:19], s[0:1], 0xa0
	s_load_dwordx2 s[20:21], s[0:1], 0xc0
	s_load_dwordx4 s[12:15], s[0:1], 0xb0
	s_load_dwordx2 s[22:23], s[0:1], 0xd0
	s_ashr_i32 s0, s60, 31
	v_mov_b32_e32 v11, v0
	s_cmpk_lt_i32 s2, 0x30c
	s_nop 0
	v_readfirstlane_b32 s7, v11
	s_cbranch_scc0 .LBB0_341
	v_lshlrev_b32_e32 v1, 4, v11
	v_add_u32_e32 v2, 0x2000, v1
	v_ashrrev_i32_e32 v3, 31, v2
	v_lshrrev_b32_e32 v3, 22, v3
	v_add_u32_e32 v3, v2, v3
	v_ashrrev_i32_e32 v10, 10, v3
	v_mul_i32_i24_e32 v3, 0x400, v10
	v_sub_u32_e32 v2, v2, v3
	v_lshrrev_b32_e32 v3, 4, v2
	v_bitop3_b32 v2, v3, v2, 32 bitop3:0x6c
	v_ashrrev_i32_e32 v3, 31, v2
	v_lshrrev_b32_e32 v3, 26, v3
	v_add_u32_e32 v3, v2, v3
	v_lshlrev_b32_e32 v4, 3, v10
	v_ashrrev_i32_e32 v12, 6, v3
	v_and_b32_e32 v4, -16, v4
	v_add_u32_e32 v4, v12, v4
	v_and_b32_e32 v5, 3, v12
	s_mov_b32 s6, 0x3fffe0
	v_lshrrev_b32_e32 v6, 2, v4
	v_lshlrev_b32_e32 v7, 1, v4
	v_and_b32_e32 v3, 0xc0, v3
	v_and_or_b32 v5, v4, s6, v5
	v_and_b32_e32 v6, 4, v6
	v_and_b32_e32 v7, 24, v7
	v_sub_u32_e32 v2, v2, v3
	v_mov_b32_e32 v3, 1
	v_or3_b32 v5, v5, v6, v7
	v_lshlrev_b32_e32 v6, 5, v10
	v_ashrrev_i16_sdwa v2, v3, sext(v2) dst_sel:DWORD dst_unused:UNUSED_PAD src0_sel:DWORD src1_sel:BYTE_0
	v_and_b32_e32 v13, 32, v6
	v_bfe_i32 v14, v2, 0, 16
	s_movk_i32 s9, 0x500
	v_add_u32_e32 v2, v13, v14
	v_mul_lo_u32 v4, v4, s9
	v_lshlrev_b32_e32 v6, 1, v2
	v_add_lshl_u32 v132, v2, v4, 1
	v_bfe_i32 v2, v11, 27, 1
	v_lshrrev_b32_e32 v2, 22, v2
	v_add_u32_e32 v2, v1, v2
	v_and_b32_e32 v2, 0xfffffc00, v2
	v_sub_u32_e32 v1, v1, v2
	v_lshrrev_b32_e32 v2, 4, v1
	v_bitop3_b32 v2, v2, v1, 32 bitop3:0x6c
	v_ashrrev_i32_e32 v1, 31, v1
	v_lshrrev_b32_e32 v1, 26, v1
	v_add_u32_e32 v1, v2, v1
	v_ashrrev_i32_e32 v15, 6, v1
	v_ashrrev_i32_e32 v1, 31, v11
	v_lshrrev_b32_e32 v1, 26, v1
	v_add_u32_e32 v1, v11, v1
	s_waitcnt lgkmcnt(0)
	s_add_u32 s1, s22, 0x31300000
	v_ashrrev_i32_e32 v16, 6, v1
	s_addc_u32 s3, s23, 0
	v_lshlrev_b32_e32 v1, 3, v16
	s_add_u32 s4, s22, 0x1100000
	v_and_b32_e32 v1, -16, v1
	s_addc_u32 s5, s23, 0
	v_add_u32_e32 v1, v15, v1
	v_and_b32_e32 v4, 3, v15
	s_ashr_i32 s46, s2, 31
	v_and_or_b32 v4, v1, s6, v4
	s_lshr_b32 s6, s46, 29
	s_add_i32 s6, s2, s6
	s_and_b32 s24, s6, -8
	s_sub_i32 s24, s2, s24
	s_ashr_i32 s28, s7, 6
	s_mul_i32 s26, s24, 0x61
	s_ashr_i32 s8, s7, 8
	s_lshl_b32 s33, s28, 10
	s_add_i32 s26, s26, 4
	s_ashr_i32 s6, s6, 3
	v_lshl_add_u32 v130, v5, 10, v6
	v_lshrrev_b32_e32 v5, 2, v1
	v_lshlrev_b32_e32 v6, 1, v1
	s_mul_i32 s25, s24, 0x62
	s_cmp_lt_i32 s24, 4
	v_and_b32_e32 v5, 4, v5
	v_and_b32_e32 v6, 24, v6
	s_cselect_b32 s24, s25, s26
	v_or3_b32 v4, v4, v5, v6
	v_lshlrev_b32_e32 v5, 5, v16
	s_add_i32 s24, s24, s6
	v_and_b32_e32 v17, 32, v5
	v_mul_i32_i24_e32 v5, 64, v15
	s_mul_hi_i32 s6, s24, 0x2aaaaaab
	v_sub_u32_e32 v2, v2, v5
	s_lshr_b32 s25, s6, 31
	s_ashr_i32 s6, s6, 4
	v_ashrrev_i16_sdwa v2, v3, sext(v2) dst_sel:DWORD dst_unused:UNUSED_PAD src0_sel:DWORD src1_sel:BYTE_0
	s_add_i32 s6, s6, s25
	v_bfe_i32 v18, v2, 0, 16
	s_lshl_b32 s26, s6, 3
	v_add_u32_e32 v2, v17, v18
	s_sub_i32 s25, 0x41, s26
	s_mulk_i32 s6, 0x60
	v_lshlrev_b32_e32 v3, 1, v2
	s_min_u32 s27, s25, 8
	s_sub_i32 s29, s24, s6
	v_lshl_add_u32 v134, v4, 10, v3
	s_sext_i32_i8 s6, s29
	v_cvt_f32_ubyte0_e32 v4, s27
	v_cvt_f32_i32_e32 v3, s6
	v_rcp_iflag_f32_e32 v5, v4
	v_mul_lo_u32 v1, v1, s9
	v_add_lshl_u32 v136, v2, v1, 1
	s_ashr_i32 s6, s6, 30
	v_mul_f32_e32 v1, v3, v5
	v_trunc_f32_e32 v1, v1
	v_fma_f32 v2, -v1, v4, v3
	v_cvt_i32_f32_e32 v1, v1
	s_or_b32 s6, s6, 1
	v_cmp_ge_f32_e64 s[24:25], |v2|, v4
	s_and_b64 s[24:25], s[24:25], exec
	s_cselect_b32 s6, s6, 0
	v_readfirstlane_b32 s24, v1
	s_add_i32 s6, s24, s6
	s_mul_i32 s24, s6, s27
	s_sub_i32 s24, s29, s24
	s_sext_i32_i8 s24, s24
	s_add_i32 s58, s26, s24
	s_bfe_i64 s[24:25], s[6:7], 0x80000
	s_lshl_b64 s[24:25], s[24:25], 18
	s_add_u32 s42, s4, s24
	s_addc_u32 s43, s5, s25
	s_add_i32 s47, s33, 0
	s_add_i32 m0, s47, 0x10000
	s_mul_i32 s27, s58, 0xa0000
	global_load_lds_dwordx4 v134, s[42:43]
	s_add_i32 m0, s47, 0x12000
	s_add_u32 s24, s42, 0x20000
	global_load_lds_dwordx4 v130, s[42:43]
	s_addc_u32 s25, s43, 0
	s_add_i32 m0, s47, 0x14000
	s_mul_hi_i32 s26, s58, 0xa0000
	global_load_lds_dwordx4 v134, s[24:25]
	s_add_i32 m0, s47, 0x16000
	s_add_u32 s40, s1, s27
	s_addc_u32 s41, s3, s26
	s_add_i32 s48, s47, 0x2000
	global_load_lds_dwordx4 v130, s[24:25]
	s_mov_b32 m0, s47
	s_add_u32 s24, s40, 0x50000
	global_load_lds_dwordx4 v136, s[40:41]
	s_mov_b32 m0, s48
	s_addc_u32 s25, s41, 0
	s_add_i32 s49, s47, 0x4000
	global_load_lds_dwordx4 v132, s[40:41]
	s_mov_b32 m0, s49
	s_add_i32 s50, s47, 0x6000
	global_load_lds_dwordx4 v136, s[24:25]
	s_mov_b32 m0, s50
	v_mov_b32_e32 v135, 0
	global_load_lds_dwordx4 v132, s[24:25]
	v_mov_b32_e32 v131, v135
	v_mov_b32_e32 v137, v135
	v_mov_b32_e32 v133, v135
	s_cmp_eq_u32 s8, 1
	s_mov_b32 s51, 0
	v_lshl_add_u64 v[8:9], s[42:43], 0, v[134:135]
	v_lshl_add_u64 v[6:7], s[42:43], 0, v[130:131]
	v_lshl_add_u64 v[2:3], s[40:41], 0, v[136:137]
	s_cselect_b64 s[24:25], -1, 0
	s_cmp_lg_u32 s8, 1
	v_lshl_add_u64 v[4:5], s[40:41], 0, v[132:133]
	s_cbranch_scc1 .LBB0_322
	s_barrier

.LBB0_334:
	s_cmp_eq_u32 s99, 0
	s_cbranch_scc1 .Lbal_skip_334
	s_mov_b32 m0, s52
	s_nop 0
	global_load_lds_dwordx4 v[240:241], off
	s_mov_b32 m0, s53
	s_nop 0
	global_load_lds_dwordx4 v[242:243], off
.Lbal_skip_334:
	ds_read_b128 v[146:149], v152
	ds_read_b128 v[156:159], v152 offset:1024
	ds_read_b128 v[160:163], v152 offset:2048
	ds_read_b128 v[164:167], v152 offset:3072
	ds_read_b128 v[168:171], v153
	ds_read_b128 v[172:175], v153 offset:1024
	ds_read_b128 v[176:179], v153 offset:2048
	ds_read_b128 v[180:183], v153 offset:3072
	s_add_u32 s8, s40, 0x100
	s_addc_u32 s9, s41, 0
	s_cmp_eq_u32 s66, 4
	s_cselect_b32 s45, s37, s9
	s_cselect_b32 s44, s36, s8
	s_cselect_b32 s43, s35, s65
	s_cselect_b32 s42, s61, s64
	v_lshl_add_u64 v[216:217], s[40:41], 0, v[138:139]
	s_add_i32 m0, s47, 0xc000
	ds_read_b128 v[184:187], v154
	ds_read_b128 v[188:191], v154 offset:1024
	ds_read_b128 v[192:195], v154 offset:2048
	ds_read_b128 v[196:199], v154 offset:3072
	ds_read_b128 v[200:203], v154 offset:4096
	ds_read_b128 v[204:207], v154 offset:5120
	ds_read_b128 v[208:211], v154 offset:6144
	ds_read_b128 v[212:215], v154 offset:7168
	global_load_lds_dwordx4 v[216:217], off
	v_lshl_add_u64 v[216:217], s[40:41], 0, v[140:141]
	s_add_i32 m0, s47, 0xe000
	s_nop 0
	global_load_lds_dwordx4 v[216:217], off
	s_waitcnt vmcnt(8)
	s_waitcnt lgkmcnt(0)
	s_barrier
	s_setprio 1
	s_waitcnt lgkmcnt(0)
	v_mfma_f32_16x16x32_bf16 v[126:129], v[146:149], v[184:187], v[126:129]
	v_mfma_f32_16x16x32_bf16 v[122:125], v[160:163], v[184:187], v[122:125]
	v_mfma_f32_16x16x32_bf16 v[118:121], v[146:149], v[192:195], v[118:121]
	v_mfma_f32_16x16x32_bf16 v[110:113], v[160:163], v[192:195], v[110:113]
	v_mfma_f32_16x16x32_bf16 v[102:105], v[146:149], v[200:203], v[102:105]
	v_mfma_f32_16x16x32_bf16 v[94:97], v[160:163], v[200:203], v[94:97]
	v_mfma_f32_16x16x32_bf16 v[86:89], v[146:149], v[208:211], v[86:89]
	v_mfma_f32_16x16x32_bf16 v[78:81], v[160:163], v[208:211], v[78:81]
	v_mfma_f32_16x16x32_bf16 v[126:129], v[156:159], v[188:191], v[126:129]
	v_mfma_f32_16x16x32_bf16 v[122:125], v[164:167], v[188:191], v[122:125]
	v_mfma_f32_16x16x32_bf16 v[118:121], v[156:159], v[196:199], v[118:121]
	v_mfma_f32_16x16x32_bf16 v[110:113], v[164:167], v[196:199], v[110:113]
	v_mfma_f32_16x16x32_bf16 v[102:105], v[156:159], v[204:207], v[102:105]
	v_mfma_f32_16x16x32_bf16 v[94:97], v[164:167], v[204:207], v[94:97]
	v_mfma_f32_16x16x32_bf16 v[86:89], v[156:159], v[212:215], v[86:89]
	v_mfma_f32_16x16x32_bf16 v[78:81], v[164:167], v[212:215], v[78:81]
	s_setprio 0
	s_setprio 1
	v_mfma_f32_16x16x32_bf16 v[114:117], v[168:171], v[184:187], v[114:117]
	v_mfma_f32_16x16x32_bf16 v[106:109], v[176:179], v[184:187], v[106:109]
	v_mfma_f32_16x16x32_bf16 v[98:101], v[168:171], v[192:195], v[98:101]
	v_mfma_f32_16x16x32_bf16 v[90:93], v[176:179], v[192:195], v[90:93]
	v_mfma_f32_16x16x32_bf16 v[82:85], v[168:171], v[200:203], v[82:85]
	v_mfma_f32_16x16x32_bf16 v[74:77], v[176:179], v[200:203], v[74:77]
	v_mfma_f32_16x16x32_bf16 v[70:73], v[168:171], v[208:211], v[70:73]
	v_mfma_f32_16x16x32_bf16 v[66:69], v[176:179], v[208:211], v[66:69]
	v_mfma_f32_16x16x32_bf16 v[114:117], v[172:175], v[188:191], v[114:117]
	v_mfma_f32_16x16x32_bf16 v[106:109], v[180:183], v[188:191], v[106:109]
	v_mfma_f32_16x16x32_bf16 v[98:101], v[172:175], v[196:199], v[98:101]
	v_mfma_f32_16x16x32_bf16 v[90:93], v[180:183], v[196:199], v[90:93]
	v_mfma_f32_16x16x32_bf16 v[82:85], v[172:175], v[204:207], v[82:85]
	v_mfma_f32_16x16x32_bf16 v[74:77], v[180:183], v[204:207], v[74:77]
	v_mfma_f32_16x16x32_bf16 v[70:73], v[172:175], v[212:215], v[70:73]
	v_mfma_f32_16x16x32_bf16 v[66:69], v[180:183], v[212:215], v[66:69]
	s_setprio 0
	s_barrier
	s_add_i32 s40, s54, s33
	v_lshl_add_u64 v[216:217], s[42:43], 0, v[134:135]
	s_mov_b32 m0, s40
	ds_read_b128 v[184:187], v154 offset:16384
	ds_read_b128 v[188:191], v154 offset:17408
	ds_read_b128 v[192:195], v154 offset:18432
	ds_read_b128 v[196:199], v154 offset:19456
	ds_read_b128 v[200:203], v154 offset:20480
	ds_read_b128 v[204:207], v154 offset:21504
	ds_read_b128 v[208:211], v154 offset:22528
	ds_read_b128 v[212:215], v154 offset:23552
	global_load_lds_dwordx4 v[216:217], off
	s_add_i32 m0, s40, 0x2000
	s_add_u32 s40, s42, 0x20000
	v_lshl_add_u64 v[218:219], s[42:43], 0, v[130:131]
	s_addc_u32 s41, s43, 0
	s_add_i32 s67, s55, s33
	global_load_lds_dwordx4 v[218:219], off
	v_lshl_add_u64 v[220:221], s[40:41], 0, v[134:135]
	s_mov_b32 m0, s67
	v_lshl_add_u64 v[222:223], s[44:45], 0, v[132:133]
	global_load_lds_dwordx4 v[220:221], off
	v_lshl_add_u64 v[220:221], s[40:41], 0, v[130:131]
	s_add_i32 m0, s67, 0x2000
	s_nop 0
	global_load_lds_dwordx4 v[220:221], off
	s_waitcnt vmcnt(6)
	s_waitcnt lgkmcnt(0)
	s_barrier
	s_setprio 1
	s_waitcnt lgkmcnt(0)
	v_mfma_f32_16x16x32_bf16 v[62:65], v[146:149], v[184:187], v[62:65]
	v_mfma_f32_16x16x32_bf16 v[58:61], v[160:163], v[184:187], v[58:61]
	v_mfma_f32_16x16x32_bf16 v[54:57], v[146:149], v[192:195], v[54:57]
	v_mfma_f32_16x16x32_bf16 v[46:49], v[160:163], v[192:195], v[46:49]
	v_mfma_f32_16x16x32_bf16 v[38:41], v[146:149], v[200:203], v[38:41]
	v_mfma_f32_16x16x32_bf16 v[30:33], v[160:163], v[200:203], v[30:33]
	v_mfma_f32_16x16x32_bf16 v[22:25], v[146:149], v[208:211], v[22:25]
	v_mfma_f32_16x16x32_bf16 v[14:17], v[160:163], v[208:211], v[14:17]
	v_mfma_f32_16x16x32_bf16 v[62:65], v[156:159], v[188:191], v[62:65]
	v_mfma_f32_16x16x32_bf16 v[58:61], v[164:167], v[188:191], v[58:61]
	v_mfma_f32_16x16x32_bf16 v[54:57], v[156:159], v[196:199], v[54:57]
	v_mfma_f32_16x16x32_bf16 v[46:49], v[164:167], v[196:199], v[46:49]
	v_mfma_f32_16x16x32_bf16 v[38:41], v[156:159], v[204:207], v[38:41]
	v_mfma_f32_16x16x32_bf16 v[30:33], v[164:167], v[204:207], v[30:33]
	v_mfma_f32_16x16x32_bf16 v[22:25], v[156:159], v[212:215], v[22:25]
	v_mfma_f32_16x16x32_bf16 v[14:17], v[164:167], v[212:215], v[14:17]
	s_setprio 0
	s_setprio 1
	v_mfma_f32_16x16x32_bf16 v[50:53], v[168:171], v[184:187], v[50:53]
	v_mfma_f32_16x16x32_bf16 v[42:45], v[176:179], v[184:187], v[42:45]
	v_mfma_f32_16x16x32_bf16 v[34:37], v[168:171], v[192:195], v[34:37]
	v_mfma_f32_16x16x32_bf16 v[26:29], v[176:179], v[192:195], v[26:29]
	v_mfma_f32_16x16x32_bf16 v[18:21], v[168:171], v[200:203], v[18:21]
	v_mfma_f32_16x16x32_bf16 v[10:13], v[176:179], v[200:203], v[10:13]
	v_mfma_f32_16x16x32_bf16 v[6:9], v[168:171], v[208:211], v[6:9]
	v_mfma_f32_16x16x32_bf16 v[2:5], v[176:179], v[208:211], v[2:5]
	v_mfma_f32_16x16x32_bf16 v[50:53], v[172:175], v[188:191], v[50:53]
	v_mfma_f32_16x16x32_bf16 v[42:45], v[180:183], v[188:191], v[42:45]
	v_mfma_f32_16x16x32_bf16 v[34:37], v[172:175], v[196:199], v[34:37]
	v_mfma_f32_16x16x32_bf16 v[26:29], v[180:183], v[196:199], v[26:29]
	v_mfma_f32_16x16x32_bf16 v[18:21], v[172:175], v[204:207], v[18:21]
	v_mfma_f32_16x16x32_bf16 v[10:13], v[180:183], v[204:207], v[10:13]
	v_mfma_f32_16x16x32_bf16 v[6:9], v[172:175], v[212:215], v[6:9]
	v_mfma_f32_16x16x32_bf16 v[2:5], v[180:183], v[212:215], v[2:5]
	s_setprio 0
	s_barrier
	v_lshl_add_u64 v[220:221], s[44:45], 0, v[136:137]
	s_mov_b32 m0, s47
	s_nop 0
	global_load_lds_dwordx4 v[220:221], off
	s_mov_b32 m0, s48
	s_nop 0
	global_load_lds_dwordx4 v[222:223], off
	s_add_i32 s67, 0, 0x18000
	v_add_u32_e32 v155, s67, v150
	s_add_i32 s68, 0, 0x1c000
	ds_read_b128 v[146:149], v155
	ds_read_b128 v[156:159], v155 offset:1024
	ds_read_b128 v[160:163], v155 offset:2048
	ds_read_b128 v[164:167], v155 offset:3072
	v_add_u32_e32 v155, s68, v150
	ds_read_b128 v[168:171], v155
	ds_read_b128 v[172:175], v155 offset:1024
	ds_read_b128 v[176:179], v155 offset:2048
	ds_read_b128 v[180:183], v155 offset:3072
	s_add_u32 s40, s44, 0x50000
	s_addc_u32 s41, s45, 0
	s_mov_b32 m0, s49
	v_lshl_add_u64 v[224:225], s[40:41], 0, v[136:137]
	ds_read_b128 v[184:187], v154 offset:32768
	ds_read_b128 v[188:191], v154 offset:33792
	ds_read_b128 v[192:195], v154 offset:34816
	ds_read_b128 v[196:199], v154 offset:35840
	ds_read_b128 v[200:203], v154 offset:36864
	ds_read_b128 v[204:207], v154 offset:37888
	ds_read_b128 v[208:211], v154 offset:38912
	ds_read_b128 v[212:215], v154 offset:39936
	global_load_lds_dwordx4 v[224:225], off
	v_lshl_add_u64 v[224:225], s[40:41], 0, v[132:133]
	s_mov_b32 m0, s50
	s_nop 0
	global_load_lds_dwordx4 v[224:225], off
	s_waitcnt vmcnt(8)
	s_waitcnt lgkmcnt(0)
	s_barrier
	s_setprio 1
	s_waitcnt lgkmcnt(0)
	v_mfma_f32_16x16x32_bf16 v[126:129], v[146:149], v[184:187], v[126:129]
	v_mfma_f32_16x16x32_bf16 v[122:125], v[160:163], v[184:187], v[122:125]
	v_mfma_f32_16x16x32_bf16 v[118:121], v[146:149], v[192:195], v[118:121]
	v_mfma_f32_16x16x32_bf16 v[110:113], v[160:163], v[192:195], v[110:113]
	v_mfma_f32_16x16x32_bf16 v[102:105], v[146:149], v[200:203], v[102:105]
	v_mfma_f32_16x16x32_bf16 v[94:97], v[160:163], v[200:203], v[94:97]
	v_mfma_f32_16x16x32_bf16 v[86:89], v[146:149], v[208:211], v[86:89]
	v_mfma_f32_16x16x32_bf16 v[78:81], v[160:163], v[208:211], v[78:81]
	v_mfma_f32_16x16x32_bf16 v[126:129], v[156:159], v[188:191], v[126:129]
	v_mfma_f32_16x16x32_bf16 v[122:125], v[164:167], v[188:191], v[122:125]
	v_mfma_f32_16x16x32_bf16 v[118:121], v[156:159], v[196:199], v[118:121]
	v_mfma_f32_16x16x32_bf16 v[110:113], v[164:167], v[196:199], v[110:113]
	v_mfma_f32_16x16x32_bf16 v[102:105], v[156:159], v[204:207], v[102:105]
	v_mfma_f32_16x16x32_bf16 v[94:97], v[164:167], v[204:207], v[94:97]
	v_mfma_f32_16x16x32_bf16 v[86:89], v[156:159], v[212:215], v[86:89]
	v_mfma_f32_16x16x32_bf16 v[78:81], v[164:167], v[212:215], v[78:81]
	s_setprio 0
	s_setprio 1
	v_mfma_f32_16x16x32_bf16 v[114:117], v[168:171], v[184:187], v[114:117]
	v_mfma_f32_16x16x32_bf16 v[106:109], v[176:179], v[184:187], v[106:109]
	v_mfma_f32_16x16x32_bf16 v[98:101], v[168:171], v[192:195], v[98:101]
	v_mfma_f32_16x16x32_bf16 v[90:93], v[176:179], v[192:195], v[90:93]
	v_mfma_f32_16x16x32_bf16 v[82:85], v[168:171], v[200:203], v[82:85]
	v_mfma_f32_16x16x32_bf16 v[74:77], v[176:179], v[200:203], v[74:77]
	v_mfma_f32_16x16x32_bf16 v[70:73], v[168:171], v[208:211], v[70:73]
	v_mfma_f32_16x16x32_bf16 v[66:69], v[176:179], v[208:211], v[66:69]
	v_mfma_f32_16x16x32_bf16 v[114:117], v[172:175], v[188:191], v[114:117]
	v_mfma_f32_16x16x32_bf16 v[106:109], v[180:183], v[188:191], v[106:109]
	v_mfma_f32_16x16x32_bf16 v[98:101], v[172:175], v[196:199], v[98:101]
	v_mfma_f32_16x16x32_bf16 v[90:93], v[180:183], v[196:199], v[90:93]
	v_mfma_f32_16x16x32_bf16 v[82:85], v[172:175], v[204:207], v[82:85]
	v_mfma_f32_16x16x32_bf16 v[74:77], v[180:183], v[204:207], v[74:77]
	v_mfma_f32_16x16x32_bf16 v[70:73], v[172:175], v[212:215], v[70:73]
	v_mfma_f32_16x16x32_bf16 v[66:69], v[180:183], v[212:215], v[66:69]
	s_setprio 0
	s_barrier
	s_add_i32 s40, s67, s33
	v_lshl_add_u64 v[216:217], v[216:217], 0, s[28:29]
	s_mov_b32 m0, s40
	ds_read_b128 v[184:187], v154 offset:49152
	ds_read_b128 v[188:191], v154 offset:50176
	ds_read_b128 v[192:195], v154 offset:51200
	ds_read_b128 v[196:199], v154 offset:52224
	ds_read_b128 v[200:203], v154 offset:53248
	ds_read_b128 v[204:207], v154 offset:54272
	ds_read_b128 v[208:211], v154 offset:55296
	ds_read_b128 v[212:215], v154 offset:56320
	global_load_lds_dwordx4 v[216:217], off
	s_add_i32 m0, s40, 0x2000
	s_add_u32 s40, s42, 0x20080
	v_lshl_add_u64 v[216:217], v[218:219], 0, s[28:29]
	s_addc_u32 s41, s43, 0
	s_add_i32 s42, s68, s33
	global_load_lds_dwordx4 v[216:217], off
	v_lshl_add_u64 v[216:217], s[40:41], 0, v[134:135]
	s_mov_b32 m0, s42
	s_nop 0
	global_load_lds_dwordx4 v[216:217], off
	v_lshl_add_u64 v[216:217], s[40:41], 0, v[130:131]
	s_add_i32 m0, s42, 0x2000
	s_nop 0
	global_load_lds_dwordx4 v[216:217], off
	v_lshl_add_u64 v[240:241], v[220:221], 0, s[28:29]
	v_lshl_add_u64 v[242:243], v[222:223], 0, s[28:29]
	s_waitcnt vmcnt(6)
	s_waitcnt lgkmcnt(0)
	s_barrier
	s_setprio 1
	s_waitcnt lgkmcnt(0)
	v_mfma_f32_16x16x32_bf16 v[62:65], v[146:149], v[184:187], v[62:65]
	v_mfma_f32_16x16x32_bf16 v[58:61], v[160:163], v[184:187], v[58:61]
	v_mfma_f32_16x16x32_bf16 v[54:57], v[146:149], v[192:195], v[54:57]
	v_mfma_f32_16x16x32_bf16 v[46:49], v[160:163], v[192:195], v[46:49]
	v_mfma_f32_16x16x32_bf16 v[38:41], v[146:149], v[200:203], v[38:41]
	v_mfma_f32_16x16x32_bf16 v[30:33], v[160:163], v[200:203], v[30:33]
	v_mfma_f32_16x16x32_bf16 v[22:25], v[146:149], v[208:211], v[22:25]
	v_mfma_f32_16x16x32_bf16 v[14:17], v[160:163], v[208:211], v[14:17]
	v_mfma_f32_16x16x32_bf16 v[62:65], v[156:159], v[188:191], v[62:65]
	v_mfma_f32_16x16x32_bf16 v[58:61], v[164:167], v[188:191], v[58:61]
	v_mfma_f32_16x16x32_bf16 v[54:57], v[156:159], v[196:199], v[54:57]
	v_mfma_f32_16x16x32_bf16 v[46:49], v[164:167], v[196:199], v[46:49]
	v_mfma_f32_16x16x32_bf16 v[38:41], v[156:159], v[204:207], v[38:41]
	v_mfma_f32_16x16x32_bf16 v[30:33], v[164:167], v[204:207], v[30:33]
	v_mfma_f32_16x16x32_bf16 v[22:25], v[156:159], v[212:215], v[22:25]
	v_mfma_f32_16x16x32_bf16 v[14:17], v[164:167], v[212:215], v[14:17]
	s_setprio 0
	s_setprio 1
	v_mfma_f32_16x16x32_bf16 v[50:53], v[168:171], v[184:187], v[50:53]
	v_mfma_f32_16x16x32_bf16 v[42:45], v[176:179], v[184:187], v[42:45]
	v_mfma_f32_16x16x32_bf16 v[34:37], v[168:171], v[192:195], v[34:37]
	v_mfma_f32_16x16x32_bf16 v[26:29], v[176:179], v[192:195], v[26:29]
	v_mfma_f32_16x16x32_bf16 v[18:21], v[168:171], v[200:203], v[18:21]
	v_mfma_f32_16x16x32_bf16 v[10:13], v[176:179], v[200:203], v[10:13]
	v_mfma_f32_16x16x32_bf16 v[6:9], v[168:171], v[208:211], v[6:9]
	v_mfma_f32_16x16x32_bf16 v[2:5], v[176:179], v[208:211], v[2:5]
	v_mfma_f32_16x16x32_bf16 v[50:53], v[172:175], v[188:191], v[50:53]
	v_mfma_f32_16x16x32_bf16 v[42:45], v[180:183], v[188:191], v[42:45]
	v_mfma_f32_16x16x32_bf16 v[34:37], v[172:175], v[196:199], v[34:37]
	v_mfma_f32_16x16x32_bf16 v[26:29], v[180:183], v[196:199], v[26:29]
	v_mfma_f32_16x16x32_bf16 v[18:21], v[172:175], v[204:207], v[18:21]
	v_mfma_f32_16x16x32_bf16 v[10:13], v[180:183], v[204:207], v[10:13]
	v_mfma_f32_16x16x32_bf16 v[6:9], v[172:175], v[212:215], v[6:9]
	v_mfma_f32_16x16x32_bf16 v[2:5], v[180:183], v[212:215], v[2:5]
	s_setprio 0
	s_barrier
	s_mov_b32 s99, 1
	s_add_i32 s66, s66, 2
	s_add_u32 s64, s64, 0x100
	s_addc_u32 s65, s65, 0
	s_cmp_gt_u32 s66, 5
	s_mov_b64 s[40:41], s[8:9]
	s_cbranch_scc0 .LBB0_334
	s_and_b64 vcc, exec, s[30:31]
	s_cbranch_vccz .LBB0_337
	s_barrier

.LBB0_341:
	s_mov_b32 s99, 0
	s_abs_i32 s1, s60
	v_cvt_f32_u32_e32 v1, s1
	s_sub_i32 s5, 0, s1
	s_add_i32 s3, s2, 28
	s_ashr_i32 s4, s3, 31
	v_rcp_iflag_f32_e32 v1, v1
	s_abs_i32 s3, s3
	v_mov_b32_e32 v10, v0
	s_waitcnt vmcnt(0) lgkmcnt(0)
	v_mul_f32_e32 v1, 0x4f7ffffe, v1
	v_cvt_u32_f32_e32 v1, v1
	s_barrier
	v_readfirstlane_b32 s6, v1
	s_mul_i32 s5, s5, s6
	s_mul_hi_u32 s5, s6, s5
	s_add_i32 s6, s6, s5
	s_mul_hi_u32 s5, s3, s6
	s_mul_i32 s5, s5, s1
	s_sub_i32 s3, s3, s5
	s_sub_i32 s5, s3, s1
	s_cmp_ge_u32 s3, s1
	s_cselect_b32 s3, s5, s3
	s_sub_i32 s5, s3, s1
	s_cmp_ge_u32 s3, s1
	s_cselect_b32 s1, s5, s3
	s_xor_b32 s1, s1, s4
	s_sub_i32 s1, s1, s4
	s_cmpk_lt_i32 s1, 0x410
	s_cselect_b64 s[6:7], -1, 0
	s_cmpk_gt_i32 s1, 0x40f
	v_readfirstlane_b32 s8, v10
	s_cbranch_scc1 .LBB0_343
	s_ashr_i32 s3, s1, 31
	s_lshr_b32 s3, s3, 29
	s_add_i32 s3, s1, s3
	s_ashr_i32 s4, s3, 3
	s_and_b32 s3, s3, -8
	s_sub_i32 s3, s1, s3
	s_cmp_lt_i32 s3, 0
	s_movk_i32 s5, 0x83
	s_cselect_b32 s5, s5, 0x82
	s_mul_i32 s3, s3, s5
	s_add_i32 s3, s3, s4
	s_ashr_i32 s4, s3, 31
	s_lshr_b32 s4, s4, 25
	s_add_i32 s4, s3, s4
	s_ashr_i32 s5, s4, 7
	s_lshl_b32 s9, s5, 3
	s_sub_i32 s5, 0x41, s9
	s_min_u32 s24, s5, 8
	s_and_b32 s4, s4, 0xffffff80
	s_sub_i32 s3, s3, s4
	v_cvt_f32_ubyte0_e32 v2, s24
	v_cvt_f32_i32_e32 v1, s3
	v_rcp_iflag_f32_e32 v3, v2
	s_ashr_i32 s4, s3, 30
	s_or_b32 s25, s4, 1
	v_mul_f32_e32 v3, v1, v3
	v_trunc_f32_e32 v3, v3
	v_fma_f32 v1, -v3, v2, v1
	v_cvt_i32_f32_e32 v3, v3
	v_cmp_ge_f32_e64 s[4:5], |v1|, v2
	s_and_b64 s[4:5], s[4:5], exec
	s_cselect_b32 s4, s25, 0
	v_readfirstlane_b32 s5, v3
	s_add_i32 s4, s5, s4
	s_sext_i32_i8 s46, s4
	s_mul_i32 s4, s4, s24
	s_sub_i32 s3, s3, s4
	s_sext_i32_i8 s3, s3
	s_add_i32 s73, s9, s3

.LBB0_354:
	s_cmp_eq_u32 s99, 0
	s_cbranch_scc1 .Lbal_skip_354
	s_mov_b32 m0, s59
	s_nop 0
	global_load_lds_dwordx4 v[240:241], off
	s_mov_b32 m0, s61
	s_nop 0
	global_load_lds_dwordx4 v[242:243], off
.Lbal_skip_354:
	ds_read_b128 v[90:93], v171
	ds_read_b128 v[94:97], v171 offset:1024
	ds_read_b128 v[164:167], v171 offset:2048
	ds_read_b128 v[176:179], v171 offset:3072
	ds_read_b128 v[180:183], v172
	ds_read_b128 v[184:187], v172 offset:1024
	ds_read_b128 v[188:191], v172 offset:2048
	ds_read_b128 v[192:195], v172 offset:3072
	s_add_u32 s10, s48, 0x100
	s_addc_u32 s11, s49, 0
	s_cmp_eq_u32 s77, 4
	s_cselect_b32 s53, s43, s11
	s_cselect_b32 s52, s42, s10
	s_cselect_b32 s51, s41, s76
	s_cselect_b32 s50, s74, s75
	v_lshl_add_u64 v[228:229], s[48:49], 0, v[156:157]
	s_add_i32 m0, s47, 0xc000
	ds_read_b128 v[196:199], v173
	ds_read_b128 v[200:203], v173 offset:1024
	ds_read_b128 v[204:207], v173 offset:2048
	ds_read_b128 v[208:211], v173 offset:3072
	ds_read_b128 v[212:215], v173 offset:4096
	ds_read_b128 v[216:219], v173 offset:5120
	ds_read_b128 v[220:223], v173 offset:6144
	ds_read_b128 v[224:227], v173 offset:7168
	global_load_lds_dwordx4 v[228:229], off
	v_lshl_add_u64 v[228:229], s[48:49], 0, v[158:159]
	s_add_i32 m0, s47, 0xe000
	s_nop 0
	global_load_lds_dwordx4 v[228:229], off
	s_waitcnt vmcnt(8)
	s_waitcnt lgkmcnt(0)
	s_barrier
	s_setprio 1
	s_waitcnt lgkmcnt(0)
	v_mfma_f32_16x16x32_bf16 v[134:137], v[90:93], v[196:199], v[134:137]
	v_mfma_f32_16x16x32_bf16 v[130:133], v[164:167], v[196:199], v[130:133]
	v_mfma_f32_16x16x32_bf16 v[126:129], v[90:93], v[204:207], v[126:129]
	v_mfma_f32_16x16x32_bf16 v[122:125], v[164:167], v[204:207], v[122:125]
	v_mfma_f32_16x16x32_bf16 v[118:121], v[90:93], v[212:215], v[118:121]
	v_mfma_f32_16x16x32_bf16 v[114:117], v[164:167], v[212:215], v[114:117]
	v_mfma_f32_16x16x32_bf16 v[110:113], v[90:93], v[220:223], v[110:113]
	v_mfma_f32_16x16x32_bf16 v[106:109], v[164:167], v[220:223], v[106:109]
	v_mfma_f32_16x16x32_bf16 v[134:137], v[94:97], v[200:203], v[134:137]
	v_mfma_f32_16x16x32_bf16 v[130:133], v[176:179], v[200:203], v[130:133]
	v_mfma_f32_16x16x32_bf16 v[126:129], v[94:97], v[208:211], v[126:129]
	v_mfma_f32_16x16x32_bf16 v[122:125], v[176:179], v[208:211], v[122:125]
	v_mfma_f32_16x16x32_bf16 v[118:121], v[94:97], v[216:219], v[118:121]
	v_mfma_f32_16x16x32_bf16 v[114:117], v[176:179], v[216:219], v[114:117]
	v_mfma_f32_16x16x32_bf16 v[110:113], v[94:97], v[224:227], v[110:113]
	v_mfma_f32_16x16x32_bf16 v[106:109], v[176:179], v[224:227], v[106:109]
	s_setprio 0
	s_setprio 1
	v_mfma_f32_16x16x32_bf16 v[70:73], v[180:183], v[196:199], v[70:73]
	v_mfma_f32_16x16x32_bf16 v[66:69], v[188:191], v[196:199], v[66:69]
	v_mfma_f32_16x16x32_bf16 v[62:65], v[180:183], v[204:207], v[62:65]
	v_mfma_f32_16x16x32_bf16 v[58:61], v[188:191], v[204:207], v[58:61]
	v_mfma_f32_16x16x32_bf16 v[54:57], v[180:183], v[212:215], v[54:57]
	v_mfma_f32_16x16x32_bf16 v[50:53], v[188:191], v[212:215], v[50:53]
	v_mfma_f32_16x16x32_bf16 v[46:49], v[180:183], v[220:223], v[46:49]
	v_mfma_f32_16x16x32_bf16 v[42:45], v[188:191], v[220:223], v[42:45]
	v_mfma_f32_16x16x32_bf16 v[70:73], v[184:187], v[200:203], v[70:73]
	v_mfma_f32_16x16x32_bf16 v[66:69], v[192:195], v[200:203], v[66:69]
	v_mfma_f32_16x16x32_bf16 v[62:65], v[184:187], v[208:211], v[62:65]
	v_mfma_f32_16x16x32_bf16 v[58:61], v[192:195], v[208:211], v[58:61]
	v_mfma_f32_16x16x32_bf16 v[54:57], v[184:187], v[216:219], v[54:57]
	v_mfma_f32_16x16x32_bf16 v[50:53], v[192:195], v[216:219], v[50:53]
	v_mfma_f32_16x16x32_bf16 v[46:49], v[184:187], v[224:227], v[46:49]
	v_mfma_f32_16x16x32_bf16 v[42:45], v[192:195], v[224:227], v[42:45]
	s_setprio 0
	s_barrier
	s_add_i32 s48, s67, s4
	v_lshl_add_u64 v[228:229], s[50:51], 0, v[140:141]
	s_mov_b32 m0, s48
	ds_read_b128 v[196:199], v173 offset:16384
	ds_read_b128 v[200:203], v173 offset:17408
	ds_read_b128 v[204:207], v173 offset:18432
	ds_read_b128 v[208:211], v173 offset:19456
	ds_read_b128 v[212:215], v173 offset:20480
	ds_read_b128 v[216:219], v173 offset:21504
	ds_read_b128 v[220:223], v173 offset:22528
	ds_read_b128 v[224:227], v173 offset:23552
	global_load_lds_dwordx4 v[228:229], off
	s_add_i32 m0, s48, 0x2000
	s_add_u32 s48, s50, 0x20000
	v_lshl_add_u64 v[230:231], s[50:51], 0, v[144:145]
	s_addc_u32 s49, s51, 0
	s_add_i32 s78, s68, s4
	global_load_lds_dwordx4 v[230:231], off
	v_lshl_add_u64 v[232:233], s[48:49], 0, v[140:141]
	s_mov_b32 m0, s78
	v_lshl_add_u64 v[234:235], s[52:53], 0, v[142:143]
	global_load_lds_dwordx4 v[232:233], off
	v_lshl_add_u64 v[232:233], s[48:49], 0, v[144:145]
	s_add_i32 m0, s78, 0x2000
	s_nop 0
	global_load_lds_dwordx4 v[232:233], off
	s_waitcnt vmcnt(6)
	s_waitcnt lgkmcnt(0)
	s_barrier
	s_setprio 1
	s_waitcnt lgkmcnt(0)
	v_mfma_f32_16x16x32_bf16 v[102:105], v[90:93], v[196:199], v[102:105]
	v_mfma_f32_16x16x32_bf16 v[98:101], v[164:167], v[196:199], v[98:101]
	v_mfma_f32_16x16x32_bf16 v[86:89], v[90:93], v[204:207], v[86:89]
	v_mfma_f32_16x16x32_bf16 v[82:85], v[164:167], v[204:207], v[82:85]
	v_mfma_f32_16x16x32_bf16 v[78:81], v[90:93], v[212:215], v[78:81]
	v_mfma_f32_16x16x32_bf16 v[74:77], v[164:167], v[212:215], v[74:77]
	v_mfma_f32_16x16x32_bf16 v[26:29], v[90:93], v[220:223], v[26:29]
	v_mfma_f32_16x16x32_bf16 v[22:25], v[164:167], v[220:223], v[22:25]
	v_mfma_f32_16x16x32_bf16 v[102:105], v[94:97], v[200:203], v[102:105]
	v_mfma_f32_16x16x32_bf16 v[98:101], v[176:179], v[200:203], v[98:101]
	v_mfma_f32_16x16x32_bf16 v[86:89], v[94:97], v[208:211], v[86:89]
	v_mfma_f32_16x16x32_bf16 v[82:85], v[176:179], v[208:211], v[82:85]
	v_mfma_f32_16x16x32_bf16 v[78:81], v[94:97], v[216:219], v[78:81]
	v_mfma_f32_16x16x32_bf16 v[74:77], v[176:179], v[216:219], v[74:77]
	v_mfma_f32_16x16x32_bf16 v[26:29], v[94:97], v[224:227], v[26:29]
	v_mfma_f32_16x16x32_bf16 v[22:25], v[176:179], v[224:227], v[22:25]
	s_setprio 0
	s_setprio 1
	v_mfma_f32_16x16x32_bf16 v[38:41], v[180:183], v[196:199], v[38:41]
	v_mfma_f32_16x16x32_bf16 v[34:37], v[188:191], v[196:199], v[34:37]
	v_mfma_f32_16x16x32_bf16 v[30:33], v[180:183], v[204:207], v[30:33]
	v_mfma_f32_16x16x32_bf16 v[18:21], v[188:191], v[204:207], v[18:21]
	v_mfma_f32_16x16x32_bf16 v[14:17], v[180:183], v[212:215], v[14:17]
	v_mfma_f32_16x16x32_bf16 v[10:13], v[188:191], v[212:215], v[10:13]
	v_mfma_f32_16x16x32_bf16 v[6:9], v[180:183], v[220:223], v[6:9]
	v_mfma_f32_16x16x32_bf16 v[2:5], v[188:191], v[220:223], v[2:5]
	v_mfma_f32_16x16x32_bf16 v[38:41], v[184:187], v[200:203], v[38:41]
	v_mfma_f32_16x16x32_bf16 v[34:37], v[192:195], v[200:203], v[34:37]
	v_mfma_f32_16x16x32_bf16 v[30:33], v[184:187], v[208:211], v[30:33]
	v_mfma_f32_16x16x32_bf16 v[18:21], v[192:195], v[208:211], v[18:21]
	v_mfma_f32_16x16x32_bf16 v[14:17], v[184:187], v[216:219], v[14:17]
	v_mfma_f32_16x16x32_bf16 v[10:13], v[192:195], v[216:219], v[10:13]
	v_mfma_f32_16x16x32_bf16 v[6:9], v[184:187], v[224:227], v[6:9]
	v_mfma_f32_16x16x32_bf16 v[2:5], v[192:195], v[224:227], v[2:5]
	s_setprio 0
	s_barrier
	v_lshl_add_u64 v[232:233], s[52:53], 0, v[138:139]
	s_mov_b32 m0, s47
	s_nop 0
	global_load_lds_dwordx4 v[232:233], off
	s_mov_b32 m0, s33
	s_nop 0
	global_load_lds_dwordx4 v[234:235], off
	s_add_i32 s78, 0, 0x18000
	s_add_i32 s79, 0, 0x1c000
	v_add_u32_e32 v176, s78, v168
	v_add_u32_e32 v192, s79, v168
	ds_read_b128 v[90:93], v176
	ds_read_b128 v[94:97], v176 offset:1024
	ds_read_b128 v[164:167], v176 offset:2048
	ds_read_b128 v[176:179], v176 offset:3072
	ds_read_b128 v[180:183], v192
	ds_read_b128 v[184:187], v192 offset:1024
	ds_read_b128 v[188:191], v192 offset:2048
	ds_read_b128 v[192:195], v192 offset:3072
	s_add_u32 s48, s52, 0x50000
	s_addc_u32 s49, s53, 0
	s_mov_b32 m0, s57
	v_lshl_add_u64 v[236:237], s[48:49], 0, v[138:139]
	ds_read_b128 v[196:199], v173 offset:32768
	ds_read_b128 v[200:203], v173 offset:33792
	ds_read_b128 v[204:207], v173 offset:34816
	ds_read_b128 v[208:211], v173 offset:35840
	ds_read_b128 v[212:215], v173 offset:36864
	ds_read_b128 v[216:219], v173 offset:37888
	ds_read_b128 v[220:223], v173 offset:38912
	ds_read_b128 v[224:227], v173 offset:39936
	global_load_lds_dwordx4 v[236:237], off
	v_lshl_add_u64 v[236:237], s[48:49], 0, v[142:143]
	s_mov_b32 m0, s58
	s_nop 0
	global_load_lds_dwordx4 v[236:237], off
	s_waitcnt vmcnt(8)
	s_waitcnt lgkmcnt(0)
	s_barrier
	s_setprio 1
	s_waitcnt lgkmcnt(0)
	v_mfma_f32_16x16x32_bf16 v[134:137], v[90:93], v[196:199], v[134:137]
	v_mfma_f32_16x16x32_bf16 v[130:133], v[164:167], v[196:199], v[130:133]
	v_mfma_f32_16x16x32_bf16 v[126:129], v[90:93], v[204:207], v[126:129]
	v_mfma_f32_16x16x32_bf16 v[122:125], v[164:167], v[204:207], v[122:125]
	v_mfma_f32_16x16x32_bf16 v[118:121], v[90:93], v[212:215], v[118:121]
	v_mfma_f32_16x16x32_bf16 v[114:117], v[164:167], v[212:215], v[114:117]
	v_mfma_f32_16x16x32_bf16 v[110:113], v[90:93], v[220:223], v[110:113]
	v_mfma_f32_16x16x32_bf16 v[106:109], v[164:167], v[220:223], v[106:109]
	v_mfma_f32_16x16x32_bf16 v[134:137], v[94:97], v[200:203], v[134:137]
	v_mfma_f32_16x16x32_bf16 v[130:133], v[176:179], v[200:203], v[130:133]
	v_mfma_f32_16x16x32_bf16 v[126:129], v[94:97], v[208:211], v[126:129]
	v_mfma_f32_16x16x32_bf16 v[122:125], v[176:179], v[208:211], v[122:125]
	v_mfma_f32_16x16x32_bf16 v[118:121], v[94:97], v[216:219], v[118:121]
	v_mfma_f32_16x16x32_bf16 v[114:117], v[176:179], v[216:219], v[114:117]
	v_mfma_f32_16x16x32_bf16 v[110:113], v[94:97], v[224:227], v[110:113]
	v_mfma_f32_16x16x32_bf16 v[106:109], v[176:179], v[224:227], v[106:109]
	s_setprio 0
	s_setprio 1
	v_mfma_f32_16x16x32_bf16 v[70:73], v[180:183], v[196:199], v[70:73]
	v_mfma_f32_16x16x32_bf16 v[66:69], v[188:191], v[196:199], v[66:69]
	v_mfma_f32_16x16x32_bf16 v[62:65], v[180:183], v[204:207], v[62:65]
	v_mfma_f32_16x16x32_bf16 v[58:61], v[188:191], v[204:207], v[58:61]
	v_mfma_f32_16x16x32_bf16 v[54:57], v[180:183], v[212:215], v[54:57]
	v_mfma_f32_16x16x32_bf16 v[50:53], v[188:191], v[212:215], v[50:53]
	v_mfma_f32_16x16x32_bf16 v[46:49], v[180:183], v[220:223], v[46:49]
	v_mfma_f32_16x16x32_bf16 v[42:45], v[188:191], v[220:223], v[42:45]
	v_mfma_f32_16x16x32_bf16 v[70:73], v[184:187], v[200:203], v[70:73]
	v_mfma_f32_16x16x32_bf16 v[66:69], v[192:195], v[200:203], v[66:69]
	v_mfma_f32_16x16x32_bf16 v[62:65], v[184:187], v[208:211], v[62:65]
	v_mfma_f32_16x16x32_bf16 v[58:61], v[192:195], v[208:211], v[58:61]
	v_mfma_f32_16x16x32_bf16 v[54:57], v[184:187], v[216:219], v[54:57]
	v_mfma_f32_16x16x32_bf16 v[50:53], v[192:195], v[216:219], v[50:53]
	v_mfma_f32_16x16x32_bf16 v[46:49], v[184:187], v[224:227], v[46:49]
	v_mfma_f32_16x16x32_bf16 v[42:45], v[192:195], v[224:227], v[42:45]
	s_setprio 0
	s_barrier
	s_add_i32 s48, s78, s4
	v_lshl_add_u64 v[228:229], v[228:229], 0, s[34:35]
	s_mov_b32 m0, s48
	ds_read_b128 v[196:199], v173 offset:49152
	ds_read_b128 v[200:203], v173 offset:50176
	ds_read_b128 v[204:207], v173 offset:51200
	ds_read_b128 v[208:211], v173 offset:52224
	ds_read_b128 v[212:215], v173 offset:53248
	ds_read_b128 v[216:219], v173 offset:54272
	ds_read_b128 v[220:223], v173 offset:55296
	ds_read_b128 v[224:227], v173 offset:56320
	global_load_lds_dwordx4 v[228:229], off
	s_add_i32 m0, s48, 0x2000
	s_add_u32 s48, s50, 0x20080
	v_lshl_add_u64 v[228:229], v[230:231], 0, s[34:35]
	s_addc_u32 s49, s51, 0
	s_add_i32 s50, s79, s4
	global_load_lds_dwordx4 v[228:229], off
	v_lshl_add_u64 v[228:229], s[48:49], 0, v[140:141]
	s_mov_b32 m0, s50
	s_nop 0
	global_load_lds_dwordx4 v[228:229], off
	v_lshl_add_u64 v[228:229], s[48:49], 0, v[144:145]
	s_add_i32 m0, s50, 0x2000
	s_nop 0
	global_load_lds_dwordx4 v[228:229], off
	v_lshl_add_u64 v[240:241], v[232:233], 0, s[34:35]
	v_lshl_add_u64 v[242:243], v[234:235], 0, s[34:35]
	s_waitcnt vmcnt(6)
	s_waitcnt lgkmcnt(0)
	s_barrier
	s_setprio 1
	s_waitcnt lgkmcnt(0)
	v_mfma_f32_16x16x32_bf16 v[102:105], v[90:93], v[196:199], v[102:105]
	v_mfma_f32_16x16x32_bf16 v[98:101], v[164:167], v[196:199], v[98:101]
	v_mfma_f32_16x16x32_bf16 v[86:89], v[90:93], v[204:207], v[86:89]
	v_mfma_f32_16x16x32_bf16 v[82:85], v[164:167], v[204:207], v[82:85]
	v_mfma_f32_16x16x32_bf16 v[78:81], v[90:93], v[212:215], v[78:81]
	v_mfma_f32_16x16x32_bf16 v[74:77], v[164:167], v[212:215], v[74:77]
	v_mfma_f32_16x16x32_bf16 v[26:29], v[90:93], v[220:223], v[26:29]
	v_mfma_f32_16x16x32_bf16 v[22:25], v[164:167], v[220:223], v[22:25]
	v_mfma_f32_16x16x32_bf16 v[102:105], v[94:97], v[200:203], v[102:105]
	v_mfma_f32_16x16x32_bf16 v[98:101], v[176:179], v[200:203], v[98:101]
	v_mfma_f32_16x16x32_bf16 v[86:89], v[94:97], v[208:211], v[86:89]
	v_mfma_f32_16x16x32_bf16 v[82:85], v[176:179], v[208:211], v[82:85]
	v_mfma_f32_16x16x32_bf16 v[78:81], v[94:97], v[216:219], v[78:81]
	v_mfma_f32_16x16x32_bf16 v[74:77], v[176:179], v[216:219], v[74:77]
	v_mfma_f32_16x16x32_bf16 v[26:29], v[94:97], v[224:227], v[26:29]
	v_mfma_f32_16x16x32_bf16 v[22:25], v[176:179], v[224:227], v[22:25]
	s_setprio 0
	s_setprio 1
	v_mfma_f32_16x16x32_bf16 v[38:41], v[180:183], v[196:199], v[38:41]
	v_mfma_f32_16x16x32_bf16 v[34:37], v[188:191], v[196:199], v[34:37]
	v_mfma_f32_16x16x32_bf16 v[30:33], v[180:183], v[204:207], v[30:33]
	v_mfma_f32_16x16x32_bf16 v[18:21], v[188:191], v[204:207], v[18:21]
	v_mfma_f32_16x16x32_bf16 v[14:17], v[180:183], v[212:215], v[14:17]
	v_mfma_f32_16x16x32_bf16 v[10:13], v[188:191], v[212:215], v[10:13]
	v_mfma_f32_16x16x32_bf16 v[6:9], v[180:183], v[220:223], v[6:9]
	v_mfma_f32_16x16x32_bf16 v[2:5], v[188:191], v[220:223], v[2:5]
	v_mfma_f32_16x16x32_bf16 v[38:41], v[184:187], v[200:203], v[38:41]
	v_mfma_f32_16x16x32_bf16 v[34:37], v[192:195], v[200:203], v[34:37]
	v_mfma_f32_16x16x32_bf16 v[30:33], v[184:187], v[208:211], v[30:33]
	v_mfma_f32_16x16x32_bf16 v[18:21], v[192:195], v[208:211], v[18:21]
	v_mfma_f32_16x16x32_bf16 v[14:17], v[184:187], v[216:219], v[14:17]
	v_mfma_f32_16x16x32_bf16 v[10:13], v[192:195], v[216:219], v[10:13]
	v_mfma_f32_16x16x32_bf16 v[6:9], v[184:187], v[224:227], v[6:9]
	v_mfma_f32_16x16x32_bf16 v[2:5], v[192:195], v[224:227], v[2:5]
	s_setprio 0
	s_barrier
	s_mov_b32 s99, 1
	s_add_i32 s77, s77, 2
	s_add_u32 s75, s75, 0x100
	s_addc_u32 s76, s76, 0
	s_cmp_gt_u32 s77, 5
	s_mov_b64 s[48:49], s[10:11]
	s_cbranch_scc0 .LBB0_354
	s_and_b64 vcc, exec, s[36:37]
	s_cbranch_vccz .LBB0_357
	s_barrier

.LBB0_692:
	s_mov_b32 s99, 0
	v_readlane_b32 s0, v253, 11
	v_readlane_b32 s1, v253, 12
	s_mov_b32 s3, s1
	s_cmp_lt_i32 s0, 9
	s_cselect_b64 s[0:1], -1, 0
	s_cmp_gt_i32 s3, 8
	s_cselect_b64 s[4:5], -1, 0
	s_and_b64 s[0:1], s[0:1], s[4:5]
	s_andn2_b64 vcc, exec, s[0:1]
	s_cbranch_vccnz .LBB0_739
	v_readlane_b32 s6, v253, 0
	v_readlane_b32 s7, v253, 1
	s_load_dwordx2 s[12:13], s[6:7], 0x80
	s_load_dwordx2 s[14:15], s[6:7], 0xa0
	s_load_dwordx4 s[8:11], s[6:7], 0xb0
	s_load_dwordx2 s[16:17], s[6:7], 0xc0
	s_load_dwordx2 s[18:19], s[6:7], 0xd0
	v_mov_b32_e32 v11, v0
	s_cmpk_lt_i32 s2, 0x208
	s_nop 0
	v_readfirstlane_b32 s31, v11
	s_cbranch_scc0 .LBB0_709
	v_lshlrev_b32_e32 v1, 4, v11
	v_add_u32_e32 v2, 0x2000, v1
	v_ashrrev_i32_e32 v3, 31, v2
	v_lshrrev_b32_e32 v3, 22, v3
	v_add_u32_e32 v3, v2, v3
	v_ashrrev_i32_e32 v10, 10, v3
	v_mul_i32_i24_e32 v3, 0x400, v10
	v_sub_u32_e32 v2, v2, v3
	v_lshrrev_b32_e32 v3, 4, v2
	v_bitop3_b32 v2, v3, v2, 32 bitop3:0x6c
	v_ashrrev_i32_e32 v3, 31, v2
	v_lshrrev_b32_e32 v3, 26, v3
	v_add_u32_e32 v3, v2, v3
	v_lshlrev_b32_e32 v4, 3, v10
	v_ashrrev_i32_e32 v12, 6, v3
	v_and_b32_e32 v4, -16, v4
	v_add_u32_e32 v4, v12, v4
	v_and_b32_e32 v5, 3, v12
	s_mov_b32 s20, 0xfffe0
	v_lshrrev_b32_e32 v6, 2, v4
	v_lshlrev_b32_e32 v7, 1, v4
	v_and_b32_e32 v3, 0xc0, v3
	v_and_or_b32 v5, v4, s20, v5
	v_and_b32_e32 v6, 4, v6
	v_and_b32_e32 v7, 24, v7
	v_sub_u32_e32 v2, v2, v3
	v_mov_b32_e32 v3, 1
	v_or3_b32 v5, v5, v6, v7
	v_lshlrev_b32_e32 v6, 5, v10
	v_ashrrev_i16_sdwa v2, v3, sext(v2) dst_sel:DWORD dst_unused:UNUSED_PAD src0_sel:DWORD src1_sel:BYTE_0
	v_and_b32_e32 v6, 32, v6
	v_bfe_i32 v13, v2, 0, 16
	v_add_lshl_u32 v2, v6, v13, 1
	v_lshl_add_u32 v146, v5, 12, v2
	v_lshl_add_u32 v148, v4, 12, v2
	v_bfe_i32 v2, v11, 27, 1
	v_lshrrev_b32_e32 v2, 22, v2
	v_add_u32_e32 v2, v1, v2
	v_and_b32_e32 v2, 0xfffffc00, v2
	v_sub_u32_e32 v1, v1, v2
	v_lshrrev_b32_e32 v2, 4, v1
	v_bitop3_b32 v2, v2, v1, 32 bitop3:0x6c
	v_ashrrev_i32_e32 v1, 31, v1
	v_lshrrev_b32_e32 v1, 26, v1
	v_add_u32_e32 v1, v2, v1
	v_ashrrev_i32_e32 v14, 6, v1
	v_ashrrev_i32_e32 v1, 31, v11
	v_lshrrev_b32_e32 v1, 26, v1
	v_add_u32_e32 v1, v11, v1
	s_waitcnt lgkmcnt(0)
	s_add_u32 s0, s18, 0x46300000
	v_ashrrev_i32_e32 v15, 6, v1
	s_addc_u32 s1, s19, 0
	v_lshlrev_b32_e32 v1, 3, v15
	s_add_u32 s3, s18, 0x1800000
	v_and_b32_e32 v1, -16, v1
	s_addc_u32 s4, s19, 0
	v_add_u32_e32 v1, v14, v1
	v_and_b32_e32 v4, 3, v14
	s_ashr_i32 s33, s2, 31
	v_and_or_b32 v4, v1, s20, v4
	s_lshr_b32 s20, s33, 29
	s_add_i32 s20, s2, s20
	s_ashr_i32 s28, s31, 6
	s_ashr_i32 s21, s20, 3
	s_and_b32 s20, s20, -8
	s_ashr_i32 s34, s31, 8
	s_lshl_b32 s5, s28, 10
	s_sub_i32 s20, s2, s20
	s_cmp_lt_i32 s20, 0
	s_movk_i32 s52, 0x42
	s_cselect_b32 s22, s52, 0x41
	s_mul_i32 s20, s20, s22
	s_add_i32 s20, s20, s21
	v_lshrrev_b32_e32 v5, 2, v1
	v_lshlrev_b32_e32 v6, 1, v1
	s_ashr_i32 s21, s20, 31
	v_and_b32_e32 v5, 4, v5
	v_and_b32_e32 v6, 24, v6
	s_lshr_b32 s21, s21, 26
	v_or3_b32 v4, v4, v5, v6
	v_mul_i32_i24_e32 v6, 64, v14
	s_add_i32 s21, s20, s21
	v_sub_u32_e32 v2, v2, v6
	s_ashr_i32 s21, s21, 6
	v_lshlrev_b32_e32 v5, 5, v15
	v_ashrrev_i16_sdwa v2, v3, sext(v2) dst_sel:DWORD dst_unused:UNUSED_PAD src0_sel:DWORD src1_sel:BYTE_0
	s_lshl_b32 s22, s21, 3
	v_and_b32_e32 v5, 32, v5
	v_bfe_i32 v16, v2, 0, 16
	s_sub_i32 s23, 0x41, s22
	s_lshl_b32 s21, s21, 6
	v_add_lshl_u32 v2, v5, v16, 1
	s_min_u32 s23, s23, 8
	s_sub_i32 s24, s20, s21
	v_lshl_add_u32 v150, v4, 12, v2
	s_sext_i32_i8 s20, s24
	v_cvt_f32_ubyte0_e32 v4, s23
	v_cvt_f32_i32_e32 v3, s20
	v_rcp_iflag_f32_e32 v5, v4
	v_lshl_add_u32 v152, v1, 12, v2
	s_ashr_i32 s20, s20, 30
	s_or_b32 s25, s20, 1
	v_mul_f32_e32 v1, v3, v5
	v_trunc_f32_e32 v1, v1
	v_fma_f32 v2, -v1, v4, v3
	v_cvt_i32_f32_e32 v1, v1
	v_cmp_ge_f32_e64 s[20:21], |v2|, v4
	s_and_b64 s[20:21], s[20:21], exec
	s_cselect_b32 s20, s25, 0
	v_readfirstlane_b32 s21, v1
	s_add_i32 s30, s21, s20
	s_mul_i32 s20, s30, s23
	s_sub_i32 s20, s24, s20
	s_sext_i32_i8 s20, s20
	s_add_i32 s44, s22, s20
	s_ashr_i32 s45, s44, 31
	s_bfe_i64 s[22:23], s[30:31], 0x80000
	s_lshl_b64 s[20:21], s[44:45], 20
	s_lshl_b64 s[22:23], s[22:23], 20
	s_add_u32 s48, s3, s22
	s_addc_u32 s49, s4, s23
	s_add_i32 s45, s5, 0
	s_add_i32 m0, s45, 0x10000
	v_mov_b32_e32 v151, 0
	global_load_lds_dwordx4 v150, s[48:49]
	s_add_i32 m0, s45, 0x12000
	s_add_u32 s22, s48, 0x80000
	global_load_lds_dwordx4 v146, s[48:49]
	s_addc_u32 s23, s49, 0
	s_add_i32 m0, s45, 0x14000
	v_mov_b32_e32 v147, v151
	global_load_lds_dwordx4 v150, s[22:23]
	s_add_i32 m0, s45, 0x16000
	s_add_u32 s46, s0, s20
	s_addc_u32 s47, s1, s21
	s_add_i32 s53, s45, 0x2000
	global_load_lds_dwordx4 v146, s[22:23]
	s_mov_b32 m0, s45
	s_add_u32 s20, s46, 0x80000
	global_load_lds_dwordx4 v152, s[46:47]
	s_mov_b32 m0, s53
	s_addc_u32 s21, s47, 0
	s_add_i32 s54, s45, 0x4000
	global_load_lds_dwordx4 v148, s[46:47]
	s_mov_b32 m0, s54
	s_add_i32 s55, s45, 0x6000
	global_load_lds_dwordx4 v152, s[20:21]
	s_mov_b32 m0, s55
	v_mov_b32_e32 v153, v151
	global_load_lds_dwordx4 v148, s[20:21]
	s_load_dwordx2 s[20:21], s[6:7], 0x0
	s_load_dwordx2 s[22:23], s[6:7], 0x10
	v_mov_b32_e32 v149, v151
	s_cmp_eq_u32 s34, 1
	s_mov_b32 s56, 0
	v_lshl_add_u64 v[8:9], s[48:49], 0, v[150:151]
	v_lshl_add_u64 v[6:7], s[48:49], 0, v[146:147]
	v_lshl_add_u64 v[4:5], s[46:47], 0, v[152:153]
	v_lshl_add_u64 v[2:3], s[46:47], 0, v[148:149]
	s_cselect_b64 s[24:25], -1, 0
	s_cmp_lg_u32 s34, 1
	s_movk_i32 s57, 0x4000
	s_cbranch_scc1 .LBB0_696
	s_barrier

.Lbal_skip_702:
	ds_read_b128 v[130:133], v170
	ds_read_b128 v[134:137], v170 offset:1024
	ds_read_b128 v[138:141], v170 offset:2048
	ds_read_b128 v[142:145], v170 offset:3072
	ds_read_b128 v[162:165], v171
	ds_read_b128 v[174:177], v171 offset:1024
	ds_read_b128 v[178:181], v171 offset:2048
	ds_read_b128 v[182:185], v171 offset:3072
	s_add_u32 s48, s46, 0xfff80080
	s_addc_u32 s49, s47, -1
	s_cmp_eq_u32 s72, 28
	s_cselect_b32 s51, s39, s49
	s_cselect_b32 s50, s68, s48
	s_cselect_b32 s49, s37, s71
	s_cselect_b32 s48, s69, s70
	v_lshl_add_u64 v[166:167], s[46:47], 0, v[154:155]
	s_add_i32 m0, s45, 0xc000
	ds_read_b128 v[186:189], v172
	ds_read_b128 v[190:193], v172 offset:1024
	ds_read_b128 v[194:197], v172 offset:2048
	ds_read_b128 v[198:201], v172 offset:3072
	ds_read_b128 v[202:205], v172 offset:4096
	ds_read_b128 v[206:209], v172 offset:5120
	ds_read_b128 v[210:213], v172 offset:6144
	ds_read_b128 v[214:217], v172 offset:7168
	global_load_lds_dwordx4 v[166:167], off
	v_lshl_add_u64 v[166:167], s[46:47], 0, v[156:157]
	s_add_i32 m0, s45, 0xe000
	s_nop 0
	global_load_lds_dwordx4 v[166:167], off
	s_waitcnt vmcnt(8)
	s_waitcnt lgkmcnt(0)
	s_barrier
	s_setprio 1
	s_waitcnt lgkmcnt(0)
	v_mfma_f32_16x16x32_bf16 v[126:129], v[130:133], v[186:189], v[126:129]
	v_mfma_f32_16x16x32_bf16 v[122:125], v[138:141], v[186:189], v[122:125]
	v_mfma_f32_16x16x32_bf16 v[118:121], v[130:133], v[194:197], v[118:121]
	v_mfma_f32_16x16x32_bf16 v[110:113], v[138:141], v[194:197], v[110:113]
	v_mfma_f32_16x16x32_bf16 v[102:105], v[130:133], v[202:205], v[102:105]
	v_mfma_f32_16x16x32_bf16 v[94:97], v[138:141], v[202:205], v[94:97]
	v_mfma_f32_16x16x32_bf16 v[86:89], v[130:133], v[210:213], v[86:89]
	v_mfma_f32_16x16x32_bf16 v[78:81], v[138:141], v[210:213], v[78:81]
	v_mfma_f32_16x16x32_bf16 v[126:129], v[134:137], v[190:193], v[126:129]
	v_mfma_f32_16x16x32_bf16 v[122:125], v[142:145], v[190:193], v[122:125]
	v_mfma_f32_16x16x32_bf16 v[118:121], v[134:137], v[198:201], v[118:121]
	v_mfma_f32_16x16x32_bf16 v[110:113], v[142:145], v[198:201], v[110:113]
	v_mfma_f32_16x16x32_bf16 v[102:105], v[134:137], v[206:209], v[102:105]
	v_mfma_f32_16x16x32_bf16 v[94:97], v[142:145], v[206:209], v[94:97]
	v_mfma_f32_16x16x32_bf16 v[86:89], v[134:137], v[214:217], v[86:89]
	v_mfma_f32_16x16x32_bf16 v[78:81], v[142:145], v[214:217], v[78:81]
	s_setprio 0
	s_setprio 1
	v_mfma_f32_16x16x32_bf16 v[114:117], v[162:165], v[186:189], v[114:117]
	v_mfma_f32_16x16x32_bf16 v[106:109], v[178:181], v[186:189], v[106:109]
	v_mfma_f32_16x16x32_bf16 v[98:101], v[162:165], v[194:197], v[98:101]
	v_mfma_f32_16x16x32_bf16 v[90:93], v[178:181], v[194:197], v[90:93]
	v_mfma_f32_16x16x32_bf16 v[82:85], v[162:165], v[202:205], v[82:85]
	v_mfma_f32_16x16x32_bf16 v[74:77], v[178:181], v[202:205], v[74:77]
	v_mfma_f32_16x16x32_bf16 v[70:73], v[162:165], v[210:213], v[70:73]
	v_mfma_f32_16x16x32_bf16 v[66:69], v[178:181], v[210:213], v[66:69]
	v_mfma_f32_16x16x32_bf16 v[114:117], v[174:177], v[190:193], v[114:117]
	v_mfma_f32_16x16x32_bf16 v[106:109], v[182:185], v[190:193], v[106:109]
	v_mfma_f32_16x16x32_bf16 v[98:101], v[174:177], v[198:201], v[98:101]
	v_mfma_f32_16x16x32_bf16 v[90:93], v[182:185], v[198:201], v[90:93]
	v_mfma_f32_16x16x32_bf16 v[82:85], v[174:177], v[206:209], v[82:85]
	v_mfma_f32_16x16x32_bf16 v[74:77], v[182:185], v[206:209], v[74:77]
	v_mfma_f32_16x16x32_bf16 v[70:73], v[174:177], v[214:217], v[70:73]
	v_mfma_f32_16x16x32_bf16 v[66:69], v[182:185], v[214:217], v[66:69]
	s_setprio 0
	s_barrier
	s_add_i32 s73, s64, s5
	v_lshl_add_u64 v[166:167], s[48:49], 0, v[150:151]
	s_mov_b32 m0, s73
	ds_read_b128 v[186:189], v172 offset:16384
	ds_read_b128 v[190:193], v172 offset:17408
	ds_read_b128 v[194:197], v172 offset:18432
	ds_read_b128 v[198:201], v172 offset:19456
	ds_read_b128 v[202:205], v172 offset:20480
	ds_read_b128 v[206:209], v172 offset:21504
	ds_read_b128 v[210:213], v172 offset:22528
	ds_read_b128 v[214:217], v172 offset:23552
	global_load_lds_dwordx4 v[166:167], off
	s_add_i32 m0, s73, 0x2000
	s_add_u32 s74, s48, 0x80000
	v_lshl_add_u64 v[218:219], s[48:49], 0, v[146:147]
	s_addc_u32 s75, s49, 0
	s_add_i32 s73, s65, s5
	global_load_lds_dwordx4 v[218:219], off
	v_lshl_add_u64 v[220:221], s[74:75], 0, v[150:151]
	s_mov_b32 m0, s73
	v_lshl_add_u64 v[222:223], s[50:51], 0, v[148:149]
	global_load_lds_dwordx4 v[220:221], off
	v_lshl_add_u64 v[220:221], s[74:75], 0, v[146:147]
	s_add_i32 m0, s73, 0x2000
	s_nop 0
	global_load_lds_dwordx4 v[220:221], off
	s_waitcnt vmcnt(6)
	s_waitcnt lgkmcnt(0)
	s_barrier
	s_setprio 1
	s_waitcnt lgkmcnt(0)
	v_mfma_f32_16x16x32_bf16 v[62:65], v[130:133], v[186:189], v[62:65]
	v_mfma_f32_16x16x32_bf16 v[58:61], v[138:141], v[186:189], v[58:61]
	v_mfma_f32_16x16x32_bf16 v[54:57], v[130:133], v[194:197], v[54:57]
	v_mfma_f32_16x16x32_bf16 v[46:49], v[138:141], v[194:197], v[46:49]
	v_mfma_f32_16x16x32_bf16 v[38:41], v[130:133], v[202:205], v[38:41]
	v_mfma_f32_16x16x32_bf16 v[30:33], v[138:141], v[202:205], v[30:33]
	v_mfma_f32_16x16x32_bf16 v[22:25], v[130:133], v[210:213], v[22:25]
	v_mfma_f32_16x16x32_bf16 v[14:17], v[138:141], v[210:213], v[14:17]
	v_mfma_f32_16x16x32_bf16 v[62:65], v[134:137], v[190:193], v[62:65]
	v_mfma_f32_16x16x32_bf16 v[58:61], v[142:145], v[190:193], v[58:61]
	v_mfma_f32_16x16x32_bf16 v[54:57], v[134:137], v[198:201], v[54:57]
	v_mfma_f32_16x16x32_bf16 v[46:49], v[142:145], v[198:201], v[46:49]
	v_mfma_f32_16x16x32_bf16 v[38:41], v[134:137], v[206:209], v[38:41]
	v_mfma_f32_16x16x32_bf16 v[30:33], v[142:145], v[206:209], v[30:33]
	v_mfma_f32_16x16x32_bf16 v[22:25], v[134:137], v[214:217], v[22:25]
	v_mfma_f32_16x16x32_bf16 v[14:17], v[142:145], v[214:217], v[14:17]
	s_setprio 0
	s_setprio 1
	v_mfma_f32_16x16x32_bf16 v[50:53], v[162:165], v[186:189], v[50:53]
	v_mfma_f32_16x16x32_bf16 v[42:45], v[178:181], v[186:189], v[42:45]
	v_mfma_f32_16x16x32_bf16 v[34:37], v[162:165], v[194:197], v[34:37]
	v_mfma_f32_16x16x32_bf16 v[26:29], v[178:181], v[194:197], v[26:29]
	v_mfma_f32_16x16x32_bf16 v[18:21], v[162:165], v[202:205], v[18:21]
	v_mfma_f32_16x16x32_bf16 v[10:13], v[178:181], v[202:205], v[10:13]
	v_mfma_f32_16x16x32_bf16 v[6:9], v[162:165], v[210:213], v[6:9]
	v_mfma_f32_16x16x32_bf16 v[2:5], v[178:181], v[210:213], v[2:5]
	v_mfma_f32_16x16x32_bf16 v[50:53], v[174:177], v[190:193], v[50:53]
	v_mfma_f32_16x16x32_bf16 v[42:45], v[182:185], v[190:193], v[42:45]
	v_mfma_f32_16x16x32_bf16 v[34:37], v[174:177], v[198:201], v[34:37]
	v_mfma_f32_16x16x32_bf16 v[26:29], v[182:185], v[198:201], v[26:29]
	v_mfma_f32_16x16x32_bf16 v[18:21], v[174:177], v[206:209], v[18:21]
	v_mfma_f32_16x16x32_bf16 v[10:13], v[182:185], v[206:209], v[10:13]
	v_mfma_f32_16x16x32_bf16 v[6:9], v[174:177], v[214:217], v[6:9]
	v_mfma_f32_16x16x32_bf16 v[2:5], v[182:185], v[214:217], v[2:5]
	s_setprio 0
	s_barrier
	v_lshl_add_u64 v[220:221], s[50:51], 0, v[152:153]
	s_mov_b32 m0, s45
	s_nop 0
	global_load_lds_dwordx4 v[220:221], off
	s_mov_b32 m0, s53
	s_nop 0
	global_load_lds_dwordx4 v[222:223], off
	s_add_i32 s73, 0, 0x18000
	s_add_i32 s74, 0, 0x1c000
	v_add_u32_e32 v142, s73, v168
	v_add_u32_e32 v173, s74, v168
	ds_read_b128 v[130:133], v142
	ds_read_b128 v[134:137], v142 offset:1024
	ds_read_b128 v[138:141], v142 offset:2048
	ds_read_b128 v[142:145], v142 offset:3072
	ds_read_b128 v[162:165], v173
	ds_read_b128 v[174:177], v173 offset:1024
	ds_read_b128 v[178:181], v173 offset:2048
	ds_read_b128 v[182:185], v173 offset:3072
	s_add_u32 s50, s50, 0x80000
	s_addc_u32 s51, s51, 0
	s_mov_b32 m0, s54
	v_lshl_add_u64 v[224:225], s[50:51], 0, v[152:153]
	ds_read_b128 v[186:189], v172 offset:32768
	ds_read_b128 v[190:193], v172 offset:33792
	ds_read_b128 v[194:197], v172 offset:34816
	ds_read_b128 v[198:201], v172 offset:35840
	ds_read_b128 v[202:205], v172 offset:36864
	ds_read_b128 v[206:209], v172 offset:37888
	ds_read_b128 v[210:213], v172 offset:38912
	ds_read_b128 v[214:217], v172 offset:39936
	global_load_lds_dwordx4 v[224:225], off
	v_lshl_add_u64 v[224:225], s[50:51], 0, v[148:149]
	s_mov_b32 m0, s55
	s_nop 0
	global_load_lds_dwordx4 v[224:225], off
	s_waitcnt vmcnt(8)
	s_waitcnt lgkmcnt(0)
	s_barrier
	s_setprio 1
	s_waitcnt lgkmcnt(0)
	v_mfma_f32_16x16x32_bf16 v[126:129], v[130:133], v[186:189], v[126:129]
	v_mfma_f32_16x16x32_bf16 v[122:125], v[138:141], v[186:189], v[122:125]
	v_mfma_f32_16x16x32_bf16 v[118:121], v[130:133], v[194:197], v[118:121]
	v_mfma_f32_16x16x32_bf16 v[110:113], v[138:141], v[194:197], v[110:113]
	v_mfma_f32_16x16x32_bf16 v[102:105], v[130:133], v[202:205], v[102:105]
	v_mfma_f32_16x16x32_bf16 v[94:97], v[138:141], v[202:205], v[94:97]
	v_mfma_f32_16x16x32_bf16 v[86:89], v[130:133], v[210:213], v[86:89]
	v_mfma_f32_16x16x32_bf16 v[78:81], v[138:141], v[210:213], v[78:81]
	v_mfma_f32_16x16x32_bf16 v[126:129], v[134:137], v[190:193], v[126:129]
	v_mfma_f32_16x16x32_bf16 v[122:125], v[142:145], v[190:193], v[122:125]
	v_mfma_f32_16x16x32_bf16 v[118:121], v[134:137], v[198:201], v[118:121]
	v_mfma_f32_16x16x32_bf16 v[110:113], v[142:145], v[198:201], v[110:113]
	v_mfma_f32_16x16x32_bf16 v[102:105], v[134:137], v[206:209], v[102:105]
	v_mfma_f32_16x16x32_bf16 v[94:97], v[142:145], v[206:209], v[94:97]
	v_mfma_f32_16x16x32_bf16 v[86:89], v[134:137], v[214:217], v[86:89]
	v_mfma_f32_16x16x32_bf16 v[78:81], v[142:145], v[214:217], v[78:81]
	s_setprio 0
	s_setprio 1
	v_mfma_f32_16x16x32_bf16 v[114:117], v[162:165], v[186:189], v[114:117]
	v_mfma_f32_16x16x32_bf16 v[106:109], v[178:181], v[186:189], v[106:109]
	v_mfma_f32_16x16x32_bf16 v[98:101], v[162:165], v[194:197], v[98:101]
	v_mfma_f32_16x16x32_bf16 v[90:93], v[178:181], v[194:197], v[90:93]
	v_mfma_f32_16x16x32_bf16 v[82:85], v[162:165], v[202:205], v[82:85]
	v_mfma_f32_16x16x32_bf16 v[74:77], v[178:181], v[202:205], v[74:77]
	v_mfma_f32_16x16x32_bf16 v[70:73], v[162:165], v[210:213], v[70:73]
	v_mfma_f32_16x16x32_bf16 v[66:69], v[178:181], v[210:213], v[66:69]
	v_mfma_f32_16x16x32_bf16 v[114:117], v[174:177], v[190:193], v[114:117]
	v_mfma_f32_16x16x32_bf16 v[106:109], v[182:185], v[190:193], v[106:109]
	v_mfma_f32_16x16x32_bf16 v[98:101], v[174:177], v[198:201], v[98:101]
	v_mfma_f32_16x16x32_bf16 v[90:93], v[182:185], v[198:201], v[90:93]
	v_mfma_f32_16x16x32_bf16 v[82:85], v[174:177], v[206:209], v[82:85]
	v_mfma_f32_16x16x32_bf16 v[74:77], v[182:185], v[206:209], v[74:77]
	v_mfma_f32_16x16x32_bf16 v[70:73], v[174:177], v[214:217], v[70:73]
	v_mfma_f32_16x16x32_bf16 v[66:69], v[182:185], v[214:217], v[66:69]
	s_setprio 0
	s_barrier
	s_add_i32 s50, s73, s5
	v_lshl_add_u64 v[166:167], v[166:167], 0, s[28:29]
	s_mov_b32 m0, s50
	ds_read_b128 v[186:189], v172 offset:49152
	ds_read_b128 v[190:193], v172 offset:50176
	ds_read_b128 v[194:197], v172 offset:51200
	ds_read_b128 v[198:201], v172 offset:52224
	ds_read_b128 v[202:205], v172 offset:53248
	ds_read_b128 v[206:209], v172 offset:54272
	ds_read_b128 v[210:213], v172 offset:55296
	ds_read_b128 v[214:217], v172 offset:56320
	global_load_lds_dwordx4 v[166:167], off
	s_add_i32 m0, s50, 0x2000
	s_add_u32 s48, s48, 0x80080
	v_lshl_add_u64 v[166:167], v[218:219], 0, s[28:29]
	s_addc_u32 s49, s49, 0
	s_add_i32 s50, s74, s5
	global_load_lds_dwordx4 v[166:167], off
	v_lshl_add_u64 v[166:167], s[48:49], 0, v[150:151]
	s_mov_b32 m0, s50
	s_nop 0
	global_load_lds_dwordx4 v[166:167], off
	v_lshl_add_u64 v[166:167], s[48:49], 0, v[146:147]
	s_add_i32 m0, s50, 0x2000
	s_nop 0
	global_load_lds_dwordx4 v[166:167], off
	v_lshl_add_u64 v[240:241], v[220:221], 0, s[28:29]
	v_lshl_add_u64 v[242:243], v[222:223], 0, s[28:29]
	s_waitcnt vmcnt(6)
	s_waitcnt lgkmcnt(0)
	s_barrier
	s_setprio 1
	s_waitcnt lgkmcnt(0)
	v_mfma_f32_16x16x32_bf16 v[62:65], v[130:133], v[186:189], v[62:65]
	v_mfma_f32_16x16x32_bf16 v[58:61], v[138:141], v[186:189], v[58:61]
	v_mfma_f32_16x16x32_bf16 v[54:57], v[130:133], v[194:197], v[54:57]
	v_mfma_f32_16x16x32_bf16 v[46:49], v[138:141], v[194:197], v[46:49]
	v_mfma_f32_16x16x32_bf16 v[38:41], v[130:133], v[202:205], v[38:41]
	v_mfma_f32_16x16x32_bf16 v[30:33], v[138:141], v[202:205], v[30:33]
	v_mfma_f32_16x16x32_bf16 v[22:25], v[130:133], v[210:213], v[22:25]
	v_mfma_f32_16x16x32_bf16 v[14:17], v[138:141], v[210:213], v[14:17]
	v_mfma_f32_16x16x32_bf16 v[62:65], v[134:137], v[190:193], v[62:65]
	v_mfma_f32_16x16x32_bf16 v[58:61], v[142:145], v[190:193], v[58:61]
	v_mfma_f32_16x16x32_bf16 v[54:57], v[134:137], v[198:201], v[54:57]
	v_mfma_f32_16x16x32_bf16 v[46:49], v[142:145], v[198:201], v[46:49]
	v_mfma_f32_16x16x32_bf16 v[38:41], v[134:137], v[206:209], v[38:41]
	v_mfma_f32_16x16x32_bf16 v[30:33], v[142:145], v[206:209], v[30:33]
	v_mfma_f32_16x16x32_bf16 v[22:25], v[134:137], v[214:217], v[22:25]
	v_mfma_f32_16x16x32_bf16 v[14:17], v[142:145], v[214:217], v[14:17]
	s_setprio 0
	s_setprio 1
	v_mfma_f32_16x16x32_bf16 v[50:53], v[162:165], v[186:189], v[50:53]
	v_mfma_f32_16x16x32_bf16 v[42:45], v[178:181], v[186:189], v[42:45]
	v_mfma_f32_16x16x32_bf16 v[34:37], v[162:165], v[194:197], v[34:37]
	v_mfma_f32_16x16x32_bf16 v[26:29], v[178:181], v[194:197], v[26:29]
	v_mfma_f32_16x16x32_bf16 v[18:21], v[162:165], v[202:205], v[18:21]
	v_mfma_f32_16x16x32_bf16 v[10:13], v[178:181], v[202:205], v[10:13]
	v_mfma_f32_16x16x32_bf16 v[6:9], v[162:165], v[210:213], v[6:9]
	v_mfma_f32_16x16x32_bf16 v[2:5], v[178:181], v[210:213], v[2:5]
	v_mfma_f32_16x16x32_bf16 v[50:53], v[174:177], v[190:193], v[50:53]
	v_mfma_f32_16x16x32_bf16 v[42:45], v[182:185], v[190:193], v[42:45]
	v_mfma_f32_16x16x32_bf16 v[34:37], v[174:177], v[198:201], v[34:37]
	v_mfma_f32_16x16x32_bf16 v[26:29], v[182:185], v[198:201], v[26:29]
	v_mfma_f32_16x16x32_bf16 v[18:21], v[174:177], v[206:209], v[18:21]
	v_mfma_f32_16x16x32_bf16 v[10:13], v[182:185], v[206:209], v[10:13]
	v_mfma_f32_16x16x32_bf16 v[6:9], v[174:177], v[214:217], v[6:9]
	v_mfma_f32_16x16x32_bf16 v[2:5], v[182:185], v[214:217], v[2:5]
	s_setprio 0
	s_barrier
	s_mov_b32 s99, 1
	s_add_i32 s72, s72, 2
	s_add_u32 s46, s46, 0x100
	s_addc_u32 s47, s47, 0
	s_add_u32 s70, s70, 0x100
	s_addc_u32 s71, s71, 0
	s_cmp_gt_u32 s72, 29
	s_cbranch_scc0 .LBB0_702
	s_and_b64 vcc, exec, s[30:31]
	s_cbranch_vccz .LBB0_705
	s_barrier

.LBB0_1088:
	s_mov_b32 s99, 0
	v_readlane_b32 s0, v253, 11
	v_readlane_b32 s1, v253, 12
	s_mov_b32 s3, s1
	s_cmp_lt_i32 s0, 13
	s_cselect_b64 s[0:1], -1, 0
	s_cmp_gt_i32 s3, 12
	s_cselect_b64 s[4:5], -1, 0
	s_and_b64 s[0:1], s[0:1], s[4:5]
	s_andn2_b64 vcc, exec, s[0:1]
	s_cbranch_vccnz .LBB0_1137
	v_readlane_b32 s0, v253, 0
	v_readlane_b32 s1, v253, 1
	s_load_dwordx2 s[12:13], s[0:1], 0xd0
	s_load_dwordx2 s[14:15], s[0:1], 0x80
	s_load_dwordx2 s[16:17], s[0:1], 0xa0
	s_load_dwordx4 s[8:11], s[0:1], 0xb0
	s_load_dwordx2 s[18:19], s[0:1], 0xc0
	s_waitcnt lgkmcnt(0)
	s_add_u32 s0, s12, 0x4000000
	s_addc_u32 s1, s13, 0
	v_mov_b32_e32 v6, v0
	s_cmpk_lt_i32 s2, 0x630
	s_nop 0
	v_readfirstlane_b32 s34, v6
	s_cbranch_scc0 .LBB0_1107
	s_add_u32 s20, s12, 0x25000000
	v_ashrrev_i32_e32 v1, 31, v6
	s_addc_u32 s21, s13, 0
	v_lshrrev_b32_e32 v1, 26, v1
	s_add_u32 s22, s12, 0x940000
	v_add_u32_e32 v1, v6, v1
	s_addc_u32 s23, s13, 0
	s_and_b32 s3, s2, 7
	v_ashrrev_i32_e32 v7, 6, v1
	v_bfe_i32 v1, v6, 27, 1
	s_mulk_i32 s3, 0xc6
	s_ashr_i32 s4, s2, 3
	v_lshlrev_b32_e32 v2, 4, v6
	v_lshrrev_b32_e32 v1, 22, v1
	s_add_i32 s3, s3, s4
	v_add_u32_e32 v1, v2, v1
	s_mul_hi_i32 s4, s3, 0xa57eb503
	v_and_b32_e32 v1, 0xfffffc00, v1
	s_add_i32 s4, s4, s3
	v_sub_u32_e32 v1, v2, v1
	s_lshr_b32 s5, s4, 31
	s_ashr_i32 s4, s4, 6
	v_lshrrev_b32_e32 v3, 4, v1
	s_add_i32 s4, s4, s5
	v_bitop3_b32 v8, v3, v1, 32 bitop3:0x6c
	v_ashrrev_i32_e32 v1, 31, v1
	s_mul_i32 s5, s4, 0xffffff9d
	v_lshrrev_b32_e32 v1, 26, v1
	s_add_i32 s5, s5, s3
	v_lshlrev_b32_e32 v3, 3, v7
	v_add_u32_e32 v1, v8, v1
	s_mul_hi_i32 s3, s5, 0x2e8ba2e9
	v_and_b32_e32 v3, -16, v3
	v_ashrrev_i32_e32 v9, 6, v1
	v_add_u32_e32 v2, 0x2000, v2
	s_lshr_b32 s6, s3, 31
	s_ashr_i32 s3, s3, 1
	v_add_u32_e32 v1, v9, v3
	v_ashrrev_i32_e32 v3, 31, v2
	s_add_i32 s3, s3, s6
	s_mul_i32 s6, s4, 9
	v_lshrrev_b32_e32 v3, 22, v3
	s_add_i32 s61, s3, s6
	s_sub_i32 s3, s4, s3
	v_add_u32_e32 v3, v2, v3
	s_mul_i32 s3, s3, 11
	v_ashrrev_i32_e32 v10, 10, v3
	s_add_i32 s40, s3, s5
	v_mul_i32_i24_e32 v3, 0x400, v10
	s_ashr_i32 s41, s40, 31
	v_sub_u32_e32 v2, v2, v3
	s_lshl_b64 s[4:5], s[40:41], 20
	v_lshrrev_b32_e32 v3, 4, v2
	s_add_u32 s42, s0, s4
	v_bitop3_b32 v11, v3, v2, 32 bitop3:0x6c
	s_addc_u32 s43, s1, s5
	v_ashrrev_i32_e32 v3, 31, v11
	s_ashr_i32 s36, s34, 6
	s_ashr_i32 s35, s34, 8
	v_lshrrev_b32_e32 v3, 26, v3
	s_lshl_b32 s3, s36, 10
	v_lshlrev_b32_e32 v2, 3, v10
	v_add_u32_e32 v12, v11, v3
	s_add_u32 s6, s42, 0x80000
	v_and_b32_e32 v2, -16, v2
	v_ashrrev_i32_e32 v13, 6, v12
	s_addc_u32 s7, s43, 0
	s_lshl_b32 s4, s61, 8
	v_add_u32_e32 v146, v13, v2
	s_or_b32 s5, s4, 0x80
	v_add_u32_e32 v2, s4, v1
	v_ashrrev_i32_e32 v3, 31, v2
	v_add_u32_e32 v4, s5, v1
	v_lshl_add_u64 v[2:3], v[2:3], 2, s[22:23]
	v_ashrrev_i32_e32 v5, 31, v4
	v_lshl_add_u64 v[4:5], v[4:5], 2, s[22:23]
	global_load_dword v14, v[2:3], off
	global_load_dword v15, v[4:5], off
	v_add_u32_e32 v2, s4, v146
	v_ashrrev_i32_e32 v3, 31, v2
	v_add_u32_e32 v4, s5, v146
	v_lshl_add_u64 v[2:3], v[2:3], 2, s[22:23]
	v_ashrrev_i32_e32 v5, 31, v4
	v_lshl_add_u64 v[4:5], v[4:5], 2, s[22:23]
	global_load_dword v16, v[2:3], off
	global_load_dword v17, v[4:5], off
	v_mul_i32_i24_e32 v3, 64, v9
	v_sub_u32_e32 v3, v8, v3
	v_mov_b32_e32 v4, 1
	v_lshlrev_b32_e32 v2, 5, v7
	v_ashrrev_i16_sdwa v3, v4, sext(v3) dst_sel:DWORD dst_unused:UNUSED_PAD src0_sel:DWORD src1_sel:BYTE_0
	v_and_b32_e32 v2, 32, v2
	v_bfe_i32 v3, v3, 0, 16
	v_add_lshl_u32 v147, v2, v3, 1
	v_and_b32_e32 v3, 0xc0, v12
	v_sub_u32_e32 v3, v11, v3
	v_lshlrev_b32_e32 v2, 5, v10
	v_ashrrev_i16_sdwa v3, v4, sext(v3) dst_sel:DWORD dst_unused:UNUSED_PAD src0_sel:DWORD src1_sel:BYTE_0
	v_and_b32_e32 v2, 32, v2
	v_bfe_i32 v3, v3, 0, 16
	v_add_lshl_u32 v148, v2, v3, 1
	v_and_b32_e32 v2, 3, v13
	s_mov_b32 s4, 0xfffe0
	v_lshrrev_b32_e32 v3, 2, v146
	v_lshlrev_b32_e32 v4, 1, v146
	v_and_or_b32 v2, v146, s4, v2
	v_and_b32_e32 v3, 4, v3
	v_and_b32_e32 v4, 24, v4
	v_or3_b32 v2, v2, v3, v4
	v_lshl_add_u32 v130, v2, 12, v148
	v_and_b32_e32 v2, 3, v9
	v_lshrrev_b32_e32 v3, 2, v1
	v_lshlrev_b32_e32 v4, 1, v1
	v_and_or_b32 v2, v1, s4, v2
	v_and_b32_e32 v3, 4, v3
	v_and_b32_e32 v4, 24, v4
	v_or3_b32 v2, v2, v3, v4
	s_add_i32 s4, s3, 0
	v_lshl_add_u32 v132, v2, 12, v147
	s_add_i32 m0, s4, 0x10000
	s_add_i32 s5, s4, 0x2000
	global_load_lds_dwordx4 v132, s[42:43]
	s_add_i32 m0, s4, 0x12000
	s_add_i32 s33, s4, 0x4000
	global_load_lds_dwordx4 v130, s[42:43]
	s_add_i32 m0, s4, 0x14000
	s_add_i32 s41, s4, 0x6000
	global_load_lds_dwordx4 v132, s[6:7]
	s_add_i32 m0, s4, 0x16000
	v_mov_b32_e32 v135, 0
	global_load_lds_dwordx4 v130, s[6:7]
	s_mov_b32 m0, s4
	v_mov_b32_e32 v133, v135
	v_mov_b32_e32 v131, v135
	s_cmp_eq_u32 s35, 1
	s_mov_b32 s48, 0
	v_lshl_add_u64 v[4:5], s[42:43], 0, v[132:133]
	s_cselect_b64 s[24:25], -1, 0
	s_cmp_lg_u32 s35, 1
	v_mov_b32_e32 v141, v135
	s_waitcnt vmcnt(0)
	v_max_i32_e32 v2, 0, v14
	v_lshl_add_u32 v134, v2, 12, v147
	v_max_i32_e32 v3, 0, v15
	global_load_lds_dwordx4 v134, s[20:21]
	s_mov_b32 m0, s5
	v_lshl_add_u32 v136, v3, 12, v147
	v_max_i32_e32 v2, 0, v16
	v_lshl_add_u32 v140, v2, 12, v148
	v_max_i32_e32 v3, 0, v17
	global_load_lds_dwordx4 v140, s[20:21]
	s_mov_b32 m0, s33
	v_lshl_add_u32 v138, v3, 12, v148
	global_load_lds_dwordx4 v136, s[20:21]
	s_mov_b32 m0, s41
	v_lshl_add_u64 v[2:3], s[42:43], 0, v[130:131]
	global_load_lds_dwordx4 v138, s[20:21]
	s_cbranch_scc1 .LBB0_1092
	s_barrier

.LBB0_1100:
	s_cmp_eq_u32 s99, 0
	s_cbranch_scc1 .Lbal_skip_1100
	s_mov_b32 m0, s49
	s_nop 0
	global_load_lds_dwordx4 v[240:241], off
	s_mov_b32 m0, s50
	s_nop 0
	global_load_lds_dwordx4 v[242:243], off
.Lbal_skip_1100:
	ds_read_b128 v[160:163], v151
	ds_read_b128 v[164:167], v151 offset:1024
	ds_read_b128 v[168:171], v151 offset:2048
	ds_read_b128 v[172:175], v151 offset:3072
	ds_read_b128 v[176:179], v152
	ds_read_b128 v[180:183], v152 offset:1024
	ds_read_b128 v[184:187], v152 offset:2048
	ds_read_b128 v[188:191], v152 offset:3072
	s_add_u32 s44, s12, s42
	s_addc_u32 s45, s13, s43
	s_add_u32 s46, s44, 0x25000100
	s_addc_u32 s47, s45, 0
	s_add_u32 s68, s65, s42
	s_addc_u32 s69, s66, s43
	s_cmpk_eq_i32 s42, 0xf00
	s_cselect_b64 vcc, -1, 0
	s_and_b64 s[44:45], vcc, exec
	v_cndmask_b32_e32 v134, v159, v155, vcc
	s_cselect_b32 s47, s21, s47
	s_cselect_b32 s46, s20, s46
	v_cndmask_b32_e32 v224, v140, v156, vcc
	v_cndmask_b32_e32 v137, v136, v158, vcc
	v_cndmask_b32_e32 v139, v138, v157, vcc
	s_cselect_b32 s45, s37, s69
	s_cselect_b32 s44, s64, s68
	s_mov_b32 m0, s52
	v_lshl_add_u64 v[226:227], v[144:145], 0, s[42:43]
	ds_read_b128 v[192:195], v153
	ds_read_b128 v[196:199], v153 offset:1024
	ds_read_b128 v[200:203], v153 offset:2048
	ds_read_b128 v[204:207], v153 offset:3072
	ds_read_b128 v[208:211], v153 offset:4096
	ds_read_b128 v[212:215], v153 offset:5120
	ds_read_b128 v[216:219], v153 offset:6144
	ds_read_b128 v[220:223], v153 offset:7168
	global_load_lds_dwordx4 v[226:227], off
	v_lshl_add_u64 v[226:227], v[142:143], 0, s[42:43]
	s_mov_b32 m0, s53
	s_nop 0
	global_load_lds_dwordx4 v[226:227], off
	s_waitcnt vmcnt(8)
	s_waitcnt lgkmcnt(0)
	s_barrier
	s_setprio 1
	s_waitcnt lgkmcnt(0)
	v_mfma_f32_16x16x32_bf16 v[126:129], v[160:163], v[192:195], v[126:129]
	v_mfma_f32_16x16x32_bf16 v[122:125], v[168:171], v[192:195], v[122:125]
	v_mfma_f32_16x16x32_bf16 v[110:113], v[160:163], v[200:203], v[110:113]
	v_mfma_f32_16x16x32_bf16 v[106:109], v[168:171], v[200:203], v[106:109]
	v_mfma_f32_16x16x32_bf16 v[94:97], v[160:163], v[208:211], v[94:97]
	v_mfma_f32_16x16x32_bf16 v[90:93], v[168:171], v[208:211], v[90:93]
	v_mfma_f32_16x16x32_bf16 v[78:81], v[160:163], v[216:219], v[78:81]
	v_mfma_f32_16x16x32_bf16 v[74:77], v[168:171], v[216:219], v[74:77]
	v_mfma_f32_16x16x32_bf16 v[126:129], v[164:167], v[196:199], v[126:129]
	v_mfma_f32_16x16x32_bf16 v[122:125], v[172:175], v[196:199], v[122:125]
	v_mfma_f32_16x16x32_bf16 v[110:113], v[164:167], v[204:207], v[110:113]
	v_mfma_f32_16x16x32_bf16 v[106:109], v[172:175], v[204:207], v[106:109]
	v_mfma_f32_16x16x32_bf16 v[94:97], v[164:167], v[212:215], v[94:97]
	v_mfma_f32_16x16x32_bf16 v[90:93], v[172:175], v[212:215], v[90:93]
	v_mfma_f32_16x16x32_bf16 v[78:81], v[164:167], v[220:223], v[78:81]
	v_mfma_f32_16x16x32_bf16 v[74:77], v[172:175], v[220:223], v[74:77]
	s_setprio 0
	s_setprio 1
	v_mfma_f32_16x16x32_bf16 v[118:121], v[176:179], v[192:195], v[118:121]
	v_mfma_f32_16x16x32_bf16 v[114:117], v[184:187], v[192:195], v[114:117]
	v_mfma_f32_16x16x32_bf16 v[102:105], v[176:179], v[200:203], v[102:105]
	v_mfma_f32_16x16x32_bf16 v[98:101], v[184:187], v[200:203], v[98:101]
	v_mfma_f32_16x16x32_bf16 v[86:89], v[176:179], v[208:211], v[86:89]
	v_mfma_f32_16x16x32_bf16 v[82:85], v[184:187], v[208:211], v[82:85]
	v_mfma_f32_16x16x32_bf16 v[70:73], v[176:179], v[216:219], v[70:73]
	v_mfma_f32_16x16x32_bf16 v[66:69], v[184:187], v[216:219], v[66:69]
	v_mfma_f32_16x16x32_bf16 v[118:121], v[180:183], v[196:199], v[118:121]
	v_mfma_f32_16x16x32_bf16 v[114:117], v[188:191], v[196:199], v[114:117]
	v_mfma_f32_16x16x32_bf16 v[102:105], v[180:183], v[204:207], v[102:105]
	v_mfma_f32_16x16x32_bf16 v[98:101], v[188:191], v[204:207], v[98:101]
	v_mfma_f32_16x16x32_bf16 v[86:89], v[180:183], v[212:215], v[86:89]
	v_mfma_f32_16x16x32_bf16 v[82:85], v[188:191], v[212:215], v[82:85]
	v_mfma_f32_16x16x32_bf16 v[70:73], v[180:183], v[220:223], v[70:73]
	v_mfma_f32_16x16x32_bf16 v[66:69], v[188:191], v[220:223], v[66:69]
	s_setprio 0
	s_barrier
	s_mov_b32 m0, s54
	v_lshl_add_u64 v[226:227], s[44:45], 0, v[132:133]
	s_add_u32 s68, s44, 0x80000
	ds_read_b128 v[192:195], v153 offset:16384
	ds_read_b128 v[196:199], v153 offset:17408
	ds_read_b128 v[200:203], v153 offset:18432
	ds_read_b128 v[204:207], v153 offset:19456
	ds_read_b128 v[208:211], v153 offset:20480
	ds_read_b128 v[212:215], v153 offset:21504
	ds_read_b128 v[216:219], v153 offset:22528
	ds_read_b128 v[220:223], v153 offset:23552
	global_load_lds_dwordx4 v[226:227], off
	v_lshl_add_u64 v[228:229], s[44:45], 0, v[130:131]
	s_mov_b32 m0, s55
	s_addc_u32 s69, s45, 0
	global_load_lds_dwordx4 v[228:229], off
	v_lshl_add_u64 v[230:231], s[68:69], 0, v[132:133]
	s_mov_b32 m0, s56
	v_mov_b32_e32 v225, v135
	global_load_lds_dwordx4 v[230:231], off
	v_lshl_add_u64 v[230:231], s[68:69], 0, v[130:131]
	s_mov_b32 m0, s57
	s_nop 0
	global_load_lds_dwordx4 v[230:231], off
	s_waitcnt vmcnt(6)
	s_waitcnt lgkmcnt(0)
	v_lshl_add_u64 v[224:225], s[46:47], 0, v[224:225]
	s_barrier
	s_setprio 1
	s_waitcnt lgkmcnt(0)
	v_mfma_f32_16x16x32_bf16 v[62:65], v[160:163], v[192:195], v[62:65]
	v_mfma_f32_16x16x32_bf16 v[58:61], v[168:171], v[192:195], v[58:61]
	v_mfma_f32_16x16x32_bf16 v[46:49], v[160:163], v[200:203], v[46:49]
	v_mfma_f32_16x16x32_bf16 v[42:45], v[168:171], v[200:203], v[42:45]
	v_mfma_f32_16x16x32_bf16 v[30:33], v[160:163], v[208:211], v[30:33]
	v_mfma_f32_16x16x32_bf16 v[26:29], v[168:171], v[208:211], v[26:29]
	v_mfma_f32_16x16x32_bf16 v[14:17], v[160:163], v[216:219], v[14:17]
	v_mfma_f32_16x16x32_bf16 v[10:13], v[168:171], v[216:219], v[10:13]
	v_mfma_f32_16x16x32_bf16 v[62:65], v[164:167], v[196:199], v[62:65]
	v_mfma_f32_16x16x32_bf16 v[58:61], v[172:175], v[196:199], v[58:61]
	v_mfma_f32_16x16x32_bf16 v[46:49], v[164:167], v[204:207], v[46:49]
	v_mfma_f32_16x16x32_bf16 v[42:45], v[172:175], v[204:207], v[42:45]
	v_mfma_f32_16x16x32_bf16 v[30:33], v[164:167], v[212:215], v[30:33]
	v_mfma_f32_16x16x32_bf16 v[26:29], v[172:175], v[212:215], v[26:29]
	v_mfma_f32_16x16x32_bf16 v[14:17], v[164:167], v[220:223], v[14:17]
	v_mfma_f32_16x16x32_bf16 v[10:13], v[172:175], v[220:223], v[10:13]
	s_setprio 0
	s_setprio 1
	v_mfma_f32_16x16x32_bf16 v[54:57], v[176:179], v[192:195], v[54:57]
	v_mfma_f32_16x16x32_bf16 v[50:53], v[184:187], v[192:195], v[50:53]
	v_mfma_f32_16x16x32_bf16 v[38:41], v[176:179], v[200:203], v[38:41]
	v_mfma_f32_16x16x32_bf16 v[34:37], v[184:187], v[200:203], v[34:37]
	v_mfma_f32_16x16x32_bf16 v[22:25], v[176:179], v[208:211], v[22:25]
	v_mfma_f32_16x16x32_bf16 v[18:21], v[184:187], v[208:211], v[18:21]
	v_mfma_f32_16x16x32_bf16 v[6:9], v[176:179], v[216:219], v[6:9]
	v_mfma_f32_16x16x32_bf16 v[2:5], v[184:187], v[216:219], v[2:5]
	v_mfma_f32_16x16x32_bf16 v[54:57], v[180:183], v[196:199], v[54:57]
	v_mfma_f32_16x16x32_bf16 v[50:53], v[188:191], v[196:199], v[50:53]
	v_mfma_f32_16x16x32_bf16 v[38:41], v[180:183], v[204:207], v[38:41]
	v_mfma_f32_16x16x32_bf16 v[34:37], v[188:191], v[204:207], v[34:37]
	v_mfma_f32_16x16x32_bf16 v[22:25], v[180:183], v[212:215], v[22:25]
	v_mfma_f32_16x16x32_bf16 v[18:21], v[188:191], v[212:215], v[18:21]
	v_mfma_f32_16x16x32_bf16 v[6:9], v[180:183], v[220:223], v[6:9]
	v_mfma_f32_16x16x32_bf16 v[2:5], v[188:191], v[220:223], v[2:5]
	s_setprio 0
	s_barrier
	s_mov_b32 m0, s4
	v_lshl_add_u64 v[230:231], s[46:47], 0, v[134:135]
	global_load_lds_dwordx4 v134, s[46:47]
	s_mov_b32 m0, s5
	s_nop 0
	global_load_lds_dwordx4 v[224:225], off
	s_add_i32 s68, 0, 0x1c000
	v_add_u32_e32 v134, s68, v149
	ds_read_b128 v[160:163], v154
	ds_read_b128 v[164:167], v154 offset:1024
	ds_read_b128 v[168:171], v154 offset:2048
	ds_read_b128 v[172:175], v154 offset:3072
	ds_read_b128 v[176:179], v134
	ds_read_b128 v[180:183], v134 offset:1024
	ds_read_b128 v[184:187], v134 offset:2048
	ds_read_b128 v[188:191], v134 offset:3072
	s_mov_b32 m0, s33
	ds_read_b128 v[192:195], v153 offset:32768
	ds_read_b128 v[196:199], v153 offset:33792
	ds_read_b128 v[200:203], v153 offset:34816
	ds_read_b128 v[204:207], v153 offset:35840
	ds_read_b128 v[208:211], v153 offset:36864
	ds_read_b128 v[212:215], v153 offset:37888
	ds_read_b128 v[216:219], v153 offset:38912
	ds_read_b128 v[220:223], v153 offset:39936
	global_load_lds_dwordx4 v137, s[46:47]
	s_mov_b32 m0, s41
	s_nop 0
	global_load_lds_dwordx4 v139, s[46:47]
	s_waitcnt vmcnt(8)
	s_waitcnt lgkmcnt(0)
	s_barrier
	s_setprio 1
	s_waitcnt lgkmcnt(0)
	v_mfma_f32_16x16x32_bf16 v[126:129], v[160:163], v[192:195], v[126:129]
	v_mfma_f32_16x16x32_bf16 v[122:125], v[168:171], v[192:195], v[122:125]
	v_mfma_f32_16x16x32_bf16 v[110:113], v[160:163], v[200:203], v[110:113]
	v_mfma_f32_16x16x32_bf16 v[106:109], v[168:171], v[200:203], v[106:109]
	v_mfma_f32_16x16x32_bf16 v[94:97], v[160:163], v[208:211], v[94:97]
	v_mfma_f32_16x16x32_bf16 v[90:93], v[168:171], v[208:211], v[90:93]
	v_mfma_f32_16x16x32_bf16 v[78:81], v[160:163], v[216:219], v[78:81]
	v_mfma_f32_16x16x32_bf16 v[74:77], v[168:171], v[216:219], v[74:77]
	v_mfma_f32_16x16x32_bf16 v[126:129], v[164:167], v[196:199], v[126:129]
	v_mfma_f32_16x16x32_bf16 v[122:125], v[172:175], v[196:199], v[122:125]
	v_mfma_f32_16x16x32_bf16 v[110:113], v[164:167], v[204:207], v[110:113]
	v_mfma_f32_16x16x32_bf16 v[106:109], v[172:175], v[204:207], v[106:109]
	v_mfma_f32_16x16x32_bf16 v[94:97], v[164:167], v[212:215], v[94:97]
	v_mfma_f32_16x16x32_bf16 v[90:93], v[172:175], v[212:215], v[90:93]
	v_mfma_f32_16x16x32_bf16 v[78:81], v[164:167], v[220:223], v[78:81]
	v_mfma_f32_16x16x32_bf16 v[74:77], v[172:175], v[220:223], v[74:77]
	s_setprio 0
	s_setprio 1
	v_mfma_f32_16x16x32_bf16 v[118:121], v[176:179], v[192:195], v[118:121]
	v_mfma_f32_16x16x32_bf16 v[114:117], v[184:187], v[192:195], v[114:117]
	v_mfma_f32_16x16x32_bf16 v[102:105], v[176:179], v[200:203], v[102:105]
	v_mfma_f32_16x16x32_bf16 v[98:101], v[184:187], v[200:203], v[98:101]
	v_mfma_f32_16x16x32_bf16 v[86:89], v[176:179], v[208:211], v[86:89]
	v_mfma_f32_16x16x32_bf16 v[82:85], v[184:187], v[208:211], v[82:85]
	v_mfma_f32_16x16x32_bf16 v[70:73], v[176:179], v[216:219], v[70:73]
	v_mfma_f32_16x16x32_bf16 v[66:69], v[184:187], v[216:219], v[66:69]
	v_mfma_f32_16x16x32_bf16 v[118:121], v[180:183], v[196:199], v[118:121]
	v_mfma_f32_16x16x32_bf16 v[114:117], v[188:191], v[196:199], v[114:117]
	v_mfma_f32_16x16x32_bf16 v[102:105], v[180:183], v[204:207], v[102:105]
	v_mfma_f32_16x16x32_bf16 v[98:101], v[188:191], v[204:207], v[98:101]
	v_mfma_f32_16x16x32_bf16 v[86:89], v[180:183], v[212:215], v[86:89]
	v_mfma_f32_16x16x32_bf16 v[82:85], v[188:191], v[212:215], v[82:85]
	v_mfma_f32_16x16x32_bf16 v[70:73], v[180:183], v[220:223], v[70:73]
	v_mfma_f32_16x16x32_bf16 v[66:69], v[188:191], v[220:223], v[66:69]
	s_setprio 0
	s_barrier
	s_add_i32 s46, s58, s3
	v_lshl_add_u64 v[226:227], v[226:227], 0, s[30:31]
	s_mov_b32 m0, s46
	ds_read_b128 v[192:195], v153 offset:49152
	ds_read_b128 v[196:199], v153 offset:50176
	ds_read_b128 v[200:203], v153 offset:51200
	ds_read_b128 v[204:207], v153 offset:52224
	ds_read_b128 v[208:211], v153 offset:53248
	ds_read_b128 v[212:215], v153 offset:54272
	ds_read_b128 v[216:219], v153 offset:55296
	ds_read_b128 v[220:223], v153 offset:56320
	global_load_lds_dwordx4 v[226:227], off
	s_add_i32 m0, s46, 0x2000
	s_add_u32 s44, s44, 0x80080
	v_lshl_add_u64 v[226:227], v[228:229], 0, s[30:31]
	s_addc_u32 s45, s45, 0
	s_add_i32 s46, s68, s3
	global_load_lds_dwordx4 v[226:227], off
	v_lshl_add_u64 v[226:227], s[44:45], 0, v[132:133]
	s_mov_b32 m0, s46
	v_lshl_add_u64 v[224:225], v[224:225], 0, s[30:31]
	global_load_lds_dwordx4 v[226:227], off
	v_lshl_add_u64 v[226:227], s[44:45], 0, v[130:131]
	s_add_i32 m0, s46, 0x2000
	s_nop 0
	global_load_lds_dwordx4 v[226:227], off
	v_lshl_add_u64 v[240:241], v[230:231], 0, s[30:31]
	v_mov_b32_e32 v242, v224
	v_mov_b32_e32 v243, v225
	s_waitcnt vmcnt(6)
	s_waitcnt lgkmcnt(0)
	s_barrier
	s_setprio 1
	s_waitcnt lgkmcnt(0)
	v_mfma_f32_16x16x32_bf16 v[62:65], v[160:163], v[192:195], v[62:65]
	v_mfma_f32_16x16x32_bf16 v[58:61], v[168:171], v[192:195], v[58:61]
	v_mfma_f32_16x16x32_bf16 v[46:49], v[160:163], v[200:203], v[46:49]
	v_mfma_f32_16x16x32_bf16 v[42:45], v[168:171], v[200:203], v[42:45]
	v_mfma_f32_16x16x32_bf16 v[30:33], v[160:163], v[208:211], v[30:33]
	v_mfma_f32_16x16x32_bf16 v[26:29], v[168:171], v[208:211], v[26:29]
	v_mfma_f32_16x16x32_bf16 v[14:17], v[160:163], v[216:219], v[14:17]
	v_mfma_f32_16x16x32_bf16 v[10:13], v[168:171], v[216:219], v[10:13]
	v_mfma_f32_16x16x32_bf16 v[62:65], v[164:167], v[196:199], v[62:65]
	v_mfma_f32_16x16x32_bf16 v[58:61], v[172:175], v[196:199], v[58:61]
	v_mfma_f32_16x16x32_bf16 v[46:49], v[164:167], v[204:207], v[46:49]
	v_mfma_f32_16x16x32_bf16 v[42:45], v[172:175], v[204:207], v[42:45]
	v_mfma_f32_16x16x32_bf16 v[30:33], v[164:167], v[212:215], v[30:33]
	v_mfma_f32_16x16x32_bf16 v[26:29], v[172:175], v[212:215], v[26:29]
	v_mfma_f32_16x16x32_bf16 v[14:17], v[164:167], v[220:223], v[14:17]
	v_mfma_f32_16x16x32_bf16 v[10:13], v[172:175], v[220:223], v[10:13]
	s_setprio 0
	s_setprio 1
	v_mfma_f32_16x16x32_bf16 v[54:57], v[176:179], v[192:195], v[54:57]
	v_mfma_f32_16x16x32_bf16 v[50:53], v[184:187], v[192:195], v[50:53]
	v_mfma_f32_16x16x32_bf16 v[38:41], v[176:179], v[200:203], v[38:41]
	v_mfma_f32_16x16x32_bf16 v[34:37], v[184:187], v[200:203], v[34:37]
	v_mfma_f32_16x16x32_bf16 v[22:25], v[176:179], v[208:211], v[22:25]
	v_mfma_f32_16x16x32_bf16 v[18:21], v[184:187], v[208:211], v[18:21]
	v_mfma_f32_16x16x32_bf16 v[6:9], v[176:179], v[216:219], v[6:9]
	v_mfma_f32_16x16x32_bf16 v[2:5], v[184:187], v[216:219], v[2:5]
	v_mfma_f32_16x16x32_bf16 v[54:57], v[180:183], v[196:199], v[54:57]
	v_mfma_f32_16x16x32_bf16 v[50:53], v[188:191], v[196:199], v[50:53]
	v_mfma_f32_16x16x32_bf16 v[38:41], v[180:183], v[204:207], v[38:41]
	v_mfma_f32_16x16x32_bf16 v[34:37], v[188:191], v[204:207], v[34:37]
	v_mfma_f32_16x16x32_bf16 v[22:25], v[180:183], v[212:215], v[22:25]
	v_mfma_f32_16x16x32_bf16 v[18:21], v[188:191], v[212:215], v[18:21]
	v_mfma_f32_16x16x32_bf16 v[6:9], v[180:183], v[220:223], v[6:9]
	v_mfma_f32_16x16x32_bf16 v[2:5], v[188:191], v[220:223], v[2:5]
	s_setprio 0
	s_barrier
	s_mov_b32 s99, 1
	s_add_i32 s67, s67, 2
	s_add_u32 s42, s42, 0x100
	s_addc_u32 s43, s43, 0
	s_cmp_gt_u32 s67, 29
	s_cbranch_scc0 .LBB0_1100
	s_and_b64 vcc, exec, s[34:35]
	s_cbranch_vccz .LBB0_1103
	s_barrier

.LBB0_1195:
	s_mov_b32 s99, 0
	v_readlane_b32 s0, v253, 11
	v_readlane_b32 s1, v253, 12
	s_mov_b32 s3, s1
	s_cmp_lt_i32 s0, 14
	s_cselect_b64 s[0:1], -1, 0
	s_cmp_gt_i32 s3, 13
	s_cselect_b64 s[4:5], -1, 0
	s_and_b64 s[0:1], s[0:1], s[4:5]
	s_andn2_b64 vcc, exec, s[0:1]
	s_cbranch_vccnz .LBB0_1246
	v_readlane_b32 s0, v253, 0
	v_readlane_b32 s1, v253, 1
	s_load_dwordx2 s[12:13], s[0:1], 0xd0
	s_load_dwordx2 s[14:15], s[0:1], 0x80
	s_load_dwordx2 s[16:17], s[0:1], 0xa0
	s_load_dwordx4 s[8:11], s[0:1], 0xb0
	s_load_dwordx2 s[18:19], s[0:1], 0xc0
	s_waitcnt lgkmcnt(0)
	s_add_u32 s0, s12, 0x1a000000
	s_addc_u32 s1, s13, 0
	v_mov_b32_e32 v10, v0
	s_cmpk_lt_i32 s2, 0x480
	s_nop 0
	v_readfirstlane_b32 s28, v10
	s_cbranch_scc0 .LBB0_1216
	v_lshlrev_b32_e32 v1, 4, v10
	v_add_u32_e32 v2, 0x2000, v1
	v_ashrrev_i32_e32 v3, 31, v2
	v_lshrrev_b32_e32 v3, 22, v3
	v_add_u32_e32 v3, v2, v3
	v_ashrrev_i32_e32 v11, 10, v3
	v_mul_i32_i24_e32 v3, 0x400, v11
	v_sub_u32_e32 v2, v2, v3
	v_lshrrev_b32_e32 v3, 4, v2
	v_bitop3_b32 v2, v3, v2, 32 bitop3:0x6c
	v_ashrrev_i32_e32 v3, 31, v2
	v_lshrrev_b32_e32 v3, 26, v3
	v_add_u32_e32 v3, v2, v3
	v_lshlrev_b32_e32 v4, 3, v11
	v_ashrrev_i32_e32 v12, 6, v3
	v_and_b32_e32 v4, -16, v4
	v_add_u32_e32 v4, v12, v4
	v_and_b32_e32 v5, 3, v12
	s_mov_b32 s22, 0x1ffffe0
	v_lshrrev_b32_e32 v6, 2, v4
	v_lshlrev_b32_e32 v7, 1, v4
	v_and_b32_e32 v3, 0xc0, v3
	v_and_or_b32 v5, v4, s22, v5
	v_and_b32_e32 v6, 4, v6
	v_and_b32_e32 v7, 24, v7
	v_sub_u32_e32 v2, v2, v3
	v_mov_b32_e32 v3, 1
	v_or3_b32 v5, v5, v6, v7
	v_lshlrev_b32_e32 v6, 5, v11
	v_ashrrev_i16_sdwa v2, v3, sext(v2) dst_sel:DWORD dst_unused:UNUSED_PAD src0_sel:DWORD src1_sel:BYTE_0
	s_add_u32 s3, s12, 0x3a300000
	s_movk_i32 s31, 0x580
	v_and_b32_e32 v13, 32, v6
	v_bfe_i32 v14, v2, 0, 16
	s_addc_u32 s4, s13, 0
	s_and_b32 s5, s2, 7
	v_mul_lo_u32 v5, v5, s31
	v_add_u32_e32 v2, v13, v14
	v_mul_lo_u32 v4, v4, s31
	s_mulk_i32 s5, 0x90
	s_ashr_i32 s6, s2, 3
	v_add_lshl_u32 v130, v5, v2, 1
	v_add_lshl_u32 v132, v2, v4, 1
	v_bfe_i32 v2, v10, 27, 1
	s_add_i32 s5, s5, s6
	v_lshrrev_b32_e32 v2, 22, v2
	s_mul_hi_i32 s6, s5, 0x38e38e39
	v_add_u32_e32 v2, v1, v2
	s_lshr_b32 s7, s6, 31
	s_ashr_i32 s6, s6, 4
	v_and_b32_e32 v2, 0xfffffc00, v2
	s_add_i32 s6, s6, s7
	v_sub_u32_e32 v1, v1, v2
	s_mul_i32 s7, s6, 0xffffffb8
	v_lshrrev_b32_e32 v2, 4, v1
	s_add_i32 s5, s7, s5
	v_bitop3_b32 v2, v2, v1, 32 bitop3:0x6c
	v_ashrrev_i32_e32 v1, 31, v1
	s_ashr_i32 s7, s5, 31
	v_lshrrev_b32_e32 v1, 26, v1
	s_lshr_b32 s7, s7, 29
	v_add_u32_e32 v1, v2, v1
	s_add_i32 s7, s5, s7
	v_ashrrev_i32_e32 v15, 6, v1
	v_ashrrev_i32_e32 v1, 31, v10
	s_ashr_i32 s7, s7, 3
	v_lshrrev_b32_e32 v1, 26, v1
	s_mul_i32 s20, s6, 9
	s_sub_i32 s6, s6, s7
	v_add_u32_e32 v1, v10, v1
	s_lshl_b32 s6, s6, 3
	v_ashrrev_i32_e32 v16, 6, v1
	s_add_i32 s70, s6, s5
	v_lshlrev_b32_e32 v1, 3, v16
	s_add_i32 s69, s7, s20
	s_mul_i32 s20, s70, 0xb0000
	v_and_b32_e32 v1, -16, v1
	s_mul_hi_i32 s7, s70, 0xb0000
	s_add_u32 s46, s0, s20
	v_add_u32_e32 v1, v15, v1
	s_mul_i32 s6, s69, 0xb0000
	s_addc_u32 s47, s1, s7
	v_and_b32_e32 v4, 3, v15
	v_lshrrev_b32_e32 v5, 2, v1
	v_lshlrev_b32_e32 v6, 1, v1
	s_mul_hi_i32 s5, s69, 0xb0000
	s_add_u32 s44, s3, s6
	v_and_or_b32 v4, v1, s22, v4
	v_and_b32_e32 v5, 4, v5
	v_and_b32_e32 v6, 24, v6
	s_addc_u32 s45, s4, s5
	s_ashr_i32 s29, s28, 6
	v_or3_b32 v4, v4, v5, v6
	v_lshlrev_b32_e32 v5, 5, v16
	s_ashr_i32 s30, s28, 8
	s_lshl_b32 s5, s29, 10
	v_and_b32_e32 v17, 32, v5
	v_mul_i32_i24_e32 v5, 64, v15
	s_add_u32 s6, s44, 0x58000
	v_sub_u32_e32 v2, v2, v5
	s_addc_u32 s7, s45, 0
	v_ashrrev_i16_sdwa v2, v3, sext(v2) dst_sel:DWORD dst_unused:UNUSED_PAD src0_sel:DWORD src1_sel:BYTE_0
	s_add_u32 s20, s46, 0x58000
	v_bfe_i32 v18, v2, 0, 16
	s_addc_u32 s21, s47, 0
	v_mul_lo_u32 v4, v4, s31
	v_add_u32_e32 v2, v17, v18
	s_add_i32 s33, s5, 0
	v_add_lshl_u32 v134, v4, v2, 1
	s_add_i32 m0, s33, 0x10000
	v_mul_lo_u32 v1, v1, s31
	global_load_lds_dwordx4 v134, s[46:47]
	s_add_i32 m0, s33, 0x12000
	v_add_lshl_u32 v136, v2, v1, 1
	global_load_lds_dwordx4 v130, s[46:47]
	s_add_i32 m0, s33, 0x14000
	s_add_i32 s52, s33, 0x2000
	global_load_lds_dwordx4 v134, s[20:21]
	s_add_i32 m0, s33, 0x16000
	s_add_i32 s53, s33, 0x4000
	global_load_lds_dwordx4 v130, s[20:21]
	s_mov_b32 m0, s33
	s_add_i32 s54, s33, 0x6000
	global_load_lds_dwordx4 v136, s[44:45]
	s_mov_b32 m0, s52
	v_mov_b32_e32 v135, 0
	global_load_lds_dwordx4 v132, s[44:45]
	s_mov_b32 m0, s53
	v_mov_b32_e32 v131, v135
	global_load_lds_dwordx4 v136, s[6:7]
	s_mov_b32 m0, s54
	v_mov_b32_e32 v137, v135
	global_load_lds_dwordx4 v132, s[6:7]
	v_mov_b32_e32 v133, v135
	s_cmp_eq_u32 s30, 1
	s_mov_b32 s55, 0xb0000
	s_mov_b32 s56, 0
	v_lshl_add_u64 v[8:9], s[46:47], 0, v[134:135]
	v_lshl_add_u64 v[6:7], s[46:47], 0, v[130:131]
	v_lshl_add_u64 v[2:3], s[44:45], 0, v[136:137]
	s_cselect_b64 s[20:21], -1, 0
	s_cmp_lg_u32 s30, 1
	v_lshl_add_u64 v[4:5], s[44:45], 0, v[132:133]
	s_cbranch_scc1 .LBB0_1199
	s_barrier

.LBB0_1209:
	s_cmp_eq_u32 s99, 0
	s_cbranch_scc1 .Lbal_skip_1209
	s_mov_b32 m0, s57
	s_nop 0
	global_load_lds_dwordx4 v[240:241], off
	s_mov_b32 m0, s58
	s_nop 0
	global_load_lds_dwordx4 v[242:243], off
.Lbal_skip_1209:
	ds_read_b128 v[142:145], v148
	ds_read_b128 v[152:155], v148 offset:1024
	ds_read_b128 v[156:159], v148 offset:2048
	ds_read_b128 v[160:163], v148 offset:3072
	ds_read_b128 v[164:167], v149
	ds_read_b128 v[168:171], v149 offset:1024
	ds_read_b128 v[172:175], v149 offset:2048
	ds_read_b128 v[176:179], v149 offset:3072
	s_add_u32 s46, s44, 0x100
	s_addc_u32 s47, s45, 0
	s_cmp_eq_u32 s73, 18
	s_cselect_b32 s51, s41, s47
	s_cselect_b32 s50, s40, s46
	s_cselect_b32 s49, s43, s72
	s_cselect_b32 s48, s42, s71
	v_lshl_add_u64 v[212:213], s[44:45], 0, v[138:139]
	s_add_i32 m0, s33, 0xc000
	ds_read_b128 v[180:183], v150
	ds_read_b128 v[184:187], v150 offset:1024
	ds_read_b128 v[188:191], v150 offset:2048
	ds_read_b128 v[192:195], v150 offset:3072
	ds_read_b128 v[196:199], v150 offset:4096
	ds_read_b128 v[200:203], v150 offset:5120
	ds_read_b128 v[204:207], v150 offset:6144
	ds_read_b128 v[208:211], v150 offset:7168
	global_load_lds_dwordx4 v[212:213], off
	v_lshl_add_u64 v[212:213], s[44:45], 0, v[140:141]
	s_add_i32 m0, s33, 0xe000
	s_nop 0
	global_load_lds_dwordx4 v[212:213], off
	s_waitcnt vmcnt(8)
	s_waitcnt lgkmcnt(0)
	s_barrier
	s_setprio 1
	s_waitcnt lgkmcnt(0)
	v_mfma_f32_16x16x32_bf16 v[126:129], v[142:145], v[180:183], v[126:129]
	v_mfma_f32_16x16x32_bf16 v[122:125], v[156:159], v[180:183], v[122:125]
	v_mfma_f32_16x16x32_bf16 v[110:113], v[142:145], v[188:191], v[110:113]
	v_mfma_f32_16x16x32_bf16 v[106:109], v[156:159], v[188:191], v[106:109]
	v_mfma_f32_16x16x32_bf16 v[94:97], v[142:145], v[196:199], v[94:97]
	v_mfma_f32_16x16x32_bf16 v[90:93], v[156:159], v[196:199], v[90:93]
	v_mfma_f32_16x16x32_bf16 v[86:89], v[142:145], v[204:207], v[86:89]
	v_mfma_f32_16x16x32_bf16 v[78:81], v[156:159], v[204:207], v[78:81]
	v_mfma_f32_16x16x32_bf16 v[126:129], v[152:155], v[184:187], v[126:129]
	v_mfma_f32_16x16x32_bf16 v[122:125], v[160:163], v[184:187], v[122:125]
	v_mfma_f32_16x16x32_bf16 v[110:113], v[152:155], v[192:195], v[110:113]
	v_mfma_f32_16x16x32_bf16 v[106:109], v[160:163], v[192:195], v[106:109]
	v_mfma_f32_16x16x32_bf16 v[94:97], v[152:155], v[200:203], v[94:97]
	v_mfma_f32_16x16x32_bf16 v[90:93], v[160:163], v[200:203], v[90:93]
	v_mfma_f32_16x16x32_bf16 v[86:89], v[152:155], v[208:211], v[86:89]
	v_mfma_f32_16x16x32_bf16 v[78:81], v[160:163], v[208:211], v[78:81]
	s_setprio 0
	s_setprio 1
	v_mfma_f32_16x16x32_bf16 v[118:121], v[164:167], v[180:183], v[118:121]
	v_mfma_f32_16x16x32_bf16 v[114:117], v[172:175], v[180:183], v[114:117]
	v_mfma_f32_16x16x32_bf16 v[102:105], v[164:167], v[188:191], v[102:105]
	v_mfma_f32_16x16x32_bf16 v[98:101], v[172:175], v[188:191], v[98:101]
	v_mfma_f32_16x16x32_bf16 v[82:85], v[164:167], v[196:199], v[82:85]
	v_mfma_f32_16x16x32_bf16 v[74:77], v[172:175], v[196:199], v[74:77]
	v_mfma_f32_16x16x32_bf16 v[70:73], v[164:167], v[204:207], v[70:73]
	v_mfma_f32_16x16x32_bf16 v[66:69], v[172:175], v[204:207], v[66:69]
	v_mfma_f32_16x16x32_bf16 v[118:121], v[168:171], v[184:187], v[118:121]
	v_mfma_f32_16x16x32_bf16 v[114:117], v[176:179], v[184:187], v[114:117]
	v_mfma_f32_16x16x32_bf16 v[102:105], v[168:171], v[192:195], v[102:105]
	v_mfma_f32_16x16x32_bf16 v[98:101], v[176:179], v[192:195], v[98:101]
	v_mfma_f32_16x16x32_bf16 v[82:85], v[168:171], v[200:203], v[82:85]
	v_mfma_f32_16x16x32_bf16 v[74:77], v[176:179], v[200:203], v[74:77]
	v_mfma_f32_16x16x32_bf16 v[70:73], v[168:171], v[208:211], v[70:73]
	v_mfma_f32_16x16x32_bf16 v[66:69], v[176:179], v[208:211], v[66:69]
	s_setprio 0
	s_barrier
	s_add_i32 s44, s59, s5
	v_lshl_add_u64 v[212:213], s[48:49], 0, v[134:135]
	s_mov_b32 m0, s44
	ds_read_b128 v[180:183], v150 offset:16384
	ds_read_b128 v[184:187], v150 offset:17408
	ds_read_b128 v[188:191], v150 offset:18432
	ds_read_b128 v[192:195], v150 offset:19456
	ds_read_b128 v[196:199], v150 offset:20480
	ds_read_b128 v[200:203], v150 offset:21504
	ds_read_b128 v[204:207], v150 offset:22528
	ds_read_b128 v[208:211], v150 offset:23552
	global_load_lds_dwordx4 v[212:213], off
	s_add_i32 m0, s44, 0x2000
	s_add_u32 s44, s48, 0x58000
	v_lshl_add_u64 v[214:215], s[48:49], 0, v[130:131]
	s_addc_u32 s45, s49, 0
	s_add_i32 s74, s61, s5
	global_load_lds_dwordx4 v[214:215], off
	v_lshl_add_u64 v[216:217], s[44:45], 0, v[134:135]
	s_mov_b32 m0, s74
	v_lshl_add_u64 v[218:219], s[50:51], 0, v[132:133]
	global_load_lds_dwordx4 v[216:217], off
	v_lshl_add_u64 v[216:217], s[44:45], 0, v[130:131]
	s_add_i32 m0, s74, 0x2000
	s_nop 0
	global_load_lds_dwordx4 v[216:217], off
	s_waitcnt vmcnt(6)
	s_waitcnt lgkmcnt(0)
	s_barrier
	s_setprio 1
	s_waitcnt lgkmcnt(0)
	v_mfma_f32_16x16x32_bf16 v[62:65], v[142:145], v[180:183], v[62:65]
	v_mfma_f32_16x16x32_bf16 v[58:61], v[156:159], v[180:183], v[58:61]
	v_mfma_f32_16x16x32_bf16 v[46:49], v[142:145], v[188:191], v[46:49]
	v_mfma_f32_16x16x32_bf16 v[42:45], v[156:159], v[188:191], v[42:45]
	v_mfma_f32_16x16x32_bf16 v[30:33], v[142:145], v[196:199], v[30:33]
	v_mfma_f32_16x16x32_bf16 v[26:29], v[156:159], v[196:199], v[26:29]
	v_mfma_f32_16x16x32_bf16 v[14:17], v[142:145], v[204:207], v[14:17]
	v_mfma_f32_16x16x32_bf16 v[10:13], v[156:159], v[204:207], v[10:13]
	v_mfma_f32_16x16x32_bf16 v[62:65], v[152:155], v[184:187], v[62:65]
	v_mfma_f32_16x16x32_bf16 v[58:61], v[160:163], v[184:187], v[58:61]
	v_mfma_f32_16x16x32_bf16 v[46:49], v[152:155], v[192:195], v[46:49]
	v_mfma_f32_16x16x32_bf16 v[42:45], v[160:163], v[192:195], v[42:45]
	v_mfma_f32_16x16x32_bf16 v[30:33], v[152:155], v[200:203], v[30:33]
	v_mfma_f32_16x16x32_bf16 v[26:29], v[160:163], v[200:203], v[26:29]
	v_mfma_f32_16x16x32_bf16 v[14:17], v[152:155], v[208:211], v[14:17]
	v_mfma_f32_16x16x32_bf16 v[10:13], v[160:163], v[208:211], v[10:13]
	s_setprio 0
	s_setprio 1
	v_mfma_f32_16x16x32_bf16 v[54:57], v[164:167], v[180:183], v[54:57]
	v_mfma_f32_16x16x32_bf16 v[50:53], v[172:175], v[180:183], v[50:53]
	v_mfma_f32_16x16x32_bf16 v[38:41], v[164:167], v[188:191], v[38:41]
	v_mfma_f32_16x16x32_bf16 v[34:37], v[172:175], v[188:191], v[34:37]
	v_mfma_f32_16x16x32_bf16 v[22:25], v[164:167], v[196:199], v[22:25]
	v_mfma_f32_16x16x32_bf16 v[18:21], v[172:175], v[196:199], v[18:21]
	v_mfma_f32_16x16x32_bf16 v[6:9], v[164:167], v[204:207], v[6:9]
	v_mfma_f32_16x16x32_bf16 v[2:5], v[172:175], v[204:207], v[2:5]
	v_mfma_f32_16x16x32_bf16 v[54:57], v[168:171], v[184:187], v[54:57]
	v_mfma_f32_16x16x32_bf16 v[50:53], v[176:179], v[184:187], v[50:53]
	v_mfma_f32_16x16x32_bf16 v[38:41], v[168:171], v[192:195], v[38:41]
	v_mfma_f32_16x16x32_bf16 v[34:37], v[176:179], v[192:195], v[34:37]
	v_mfma_f32_16x16x32_bf16 v[22:25], v[168:171], v[200:203], v[22:25]
	v_mfma_f32_16x16x32_bf16 v[18:21], v[176:179], v[200:203], v[18:21]
	v_mfma_f32_16x16x32_bf16 v[6:9], v[168:171], v[208:211], v[6:9]
	v_mfma_f32_16x16x32_bf16 v[2:5], v[176:179], v[208:211], v[2:5]
	s_setprio 0
	s_barrier
	v_lshl_add_u64 v[216:217], s[50:51], 0, v[136:137]
	s_mov_b32 m0, s33
	s_nop 0
	global_load_lds_dwordx4 v[216:217], off
	s_mov_b32 m0, s52
	s_nop 0
	global_load_lds_dwordx4 v[218:219], off
	s_add_i32 s74, 0, 0x18000
	v_add_u32_e32 v151, s74, v146
	s_add_i32 s75, 0, 0x1c000
	ds_read_b128 v[142:145], v151
	ds_read_b128 v[152:155], v151 offset:1024
	ds_read_b128 v[156:159], v151 offset:2048
	ds_read_b128 v[160:163], v151 offset:3072
	v_add_u32_e32 v151, s75, v146
	ds_read_b128 v[164:167], v151
	ds_read_b128 v[168:171], v151 offset:1024
	ds_read_b128 v[172:175], v151 offset:2048
	ds_read_b128 v[176:179], v151 offset:3072
	s_add_u32 s44, s50, 0x58000
	s_addc_u32 s45, s51, 0
	s_mov_b32 m0, s53
	v_lshl_add_u64 v[220:221], s[44:45], 0, v[136:137]
	ds_read_b128 v[180:183], v150 offset:32768
	ds_read_b128 v[184:187], v150 offset:33792
	ds_read_b128 v[188:191], v150 offset:34816
	ds_read_b128 v[192:195], v150 offset:35840
	ds_read_b128 v[196:199], v150 offset:36864
	ds_read_b128 v[200:203], v150 offset:37888
	ds_read_b128 v[204:207], v150 offset:38912
	ds_read_b128 v[208:211], v150 offset:39936
	global_load_lds_dwordx4 v[220:221], off
	v_lshl_add_u64 v[220:221], s[44:45], 0, v[132:133]
	s_mov_b32 m0, s54
	s_nop 0
	global_load_lds_dwordx4 v[220:221], off
	s_waitcnt vmcnt(8)
	s_waitcnt lgkmcnt(0)
	s_barrier
	s_setprio 1
	s_waitcnt lgkmcnt(0)
	v_mfma_f32_16x16x32_bf16 v[126:129], v[142:145], v[180:183], v[126:129]
	v_mfma_f32_16x16x32_bf16 v[122:125], v[156:159], v[180:183], v[122:125]
	v_mfma_f32_16x16x32_bf16 v[110:113], v[142:145], v[188:191], v[110:113]
	v_mfma_f32_16x16x32_bf16 v[106:109], v[156:159], v[188:191], v[106:109]
	v_mfma_f32_16x16x32_bf16 v[94:97], v[142:145], v[196:199], v[94:97]
	v_mfma_f32_16x16x32_bf16 v[90:93], v[156:159], v[196:199], v[90:93]
	v_mfma_f32_16x16x32_bf16 v[86:89], v[142:145], v[204:207], v[86:89]
	v_mfma_f32_16x16x32_bf16 v[78:81], v[156:159], v[204:207], v[78:81]
	v_mfma_f32_16x16x32_bf16 v[126:129], v[152:155], v[184:187], v[126:129]
	v_mfma_f32_16x16x32_bf16 v[122:125], v[160:163], v[184:187], v[122:125]
	v_mfma_f32_16x16x32_bf16 v[110:113], v[152:155], v[192:195], v[110:113]
	v_mfma_f32_16x16x32_bf16 v[106:109], v[160:163], v[192:195], v[106:109]
	v_mfma_f32_16x16x32_bf16 v[94:97], v[152:155], v[200:203], v[94:97]
	v_mfma_f32_16x16x32_bf16 v[90:93], v[160:163], v[200:203], v[90:93]
	v_mfma_f32_16x16x32_bf16 v[86:89], v[152:155], v[208:211], v[86:89]
	v_mfma_f32_16x16x32_bf16 v[78:81], v[160:163], v[208:211], v[78:81]
	s_setprio 0
	s_setprio 1
	v_mfma_f32_16x16x32_bf16 v[118:121], v[164:167], v[180:183], v[118:121]
	v_mfma_f32_16x16x32_bf16 v[114:117], v[172:175], v[180:183], v[114:117]
	v_mfma_f32_16x16x32_bf16 v[102:105], v[164:167], v[188:191], v[102:105]
	v_mfma_f32_16x16x32_bf16 v[98:101], v[172:175], v[188:191], v[98:101]
	v_mfma_f32_16x16x32_bf16 v[82:85], v[164:167], v[196:199], v[82:85]
	v_mfma_f32_16x16x32_bf16 v[74:77], v[172:175], v[196:199], v[74:77]
	v_mfma_f32_16x16x32_bf16 v[70:73], v[164:167], v[204:207], v[70:73]
	v_mfma_f32_16x16x32_bf16 v[66:69], v[172:175], v[204:207], v[66:69]
	v_mfma_f32_16x16x32_bf16 v[118:121], v[168:171], v[184:187], v[118:121]
	v_mfma_f32_16x16x32_bf16 v[114:117], v[176:179], v[184:187], v[114:117]
	v_mfma_f32_16x16x32_bf16 v[102:105], v[168:171], v[192:195], v[102:105]
	v_mfma_f32_16x16x32_bf16 v[98:101], v[176:179], v[192:195], v[98:101]
	v_mfma_f32_16x16x32_bf16 v[82:85], v[168:171], v[200:203], v[82:85]
	v_mfma_f32_16x16x32_bf16 v[74:77], v[176:179], v[200:203], v[74:77]
	v_mfma_f32_16x16x32_bf16 v[70:73], v[168:171], v[208:211], v[70:73]
	v_mfma_f32_16x16x32_bf16 v[66:69], v[176:179], v[208:211], v[66:69]
	s_setprio 0
	s_barrier
	s_add_i32 s44, s74, s5
	v_lshl_add_u64 v[212:213], v[212:213], 0, s[26:27]
	s_mov_b32 m0, s44
	ds_read_b128 v[180:183], v150 offset:49152
	ds_read_b128 v[184:187], v150 offset:50176
	ds_read_b128 v[188:191], v150 offset:51200
	ds_read_b128 v[192:195], v150 offset:52224
	ds_read_b128 v[196:199], v150 offset:53248
	ds_read_b128 v[200:203], v150 offset:54272
	ds_read_b128 v[204:207], v150 offset:55296
	ds_read_b128 v[208:211], v150 offset:56320
	global_load_lds_dwordx4 v[212:213], off
	s_add_i32 m0, s44, 0x2000
	s_add_u32 s44, s48, 0x58080
	v_lshl_add_u64 v[212:213], v[214:215], 0, s[26:27]
	s_addc_u32 s45, s49, 0
	s_add_i32 s48, s75, s5
	global_load_lds_dwordx4 v[212:213], off
	v_lshl_add_u64 v[212:213], s[44:45], 0, v[134:135]
	s_mov_b32 m0, s48
	s_nop 0
	global_load_lds_dwordx4 v[212:213], off
	v_lshl_add_u64 v[212:213], s[44:45], 0, v[130:131]
	s_add_i32 m0, s48, 0x2000
	s_nop 0
	global_load_lds_dwordx4 v[212:213], off
	v_lshl_add_u64 v[240:241], v[216:217], 0, s[26:27]
	v_lshl_add_u64 v[242:243], v[218:219], 0, s[26:27]
	s_waitcnt vmcnt(6)
	s_waitcnt lgkmcnt(0)
	s_barrier
	s_setprio 1
	s_waitcnt lgkmcnt(0)
	v_mfma_f32_16x16x32_bf16 v[62:65], v[142:145], v[180:183], v[62:65]
	v_mfma_f32_16x16x32_bf16 v[58:61], v[156:159], v[180:183], v[58:61]
	v_mfma_f32_16x16x32_bf16 v[46:49], v[142:145], v[188:191], v[46:49]
	v_mfma_f32_16x16x32_bf16 v[42:45], v[156:159], v[188:191], v[42:45]
	v_mfma_f32_16x16x32_bf16 v[30:33], v[142:145], v[196:199], v[30:33]
	v_mfma_f32_16x16x32_bf16 v[26:29], v[156:159], v[196:199], v[26:29]
	v_mfma_f32_16x16x32_bf16 v[14:17], v[142:145], v[204:207], v[14:17]
	v_mfma_f32_16x16x32_bf16 v[10:13], v[156:159], v[204:207], v[10:13]
	v_mfma_f32_16x16x32_bf16 v[62:65], v[152:155], v[184:187], v[62:65]
	v_mfma_f32_16x16x32_bf16 v[58:61], v[160:163], v[184:187], v[58:61]
	v_mfma_f32_16x16x32_bf16 v[46:49], v[152:155], v[192:195], v[46:49]
	v_mfma_f32_16x16x32_bf16 v[42:45], v[160:163], v[192:195], v[42:45]
	v_mfma_f32_16x16x32_bf16 v[30:33], v[152:155], v[200:203], v[30:33]
	v_mfma_f32_16x16x32_bf16 v[26:29], v[160:163], v[200:203], v[26:29]
	v_mfma_f32_16x16x32_bf16 v[14:17], v[152:155], v[208:211], v[14:17]
	v_mfma_f32_16x16x32_bf16 v[10:13], v[160:163], v[208:211], v[10:13]
	s_setprio 0
	s_setprio 1
	v_mfma_f32_16x16x32_bf16 v[54:57], v[164:167], v[180:183], v[54:57]
	v_mfma_f32_16x16x32_bf16 v[50:53], v[172:175], v[180:183], v[50:53]
	v_mfma_f32_16x16x32_bf16 v[38:41], v[164:167], v[188:191], v[38:41]
	v_mfma_f32_16x16x32_bf16 v[34:37], v[172:175], v[188:191], v[34:37]
	v_mfma_f32_16x16x32_bf16 v[22:25], v[164:167], v[196:199], v[22:25]
	v_mfma_f32_16x16x32_bf16 v[18:21], v[172:175], v[196:199], v[18:21]
	v_mfma_f32_16x16x32_bf16 v[6:9], v[164:167], v[204:207], v[6:9]
	v_mfma_f32_16x16x32_bf16 v[2:5], v[172:175], v[204:207], v[2:5]
	v_mfma_f32_16x16x32_bf16 v[54:57], v[168:171], v[184:187], v[54:57]
	v_mfma_f32_16x16x32_bf16 v[50:53], v[176:179], v[184:187], v[50:53]
	v_mfma_f32_16x16x32_bf16 v[38:41], v[168:171], v[192:195], v[38:41]
	v_mfma_f32_16x16x32_bf16 v[34:37], v[176:179], v[192:195], v[34:37]
	v_mfma_f32_16x16x32_bf16 v[22:25], v[168:171], v[200:203], v[22:25]
	v_mfma_f32_16x16x32_bf16 v[18:21], v[176:179], v[200:203], v[18:21]
	v_mfma_f32_16x16x32_bf16 v[6:9], v[168:171], v[208:211], v[6:9]
	v_mfma_f32_16x16x32_bf16 v[2:5], v[176:179], v[208:211], v[2:5]
	s_setprio 0
	s_barrier
	s_mov_b32 s99, 1
	s_add_i32 s73, s73, 2
	s_add_u32 s71, s71, 0x100
	s_addc_u32 s72, s72, 0
	s_cmp_gt_u32 s73, 19
	s_mov_b64 s[44:45], s[46:47]
	s_cbranch_scc0 .LBB0_1209
	s_and_b64 vcc, exec, s[28:29]
	s_cbranch_vccz .LBB0_1212
	s_barrier

.LBB0_1400:
	s_mov_b32 s99, 0
	v_readlane_b32 s0, v253, 11
	v_readlane_b32 s1, v253, 12
	s_mov_b32 s3, s1
	s_cmp_lt_i32 s0, 16
	s_cselect_b64 s[0:1], -1, 0
	s_cmp_gt_i32 s3, 15
	s_cselect_b64 s[4:5], -1, 0
	s_and_b64 s[0:1], s[0:1], s[4:5]
	s_andn2_b64 vcc, exec, s[0:1]
	s_cbranch_vccnz .LBB0_1483
	v_readlane_b32 s8, v253, 0
	v_readlane_b32 s9, v253, 1
	s_load_dwordx4 s[12:15], s[8:9], 0x80
	s_load_dwordx2 s[24:25], s[8:9], 0x90
	s_load_dwordx4 s[16:19], s[8:9], 0xb0
	s_load_dwordx2 s[10:11], s[8:9], 0xc0
	s_load_dwordx2 s[20:21], s[8:9], 0xd0
	s_cmpk_lt_i32 s2, 0x618
	s_cselect_b64 s[6:7], -1, 0
	v_mov_b32_e32 v10, v0
	s_and_b64 vcc, exec, s[6:7]
	v_readfirstlane_b32 s38, v10
	s_cbranch_vccz .LBB0_1403
	s_ashr_i32 s0, s2, 31
	s_lshr_b32 s0, s0, 29
	s_add_i32 s0, s2, s0
	s_ashr_i32 s1, s0, 3
	s_and_b32 s0, s0, -8
	s_sub_i32 s0, s2, s0
	s_cmp_lt_i32 s0, 0
	s_movk_i32 s3, 0xc4
	s_cselect_b32 s3, s3, 0xc3
	s_mul_i32 s0, s0, s3
	s_add_i32 s0, s0, s1
	s_mul_hi_i32 s1, s0, 0x2aaaaaab
	s_lshr_b32 s3, s1, 31
	s_ashr_i32 s1, s1, 5
	s_add_i32 s1, s1, s3
	s_lshl_b32 s3, s1, 3
	s_sub_i32 s4, 0x41, s3
	s_mulk_i32 s1, 0xc0
	s_min_u32 s4, s4, 8
	s_sub_i32 s5, s0, s1
	s_sext_i32_i16 s0, s5
	v_cvt_f32_ubyte0_e32 v2, s4
	v_cvt_f32_i32_e32 v1, s0
	v_rcp_iflag_f32_e32 v3, v2
	s_ashr_i32 s0, s0, 30
	s_or_b32 s22, s0, 1
	v_mul_f32_e32 v3, v1, v3
	v_trunc_f32_e32 v3, v3
	v_fma_f32 v1, -v3, v2, v1
	v_cvt_i32_f32_e32 v3, v3
	v_cmp_ge_f32_e64 s[0:1], |v1|, v2
	s_and_b64 s[0:1], s[0:1], exec
	s_cselect_b32 s0, s22, 0
	v_readfirstlane_b32 s1, v3
	s_add_i32 s0, s1, s0
	s_sext_i32_i16 s30, s0
	s_mul_i32 s0, s0, s4
	s_sub_i32 s0, s5, s0
	s_sext_i32_i16 s0, s0
	s_add_i32 s34, s3, s0

.LBB0_1412:
	s_cmp_eq_u32 s99, 0
	s_cbranch_scc1 .Lbal_skip_1412
	s_mov_b32 m0, s58
	s_nop 0
	global_load_lds_dwordx4 v[240:241], off
	s_mov_b32 m0, s59
	s_nop 0
	global_load_lds_dwordx4 v[242:243], off
.Lbal_skip_1412:
	ds_read_b128 v[130:133], v157
	ds_read_b128 v[134:137], v157 offset:1024
	ds_read_b128 v[164:167], v157 offset:2048
	ds_read_b128 v[168:171], v157 offset:3072
	ds_read_b128 v[172:175], v158
	ds_read_b128 v[176:179], v158 offset:1024
	ds_read_b128 v[180:183], v158 offset:2048
	ds_read_b128 v[184:187], v158 offset:3072
	s_add_u32 s50, s48, 0xfff80080
	s_addc_u32 s51, s49, -1
	s_cmp_eq_u32 s74, 28
	s_cselect_b32 s53, s43, s51
	s_cselect_b32 s52, s70, s50
	s_cselect_b32 s51, s41, s73
	s_cselect_b32 s50, s71, s72
	v_lshl_add_u64 v[220:221], s[48:49], 0, v[146:147]
	s_add_i32 m0, s31, 0xc000
	ds_read_b128 v[188:191], v159
	ds_read_b128 v[192:195], v159 offset:1024
	ds_read_b128 v[196:199], v159 offset:2048
	ds_read_b128 v[200:203], v159 offset:3072
	ds_read_b128 v[204:207], v159 offset:4096
	ds_read_b128 v[208:211], v159 offset:5120
	ds_read_b128 v[212:215], v159 offset:6144
	ds_read_b128 v[216:219], v159 offset:7168
	global_load_lds_dwordx4 v[220:221], off
	v_lshl_add_u64 v[220:221], s[48:49], 0, v[148:149]
	s_add_i32 m0, s31, 0xe000
	s_nop 0
	global_load_lds_dwordx4 v[220:221], off
	s_waitcnt vmcnt(8)
	s_waitcnt lgkmcnt(0)
	s_barrier
	s_setprio 1
	s_waitcnt lgkmcnt(0)
	v_mfma_f32_16x16x32_bf16 v[126:129], v[130:133], v[188:191], v[126:129]
	v_mfma_f32_16x16x32_bf16 v[122:125], v[164:167], v[188:191], v[122:125]
	v_mfma_f32_16x16x32_bf16 v[118:121], v[130:133], v[196:199], v[118:121]
	v_mfma_f32_16x16x32_bf16 v[114:117], v[164:167], v[196:199], v[114:117]
	v_mfma_f32_16x16x32_bf16 v[102:105], v[130:133], v[204:207], v[102:105]
	v_mfma_f32_16x16x32_bf16 v[98:101], v[164:167], v[204:207], v[98:101]
	v_mfma_f32_16x16x32_bf16 v[86:89], v[130:133], v[212:215], v[86:89]
	v_mfma_f32_16x16x32_bf16 v[82:85], v[164:167], v[212:215], v[82:85]
	v_mfma_f32_16x16x32_bf16 v[126:129], v[134:137], v[192:195], v[126:129]
	v_mfma_f32_16x16x32_bf16 v[122:125], v[168:171], v[192:195], v[122:125]
	v_mfma_f32_16x16x32_bf16 v[118:121], v[134:137], v[200:203], v[118:121]
	v_mfma_f32_16x16x32_bf16 v[114:117], v[168:171], v[200:203], v[114:117]
	v_mfma_f32_16x16x32_bf16 v[102:105], v[134:137], v[208:211], v[102:105]
	v_mfma_f32_16x16x32_bf16 v[98:101], v[168:171], v[208:211], v[98:101]
	v_mfma_f32_16x16x32_bf16 v[86:89], v[134:137], v[216:219], v[86:89]
	v_mfma_f32_16x16x32_bf16 v[82:85], v[168:171], v[216:219], v[82:85]
	s_setprio 0
	s_setprio 1
	v_mfma_f32_16x16x32_bf16 v[110:113], v[172:175], v[188:191], v[110:113]
	v_mfma_f32_16x16x32_bf16 v[106:109], v[180:183], v[188:191], v[106:109]
	v_mfma_f32_16x16x32_bf16 v[94:97], v[172:175], v[196:199], v[94:97]
	v_mfma_f32_16x16x32_bf16 v[90:93], v[180:183], v[196:199], v[90:93]
	v_mfma_f32_16x16x32_bf16 v[78:81], v[172:175], v[204:207], v[78:81]
	v_mfma_f32_16x16x32_bf16 v[74:77], v[180:183], v[204:207], v[74:77]
	v_mfma_f32_16x16x32_bf16 v[70:73], v[172:175], v[212:215], v[70:73]
	v_mfma_f32_16x16x32_bf16 v[66:69], v[180:183], v[212:215], v[66:69]
	v_mfma_f32_16x16x32_bf16 v[110:113], v[176:179], v[192:195], v[110:113]
	v_mfma_f32_16x16x32_bf16 v[106:109], v[184:187], v[192:195], v[106:109]
	v_mfma_f32_16x16x32_bf16 v[94:97], v[176:179], v[200:203], v[94:97]
	v_mfma_f32_16x16x32_bf16 v[90:93], v[184:187], v[200:203], v[90:93]
	v_mfma_f32_16x16x32_bf16 v[78:81], v[176:179], v[208:211], v[78:81]
	v_mfma_f32_16x16x32_bf16 v[74:77], v[184:187], v[208:211], v[74:77]
	v_mfma_f32_16x16x32_bf16 v[70:73], v[176:179], v[216:219], v[70:73]
	v_mfma_f32_16x16x32_bf16 v[66:69], v[184:187], v[216:219], v[66:69]
	s_setprio 0
	s_barrier
	s_add_i32 s75, s66, s5
	v_lshl_add_u64 v[220:221], s[50:51], 0, v[140:141]
	s_mov_b32 m0, s75
	ds_read_b128 v[188:191], v159 offset:16384
	ds_read_b128 v[192:195], v159 offset:17408
	ds_read_b128 v[196:199], v159 offset:18432
	ds_read_b128 v[200:203], v159 offset:19456
	ds_read_b128 v[204:207], v159 offset:20480
	ds_read_b128 v[208:211], v159 offset:21504
	ds_read_b128 v[212:215], v159 offset:22528
	ds_read_b128 v[216:219], v159 offset:23552
	global_load_lds_dwordx4 v[220:221], off
	s_add_i32 m0, s75, 0x2000
	s_add_u32 s76, s50, 0x80000
	v_lshl_add_u64 v[222:223], s[50:51], 0, v[144:145]
	s_addc_u32 s77, s51, 0
	s_add_i32 s75, s67, s5
	global_load_lds_dwordx4 v[222:223], off
	v_lshl_add_u64 v[224:225], s[76:77], 0, v[140:141]
	s_mov_b32 m0, s75
	v_lshl_add_u64 v[226:227], s[52:53], 0, v[142:143]
	global_load_lds_dwordx4 v[224:225], off
	v_lshl_add_u64 v[224:225], s[76:77], 0, v[144:145]
	s_add_i32 m0, s75, 0x2000
	s_nop 0
	global_load_lds_dwordx4 v[224:225], off
	s_waitcnt vmcnt(6)
	s_waitcnt lgkmcnt(0)
	s_barrier
	s_setprio 1
	s_waitcnt lgkmcnt(0)
	v_mfma_f32_16x16x32_bf16 v[62:65], v[130:133], v[188:191], v[62:65]
	v_mfma_f32_16x16x32_bf16 v[58:61], v[164:167], v[188:191], v[58:61]
	v_mfma_f32_16x16x32_bf16 v[54:57], v[130:133], v[196:199], v[54:57]
	v_mfma_f32_16x16x32_bf16 v[50:53], v[164:167], v[196:199], v[50:53]
	v_mfma_f32_16x16x32_bf16 v[38:41], v[130:133], v[204:207], v[38:41]
	v_mfma_f32_16x16x32_bf16 v[34:37], v[164:167], v[204:207], v[34:37]
	v_mfma_f32_16x16x32_bf16 v[22:25], v[130:133], v[212:215], v[22:25]
	v_mfma_f32_16x16x32_bf16 v[18:21], v[164:167], v[212:215], v[18:21]
	v_mfma_f32_16x16x32_bf16 v[62:65], v[134:137], v[192:195], v[62:65]
	v_mfma_f32_16x16x32_bf16 v[58:61], v[168:171], v[192:195], v[58:61]
	v_mfma_f32_16x16x32_bf16 v[54:57], v[134:137], v[200:203], v[54:57]
	v_mfma_f32_16x16x32_bf16 v[50:53], v[168:171], v[200:203], v[50:53]
	v_mfma_f32_16x16x32_bf16 v[38:41], v[134:137], v[208:211], v[38:41]
	v_mfma_f32_16x16x32_bf16 v[34:37], v[168:171], v[208:211], v[34:37]
	v_mfma_f32_16x16x32_bf16 v[22:25], v[134:137], v[216:219], v[22:25]
	v_mfma_f32_16x16x32_bf16 v[18:21], v[168:171], v[216:219], v[18:21]
	s_setprio 0
	s_setprio 1
	v_mfma_f32_16x16x32_bf16 v[46:49], v[172:175], v[188:191], v[46:49]
	v_mfma_f32_16x16x32_bf16 v[42:45], v[180:183], v[188:191], v[42:45]
	v_mfma_f32_16x16x32_bf16 v[30:33], v[172:175], v[196:199], v[30:33]
	v_mfma_f32_16x16x32_bf16 v[26:29], v[180:183], v[196:199], v[26:29]
	v_mfma_f32_16x16x32_bf16 v[14:17], v[172:175], v[204:207], v[14:17]
	v_mfma_f32_16x16x32_bf16 v[10:13], v[180:183], v[204:207], v[10:13]
	v_mfma_f32_16x16x32_bf16 v[6:9], v[172:175], v[212:215], v[6:9]
	v_mfma_f32_16x16x32_bf16 v[2:5], v[180:183], v[212:215], v[2:5]
	v_mfma_f32_16x16x32_bf16 v[46:49], v[176:179], v[192:195], v[46:49]
	v_mfma_f32_16x16x32_bf16 v[42:45], v[184:187], v[192:195], v[42:45]
	v_mfma_f32_16x16x32_bf16 v[30:33], v[176:179], v[200:203], v[30:33]
	v_mfma_f32_16x16x32_bf16 v[26:29], v[184:187], v[200:203], v[26:29]
	v_mfma_f32_16x16x32_bf16 v[14:17], v[176:179], v[208:211], v[14:17]
	v_mfma_f32_16x16x32_bf16 v[10:13], v[184:187], v[208:211], v[10:13]
	v_mfma_f32_16x16x32_bf16 v[6:9], v[176:179], v[216:219], v[6:9]
	v_mfma_f32_16x16x32_bf16 v[2:5], v[184:187], v[216:219], v[2:5]
	s_setprio 0
	s_barrier
	v_lshl_add_u64 v[224:225], s[52:53], 0, v[138:139]
	s_mov_b32 m0, s31
	s_nop 0
	global_load_lds_dwordx4 v[224:225], off
	s_mov_b32 m0, s33
	s_nop 0
	global_load_lds_dwordx4 v[226:227], off
	s_add_i32 s75, 0, 0x18000
	v_add_u32_e32 v163, s75, v154
	s_add_i32 s76, 0, 0x1c000
	ds_read_b128 v[130:133], v163
	ds_read_b128 v[134:137], v163 offset:1024
	ds_read_b128 v[164:167], v163 offset:2048
	ds_read_b128 v[168:171], v163 offset:3072
	v_add_u32_e32 v163, s76, v154
	ds_read_b128 v[172:175], v163
	ds_read_b128 v[176:179], v163 offset:1024
	ds_read_b128 v[180:183], v163 offset:2048
	ds_read_b128 v[184:187], v163 offset:3072
	s_add_u32 s52, s52, 0x80000
	s_addc_u32 s53, s53, 0
	s_mov_b32 m0, s35
	v_lshl_add_u64 v[228:229], s[52:53], 0, v[138:139]
	ds_read_b128 v[188:191], v159 offset:32768
	ds_read_b128 v[192:195], v159 offset:33792
	ds_read_b128 v[196:199], v159 offset:34816
	ds_read_b128 v[200:203], v159 offset:35840
	ds_read_b128 v[204:207], v159 offset:36864
	ds_read_b128 v[208:211], v159 offset:37888
	ds_read_b128 v[212:215], v159 offset:38912
	ds_read_b128 v[216:219], v159 offset:39936
	global_load_lds_dwordx4 v[228:229], off
	v_lshl_add_u64 v[228:229], s[52:53], 0, v[142:143]
	s_mov_b32 m0, s54
	s_nop 0
	global_load_lds_dwordx4 v[228:229], off
	s_waitcnt vmcnt(8)
	s_waitcnt lgkmcnt(0)
	s_barrier
	s_setprio 1
	s_waitcnt lgkmcnt(0)
	v_mfma_f32_16x16x32_bf16 v[126:129], v[130:133], v[188:191], v[126:129]
	v_mfma_f32_16x16x32_bf16 v[122:125], v[164:167], v[188:191], v[122:125]
	v_mfma_f32_16x16x32_bf16 v[118:121], v[130:133], v[196:199], v[118:121]
	v_mfma_f32_16x16x32_bf16 v[114:117], v[164:167], v[196:199], v[114:117]
	v_mfma_f32_16x16x32_bf16 v[102:105], v[130:133], v[204:207], v[102:105]
	v_mfma_f32_16x16x32_bf16 v[98:101], v[164:167], v[204:207], v[98:101]
	v_mfma_f32_16x16x32_bf16 v[86:89], v[130:133], v[212:215], v[86:89]
	v_mfma_f32_16x16x32_bf16 v[82:85], v[164:167], v[212:215], v[82:85]
	v_mfma_f32_16x16x32_bf16 v[126:129], v[134:137], v[192:195], v[126:129]
	v_mfma_f32_16x16x32_bf16 v[122:125], v[168:171], v[192:195], v[122:125]
	v_mfma_f32_16x16x32_bf16 v[118:121], v[134:137], v[200:203], v[118:121]
	v_mfma_f32_16x16x32_bf16 v[114:117], v[168:171], v[200:203], v[114:117]
	v_mfma_f32_16x16x32_bf16 v[102:105], v[134:137], v[208:211], v[102:105]
	v_mfma_f32_16x16x32_bf16 v[98:101], v[168:171], v[208:211], v[98:101]
	v_mfma_f32_16x16x32_bf16 v[86:89], v[134:137], v[216:219], v[86:89]
	v_mfma_f32_16x16x32_bf16 v[82:85], v[168:171], v[216:219], v[82:85]
	s_setprio 0
	s_setprio 1
	v_mfma_f32_16x16x32_bf16 v[110:113], v[172:175], v[188:191], v[110:113]
	v_mfma_f32_16x16x32_bf16 v[106:109], v[180:183], v[188:191], v[106:109]
	v_mfma_f32_16x16x32_bf16 v[94:97], v[172:175], v[196:199], v[94:97]
	v_mfma_f32_16x16x32_bf16 v[90:93], v[180:183], v[196:199], v[90:93]
	v_mfma_f32_16x16x32_bf16 v[78:81], v[172:175], v[204:207], v[78:81]
	v_mfma_f32_16x16x32_bf16 v[74:77], v[180:183], v[204:207], v[74:77]
	v_mfma_f32_16x16x32_bf16 v[70:73], v[172:175], v[212:215], v[70:73]
	v_mfma_f32_16x16x32_bf16 v[66:69], v[180:183], v[212:215], v[66:69]
	v_mfma_f32_16x16x32_bf16 v[110:113], v[176:179], v[192:195], v[110:113]
	v_mfma_f32_16x16x32_bf16 v[106:109], v[184:187], v[192:195], v[106:109]
	v_mfma_f32_16x16x32_bf16 v[94:97], v[176:179], v[200:203], v[94:97]
	v_mfma_f32_16x16x32_bf16 v[90:93], v[184:187], v[200:203], v[90:93]
	v_mfma_f32_16x16x32_bf16 v[78:81], v[176:179], v[208:211], v[78:81]
	v_mfma_f32_16x16x32_bf16 v[74:77], v[184:187], v[208:211], v[74:77]
	v_mfma_f32_16x16x32_bf16 v[70:73], v[176:179], v[216:219], v[70:73]
	v_mfma_f32_16x16x32_bf16 v[66:69], v[184:187], v[216:219], v[66:69]
	s_setprio 0
	s_barrier
	s_add_i32 s52, s75, s5
	v_lshl_add_u64 v[220:221], v[220:221], 0, s[36:37]
	s_mov_b32 m0, s52
	ds_read_b128 v[188:191], v159 offset:49152
	ds_read_b128 v[192:195], v159 offset:50176
	ds_read_b128 v[196:199], v159 offset:51200
	ds_read_b128 v[200:203], v159 offset:52224
	ds_read_b128 v[204:207], v159 offset:53248
	ds_read_b128 v[208:211], v159 offset:54272
	ds_read_b128 v[212:215], v159 offset:55296
	ds_read_b128 v[216:219], v159 offset:56320
	global_load_lds_dwordx4 v[220:221], off
	s_add_i32 m0, s52, 0x2000
	s_add_u32 s50, s50, 0x80080
	v_lshl_add_u64 v[220:221], v[222:223], 0, s[36:37]
	s_addc_u32 s51, s51, 0
	s_add_i32 s52, s76, s5
	global_load_lds_dwordx4 v[220:221], off
	v_lshl_add_u64 v[220:221], s[50:51], 0, v[140:141]
	s_mov_b32 m0, s52
	s_nop 0
	global_load_lds_dwordx4 v[220:221], off
	v_lshl_add_u64 v[220:221], s[50:51], 0, v[144:145]
	s_add_i32 m0, s52, 0x2000
	s_nop 0
	global_load_lds_dwordx4 v[220:221], off
	v_lshl_add_u64 v[240:241], v[224:225], 0, s[36:37]
	v_lshl_add_u64 v[242:243], v[226:227], 0, s[36:37]
	s_waitcnt vmcnt(6)
	s_waitcnt lgkmcnt(0)
	s_barrier
	s_setprio 1
	s_waitcnt lgkmcnt(0)
	v_mfma_f32_16x16x32_bf16 v[62:65], v[130:133], v[188:191], v[62:65]
	v_mfma_f32_16x16x32_bf16 v[58:61], v[164:167], v[188:191], v[58:61]
	v_mfma_f32_16x16x32_bf16 v[54:57], v[130:133], v[196:199], v[54:57]
	v_mfma_f32_16x16x32_bf16 v[50:53], v[164:167], v[196:199], v[50:53]
	v_mfma_f32_16x16x32_bf16 v[38:41], v[130:133], v[204:207], v[38:41]
	v_mfma_f32_16x16x32_bf16 v[34:37], v[164:167], v[204:207], v[34:37]
	v_mfma_f32_16x16x32_bf16 v[22:25], v[130:133], v[212:215], v[22:25]
	v_mfma_f32_16x16x32_bf16 v[18:21], v[164:167], v[212:215], v[18:21]
	v_mfma_f32_16x16x32_bf16 v[62:65], v[134:137], v[192:195], v[62:65]
	v_mfma_f32_16x16x32_bf16 v[58:61], v[168:171], v[192:195], v[58:61]
	v_mfma_f32_16x16x32_bf16 v[54:57], v[134:137], v[200:203], v[54:57]
	v_mfma_f32_16x16x32_bf16 v[50:53], v[168:171], v[200:203], v[50:53]
	v_mfma_f32_16x16x32_bf16 v[38:41], v[134:137], v[208:211], v[38:41]
	v_mfma_f32_16x16x32_bf16 v[34:37], v[168:171], v[208:211], v[34:37]
	v_mfma_f32_16x16x32_bf16 v[22:25], v[134:137], v[216:219], v[22:25]
	v_mfma_f32_16x16x32_bf16 v[18:21], v[168:171], v[216:219], v[18:21]
	s_setprio 0
	s_setprio 1
	v_mfma_f32_16x16x32_bf16 v[46:49], v[172:175], v[188:191], v[46:49]
	v_mfma_f32_16x16x32_bf16 v[42:45], v[180:183], v[188:191], v[42:45]
	v_mfma_f32_16x16x32_bf16 v[30:33], v[172:175], v[196:199], v[30:33]
	v_mfma_f32_16x16x32_bf16 v[26:29], v[180:183], v[196:199], v[26:29]
	v_mfma_f32_16x16x32_bf16 v[14:17], v[172:175], v[204:207], v[14:17]
	v_mfma_f32_16x16x32_bf16 v[10:13], v[180:183], v[204:207], v[10:13]
	v_mfma_f32_16x16x32_bf16 v[6:9], v[172:175], v[212:215], v[6:9]
	v_mfma_f32_16x16x32_bf16 v[2:5], v[180:183], v[212:215], v[2:5]
	v_mfma_f32_16x16x32_bf16 v[46:49], v[176:179], v[192:195], v[46:49]
	v_mfma_f32_16x16x32_bf16 v[42:45], v[184:187], v[192:195], v[42:45]
	v_mfma_f32_16x16x32_bf16 v[30:33], v[176:179], v[200:203], v[30:33]
	v_mfma_f32_16x16x32_bf16 v[26:29], v[184:187], v[200:203], v[26:29]
	v_mfma_f32_16x16x32_bf16 v[14:17], v[176:179], v[208:211], v[14:17]
	v_mfma_f32_16x16x32_bf16 v[10:13], v[184:187], v[208:211], v[10:13]
	v_mfma_f32_16x16x32_bf16 v[6:9], v[176:179], v[216:219], v[6:9]
	v_mfma_f32_16x16x32_bf16 v[2:5], v[184:187], v[216:219], v[2:5]
	s_setprio 0
	s_barrier
	s_mov_b32 s99, 1
	s_add_i32 s74, s74, 2
	s_add_u32 s48, s48, 0x100
	s_addc_u32 s49, s49, 0
	s_add_u32 s72, s72, 0x100
	s_addc_u32 s73, s73, 0
	s_cmp_gt_u32 s74, 29
	s_cbranch_scc0 .LBB0_1412
	s_and_b64 vcc, exec, s[38:39]
	s_cbranch_vccz .LBB0_1415
	s_barrier

.LBB0_1684:
	s_mov_b32 s99, 0
	v_readlane_b32 s0, v253, 11
	v_readlane_b32 s1, v253, 12
	s_mov_b32 s3, s1
	s_cmp_lt_i32 s0, 19
	s_cselect_b64 s[0:1], -1, 0
	s_cmp_gt_i32 s3, 18
	s_cselect_b64 s[4:5], -1, 0
	s_and_b64 s[0:1], s[0:1], s[4:5]
	s_andn2_b64 vcc, exec, s[0:1]
	s_cbranch_vccnz .LBB0_1735
	v_readlane_b32 s0, v253, 0
	v_readlane_b32 s1, v253, 1
	s_load_dwordx2 s[12:13], s[0:1], 0xd0
	s_load_dwordx2 s[14:15], s[0:1], 0x80
	s_load_dwordx2 s[16:17], s[0:1], 0xa0
	s_load_dwordx4 s[8:11], s[0:1], 0xb0
	s_load_dwordx2 s[18:19], s[0:1], 0xc0
	s_waitcnt lgkmcnt(0)
	s_add_u32 s0, s12, 0x3800000
	s_addc_u32 s1, s13, 0
	v_mov_b32_e32 v11, v0
	s_cmpk_lt_i32 s2, 0x200
	s_nop 0
	v_readfirstlane_b32 s7, v11
	s_cbranch_scc0 .LBB0_1705
	v_lshlrev_b32_e32 v1, 4, v11
	v_add_u32_e32 v2, 0x2000, v1
	v_ashrrev_i32_e32 v3, 31, v2
	v_lshrrev_b32_e32 v3, 22, v3
	v_add_u32_e32 v3, v2, v3
	v_ashrrev_i32_e32 v10, 10, v3
	v_mul_i32_i24_e32 v3, 0x400, v10
	v_sub_u32_e32 v2, v2, v3
	v_lshrrev_b32_e32 v3, 4, v2
	v_bitop3_b32 v2, v3, v2, 32 bitop3:0x6c
	v_ashrrev_i32_e32 v3, 31, v2
	v_lshrrev_b32_e32 v3, 26, v3
	v_add_u32_e32 v3, v2, v3
	v_lshlrev_b32_e32 v4, 3, v10
	v_ashrrev_i32_e32 v12, 6, v3
	v_and_b32_e32 v4, -16, v4
	v_add_u32_e32 v4, v12, v4
	v_and_b32_e32 v5, 3, v12
	s_mov_b32 s6, 0xfffe0
	v_lshrrev_b32_e32 v6, 2, v4
	v_lshlrev_b32_e32 v7, 1, v4
	v_and_b32_e32 v3, 0xc0, v3
	v_and_or_b32 v5, v4, s6, v5
	v_and_b32_e32 v6, 4, v6
	v_and_b32_e32 v7, 24, v7
	v_sub_u32_e32 v2, v2, v3
	v_mov_b32_e32 v3, 1
	v_or3_b32 v5, v5, v6, v7
	v_lshlrev_b32_e32 v6, 5, v10
	v_ashrrev_i16_sdwa v2, v3, sext(v2) dst_sel:DWORD dst_unused:UNUSED_PAD src0_sel:DWORD src1_sel:BYTE_0
	v_and_b32_e32 v6, 32, v6
	v_bfe_i32 v13, v2, 0, 16
	v_add_lshl_u32 v2, v6, v13, 1
	v_lshl_add_u32 v146, v5, 12, v2
	v_lshl_add_u32 v148, v4, 12, v2
	v_bfe_i32 v2, v11, 27, 1
	v_lshrrev_b32_e32 v2, 22, v2
	v_add_u32_e32 v2, v1, v2
	v_and_b32_e32 v2, 0xfffffc00, v2
	v_sub_u32_e32 v1, v1, v2
	v_lshrrev_b32_e32 v2, 4, v1
	v_bitop3_b32 v2, v2, v1, 32 bitop3:0x6c
	v_ashrrev_i32_e32 v1, 31, v1
	v_lshrrev_b32_e32 v1, 26, v1
	v_add_u32_e32 v1, v2, v1
	v_ashrrev_i32_e32 v14, 6, v1
	v_ashrrev_i32_e32 v1, 31, v11
	v_lshrrev_b32_e32 v1, 26, v1
	v_add_u32_e32 v1, v11, v1
	v_ashrrev_i32_e32 v15, 6, v1
	v_lshlrev_b32_e32 v1, 3, v15
	s_add_u32 s3, s12, 0x46300000
	v_and_b32_e32 v1, -16, v1
	s_addc_u32 s4, s13, 0
	v_add_u32_e32 v1, v14, v1
	v_and_b32_e32 v4, 3, v14
	s_ashr_i32 s33, s2, 31
	v_and_or_b32 v4, v1, s6, v4
	s_lshr_b32 s6, s33, 29
	s_add_i32 s6, s2, s6
	s_ashr_i32 s20, s6, 3
	s_and_b32 s6, s6, -8
	s_ashr_i32 s28, s7, 6
	s_sub_i32 s6, s2, s6
	s_ashr_i32 s30, s7, 8
	s_lshl_b32 s5, s28, 10
	s_lshl_b32 s22, s6, 6
	s_mul_i32 s21, s6, 0x41
	s_cmp_lt_i32 s6, 0
	s_cselect_b32 s6, s21, s22
	s_add_i32 s6, s6, s20
	s_ashr_i32 s20, s6, 31
	s_lshr_b32 s20, s20, 26
	s_add_i32 s20, s6, s20
	s_ashr_i32 s21, s20, 6
	s_and_b32 s20, s20, 0xffc0
	s_sub_i32 s20, s6, s20
	s_bfe_i32 s6, s20, 0x80000
	s_bfe_u32 s6, s6, 0x3000c
	s_add_i32 s22, s20, s6
	s_bfe_i32 s6, s22, 0x80000
	s_and_b32 s22, s22, 0xf8
	v_lshrrev_b32_e32 v5, 2, v1
	v_lshlrev_b32_e32 v6, 1, v1
	s_sub_i32 s20, s20, s22
	v_and_b32_e32 v5, 4, v5
	v_and_b32_e32 v6, 24, v6
	s_lshl_b32 s21, s21, 3
	s_sext_i32_i16 s6, s6
	s_sext_i32_i8 s20, s20
	v_or3_b32 v4, v4, v5, v6
	v_mul_i32_i24_e32 v6, 64, v14
	s_lshr_b32 s6, s6, 3
	s_add_i32 s48, s21, s20
	v_sub_u32_e32 v2, v2, v6
	s_ashr_i32 s49, s48, 31
	s_bfe_i64 s[22:23], s[6:7], 0x100000
	v_lshlrev_b32_e32 v5, 5, v15
	v_ashrrev_i16_sdwa v2, v3, sext(v2) dst_sel:DWORD dst_unused:UNUSED_PAD src0_sel:DWORD src1_sel:BYTE_0
	s_lshl_b64 s[20:21], s[48:49], 20
	s_lshl_b64 s[22:23], s[22:23], 20
	v_and_b32_e32 v5, 32, v5
	v_bfe_i32 v16, v2, 0, 16
	s_add_u32 s52, s0, s22
	v_add_lshl_u32 v2, v5, v16, 1
	s_addc_u32 s53, s1, s23
	s_add_i32 s49, s5, 0
	v_lshl_add_u32 v150, v4, 12, v2
	s_add_i32 m0, s49, 0x10000
	v_lshl_add_u32 v152, v1, 12, v2
	global_load_lds_dwordx4 v150, s[52:53]
	s_add_i32 m0, s49, 0x12000
	s_add_u32 s22, s52, 0x80000
	global_load_lds_dwordx4 v146, s[52:53]
	s_addc_u32 s23, s53, 0
	s_add_i32 m0, s49, 0x14000
	v_mov_b32_e32 v151, 0
	global_load_lds_dwordx4 v150, s[22:23]
	s_add_i32 m0, s49, 0x16000
	s_add_u32 s50, s3, s20
	s_addc_u32 s51, s4, s21
	s_add_i32 s56, s49, 0x2000
	global_load_lds_dwordx4 v146, s[22:23]
	s_mov_b32 m0, s49
	s_add_u32 s20, s50, 0x80000
	global_load_lds_dwordx4 v152, s[50:51]
	s_mov_b32 m0, s56
	s_addc_u32 s21, s51, 0
	s_add_i32 s57, s49, 0x4000
	global_load_lds_dwordx4 v148, s[50:51]
	s_mov_b32 m0, s57
	s_add_i32 s58, s49, 0x6000
	global_load_lds_dwordx4 v152, s[20:21]
	s_mov_b32 m0, s58
	v_mov_b32_e32 v147, v151
	global_load_lds_dwordx4 v148, s[20:21]
	v_mov_b32_e32 v153, v151
	v_mov_b32_e32 v149, v151
	s_cmp_eq_u32 s30, 1
	s_mov_b32 s59, 0
	v_lshl_add_u64 v[8:9], s[52:53], 0, v[150:151]
	v_lshl_add_u64 v[4:5], s[52:53], 0, v[146:147]
	s_mov_b64 s[20:21], 0x80000
	v_lshl_add_u64 v[2:3], s[50:51], 0, v[152:153]
	s_cselect_b64 s[22:23], -1, 0
	s_cmp_lg_u32 s30, 1
	v_lshl_add_u64 v[6:7], s[50:51], 0, v[148:149]
	s_cbranch_scc1 .LBB0_1688
	s_barrier

.LBB0_1698:
	s_cmp_eq_u32 s99, 0
	s_cbranch_scc1 .Lbal_skip_1698
	s_mov_b32 m0, s64
	s_nop 0
	global_load_lds_dwordx4 v[240:241], off
	s_mov_b32 m0, s65
	s_nop 0
	global_load_lds_dwordx4 v[242:243], off
.Lbal_skip_1698:
	ds_read_b128 v[106:109], v172
	ds_read_b128 v[114:117], v172 offset:1024
	ds_read_b128 v[130:133], v172 offset:2048
	ds_read_b128 v[134:137], v172 offset:3072
	ds_read_b128 v[162:165], v173
	ds_read_b128 v[166:169], v173 offset:1024
	ds_read_b128 v[176:179], v173 offset:2048
	ds_read_b128 v[180:183], v173 offset:3072
	s_add_u32 s52, s50, 0xfff80080
	s_addc_u32 s53, s51, -1
	s_cmp_eq_u32 s73, 28
	s_cselect_b32 s55, s43, s53
	s_cselect_b32 s54, s69, s52
	s_cselect_b32 s53, s41, s72
	s_cselect_b32 s52, s70, s71
	v_lshl_add_u64 v[216:217], s[50:51], 0, v[154:155]
	s_add_i32 m0, s49, 0xc000
	ds_read_b128 v[184:187], v174
	ds_read_b128 v[188:191], v174 offset:1024
	ds_read_b128 v[192:195], v174 offset:2048
	ds_read_b128 v[196:199], v174 offset:3072
	ds_read_b128 v[200:203], v174 offset:4096
	ds_read_b128 v[204:207], v174 offset:5120
	ds_read_b128 v[208:211], v174 offset:6144
	ds_read_b128 v[212:215], v174 offset:7168
	global_load_lds_dwordx4 v[216:217], off
	v_lshl_add_u64 v[216:217], s[50:51], 0, v[156:157]
	s_add_i32 m0, s49, 0xe000
	s_nop 0
	global_load_lds_dwordx4 v[216:217], off
	s_waitcnt vmcnt(8)
	s_waitcnt lgkmcnt(0)
	s_barrier
	s_setprio 1
	s_waitcnt lgkmcnt(0)
	v_mfma_f32_16x16x32_bf16 v[142:145], v[106:109], v[184:187], v[142:145]
	v_mfma_f32_16x16x32_bf16 v[138:141], v[130:133], v[184:187], v[138:141]
	v_mfma_f32_16x16x32_bf16 v[126:129], v[106:109], v[192:195], v[126:129]
	v_mfma_f32_16x16x32_bf16 v[110:113], v[130:133], v[192:195], v[110:113]
	v_mfma_f32_16x16x32_bf16 v[102:105], v[106:109], v[200:203], v[102:105]
	v_mfma_f32_16x16x32_bf16 v[90:93], v[130:133], v[200:203], v[90:93]
	v_mfma_f32_16x16x32_bf16 v[86:89], v[106:109], v[208:211], v[86:89]
	v_mfma_f32_16x16x32_bf16 v[74:77], v[130:133], v[208:211], v[74:77]
	v_mfma_f32_16x16x32_bf16 v[142:145], v[114:117], v[188:191], v[142:145]
	v_mfma_f32_16x16x32_bf16 v[138:141], v[134:137], v[188:191], v[138:141]
	v_mfma_f32_16x16x32_bf16 v[126:129], v[114:117], v[196:199], v[126:129]
	v_mfma_f32_16x16x32_bf16 v[110:113], v[134:137], v[196:199], v[110:113]
	v_mfma_f32_16x16x32_bf16 v[102:105], v[114:117], v[204:207], v[102:105]
	v_mfma_f32_16x16x32_bf16 v[90:93], v[134:137], v[204:207], v[90:93]
	v_mfma_f32_16x16x32_bf16 v[86:89], v[114:117], v[212:215], v[86:89]
	v_mfma_f32_16x16x32_bf16 v[74:77], v[134:137], v[212:215], v[74:77]
	s_setprio 0
	s_setprio 1
	v_mfma_f32_16x16x32_bf16 v[122:125], v[162:165], v[184:187], v[122:125]
	v_mfma_f32_16x16x32_bf16 v[118:121], v[176:179], v[184:187], v[118:121]
	v_mfma_f32_16x16x32_bf16 v[98:101], v[162:165], v[192:195], v[98:101]
	v_mfma_f32_16x16x32_bf16 v[94:97], v[176:179], v[192:195], v[94:97]
	v_mfma_f32_16x16x32_bf16 v[82:85], v[162:165], v[200:203], v[82:85]
	v_mfma_f32_16x16x32_bf16 v[78:81], v[176:179], v[200:203], v[78:81]
	v_mfma_f32_16x16x32_bf16 v[70:73], v[162:165], v[208:211], v[70:73]
	v_mfma_f32_16x16x32_bf16 v[66:69], v[176:179], v[208:211], v[66:69]
	v_mfma_f32_16x16x32_bf16 v[122:125], v[166:169], v[188:191], v[122:125]
	v_mfma_f32_16x16x32_bf16 v[118:121], v[180:183], v[188:191], v[118:121]
	v_mfma_f32_16x16x32_bf16 v[98:101], v[166:169], v[196:199], v[98:101]
	v_mfma_f32_16x16x32_bf16 v[94:97], v[180:183], v[196:199], v[94:97]
	v_mfma_f32_16x16x32_bf16 v[82:85], v[166:169], v[204:207], v[82:85]
	v_mfma_f32_16x16x32_bf16 v[78:81], v[180:183], v[204:207], v[78:81]
	v_mfma_f32_16x16x32_bf16 v[70:73], v[166:169], v[212:215], v[70:73]
	v_mfma_f32_16x16x32_bf16 v[66:69], v[180:183], v[212:215], v[66:69]
	s_setprio 0
	s_barrier
	s_add_i32 s62, s66, s5
	v_lshl_add_u64 v[216:217], s[52:53], 0, v[150:151]
	s_mov_b32 m0, s62
	ds_read_b128 v[184:187], v174 offset:16384
	ds_read_b128 v[188:191], v174 offset:17408
	ds_read_b128 v[192:195], v174 offset:18432
	ds_read_b128 v[196:199], v174 offset:19456
	ds_read_b128 v[200:203], v174 offset:20480
	ds_read_b128 v[204:207], v174 offset:21504
	ds_read_b128 v[208:211], v174 offset:22528
	ds_read_b128 v[212:215], v174 offset:23552
	global_load_lds_dwordx4 v[216:217], off
	s_add_i32 m0, s62, 0x2000
	s_add_u32 s74, s52, 0x80000
	v_lshl_add_u64 v[218:219], s[52:53], 0, v[146:147]
	s_addc_u32 s75, s53, 0
	s_add_i32 s62, s67, s5
	global_load_lds_dwordx4 v[218:219], off
	v_lshl_add_u64 v[220:221], s[74:75], 0, v[150:151]
	s_mov_b32 m0, s62
	v_lshl_add_u64 v[222:223], s[54:55], 0, v[148:149]
	global_load_lds_dwordx4 v[220:221], off
	v_lshl_add_u64 v[220:221], s[74:75], 0, v[146:147]
	s_add_i32 m0, s62, 0x2000
	s_nop 0
	global_load_lds_dwordx4 v[220:221], off
	s_waitcnt vmcnt(6)
	s_waitcnt lgkmcnt(0)
	s_barrier
	s_setprio 1
	s_waitcnt lgkmcnt(0)
	v_mfma_f32_16x16x32_bf16 v[62:65], v[106:109], v[184:187], v[62:65]
	v_mfma_f32_16x16x32_bf16 v[58:61], v[130:133], v[184:187], v[58:61]
	v_mfma_f32_16x16x32_bf16 v[54:57], v[106:109], v[192:195], v[54:57]
	v_mfma_f32_16x16x32_bf16 v[42:45], v[130:133], v[192:195], v[42:45]
	v_mfma_f32_16x16x32_bf16 v[38:41], v[106:109], v[200:203], v[38:41]
	v_mfma_f32_16x16x32_bf16 v[26:29], v[130:133], v[200:203], v[26:29]
	v_mfma_f32_16x16x32_bf16 v[22:25], v[106:109], v[208:211], v[22:25]
	v_mfma_f32_16x16x32_bf16 v[10:13], v[130:133], v[208:211], v[10:13]
	v_mfma_f32_16x16x32_bf16 v[62:65], v[114:117], v[188:191], v[62:65]
	v_mfma_f32_16x16x32_bf16 v[58:61], v[134:137], v[188:191], v[58:61]
	v_mfma_f32_16x16x32_bf16 v[54:57], v[114:117], v[196:199], v[54:57]
	v_mfma_f32_16x16x32_bf16 v[42:45], v[134:137], v[196:199], v[42:45]
	v_mfma_f32_16x16x32_bf16 v[38:41], v[114:117], v[204:207], v[38:41]
	v_mfma_f32_16x16x32_bf16 v[26:29], v[134:137], v[204:207], v[26:29]
	v_mfma_f32_16x16x32_bf16 v[22:25], v[114:117], v[212:215], v[22:25]
	v_mfma_f32_16x16x32_bf16 v[10:13], v[134:137], v[212:215], v[10:13]
	s_setprio 0
	s_setprio 1
	v_mfma_f32_16x16x32_bf16 v[50:53], v[162:165], v[184:187], v[50:53]
	v_mfma_f32_16x16x32_bf16 v[46:49], v[176:179], v[184:187], v[46:49]
	v_mfma_f32_16x16x32_bf16 v[34:37], v[162:165], v[192:195], v[34:37]
	v_mfma_f32_16x16x32_bf16 v[30:33], v[176:179], v[192:195], v[30:33]
	v_mfma_f32_16x16x32_bf16 v[18:21], v[162:165], v[200:203], v[18:21]
	v_mfma_f32_16x16x32_bf16 v[14:17], v[176:179], v[200:203], v[14:17]
	v_mfma_f32_16x16x32_bf16 v[6:9], v[162:165], v[208:211], v[6:9]
	v_mfma_f32_16x16x32_bf16 v[2:5], v[176:179], v[208:211], v[2:5]
	v_mfma_f32_16x16x32_bf16 v[50:53], v[166:169], v[188:191], v[50:53]
	v_mfma_f32_16x16x32_bf16 v[46:49], v[180:183], v[188:191], v[46:49]
	v_mfma_f32_16x16x32_bf16 v[34:37], v[166:169], v[196:199], v[34:37]
	v_mfma_f32_16x16x32_bf16 v[30:33], v[180:183], v[196:199], v[30:33]
	v_mfma_f32_16x16x32_bf16 v[18:21], v[166:169], v[204:207], v[18:21]
	v_mfma_f32_16x16x32_bf16 v[14:17], v[180:183], v[204:207], v[14:17]
	v_mfma_f32_16x16x32_bf16 v[6:9], v[166:169], v[212:215], v[6:9]
	v_mfma_f32_16x16x32_bf16 v[2:5], v[180:183], v[212:215], v[2:5]
	s_setprio 0
	s_barrier
	v_lshl_add_u64 v[220:221], s[54:55], 0, v[152:153]
	s_mov_b32 m0, s49
	s_nop 0
	global_load_lds_dwordx4 v[220:221], off
	s_mov_b32 m0, s56
	s_nop 0
	global_load_lds_dwordx4 v[222:223], off
	s_add_i32 s62, 0, 0x18000
	s_add_i32 s63, 0, 0x1c000
	v_add_u32_e32 v134, s62, v170
	v_add_u32_e32 v175, s63, v170
	ds_read_b128 v[106:109], v134
	ds_read_b128 v[114:117], v134 offset:1024
	ds_read_b128 v[130:133], v134 offset:2048
	ds_read_b128 v[134:137], v134 offset:3072
	ds_read_b128 v[162:165], v175
	ds_read_b128 v[166:169], v175 offset:1024
	ds_read_b128 v[176:179], v175 offset:2048
	ds_read_b128 v[180:183], v175 offset:3072
	s_add_u32 s54, s54, 0x80000
	s_addc_u32 s55, s55, 0
	s_mov_b32 m0, s57
	v_lshl_add_u64 v[224:225], s[54:55], 0, v[152:153]
	ds_read_b128 v[184:187], v174 offset:32768
	ds_read_b128 v[188:191], v174 offset:33792
	ds_read_b128 v[192:195], v174 offset:34816
	ds_read_b128 v[196:199], v174 offset:35840
	ds_read_b128 v[200:203], v174 offset:36864
	ds_read_b128 v[204:207], v174 offset:37888
	ds_read_b128 v[208:211], v174 offset:38912
	ds_read_b128 v[212:215], v174 offset:39936
	global_load_lds_dwordx4 v[224:225], off
	v_lshl_add_u64 v[224:225], s[54:55], 0, v[148:149]
	s_mov_b32 m0, s58
	s_nop 0
	global_load_lds_dwordx4 v[224:225], off
	s_waitcnt vmcnt(8)
	s_waitcnt lgkmcnt(0)
	s_barrier
	s_setprio 1
	s_waitcnt lgkmcnt(0)
	v_mfma_f32_16x16x32_bf16 v[142:145], v[106:109], v[184:187], v[142:145]
	v_mfma_f32_16x16x32_bf16 v[138:141], v[130:133], v[184:187], v[138:141]
	v_mfma_f32_16x16x32_bf16 v[126:129], v[106:109], v[192:195], v[126:129]
	v_mfma_f32_16x16x32_bf16 v[110:113], v[130:133], v[192:195], v[110:113]
	v_mfma_f32_16x16x32_bf16 v[102:105], v[106:109], v[200:203], v[102:105]
	v_mfma_f32_16x16x32_bf16 v[90:93], v[130:133], v[200:203], v[90:93]
	v_mfma_f32_16x16x32_bf16 v[86:89], v[106:109], v[208:211], v[86:89]
	v_mfma_f32_16x16x32_bf16 v[74:77], v[130:133], v[208:211], v[74:77]
	v_mfma_f32_16x16x32_bf16 v[142:145], v[114:117], v[188:191], v[142:145]
	v_mfma_f32_16x16x32_bf16 v[138:141], v[134:137], v[188:191], v[138:141]
	v_mfma_f32_16x16x32_bf16 v[126:129], v[114:117], v[196:199], v[126:129]
	v_mfma_f32_16x16x32_bf16 v[110:113], v[134:137], v[196:199], v[110:113]
	v_mfma_f32_16x16x32_bf16 v[102:105], v[114:117], v[204:207], v[102:105]
	v_mfma_f32_16x16x32_bf16 v[90:93], v[134:137], v[204:207], v[90:93]
	v_mfma_f32_16x16x32_bf16 v[86:89], v[114:117], v[212:215], v[86:89]
	v_mfma_f32_16x16x32_bf16 v[74:77], v[134:137], v[212:215], v[74:77]
	s_setprio 0
	s_setprio 1
	v_mfma_f32_16x16x32_bf16 v[122:125], v[162:165], v[184:187], v[122:125]
	v_mfma_f32_16x16x32_bf16 v[118:121], v[176:179], v[184:187], v[118:121]
	v_mfma_f32_16x16x32_bf16 v[98:101], v[162:165], v[192:195], v[98:101]
	v_mfma_f32_16x16x32_bf16 v[94:97], v[176:179], v[192:195], v[94:97]
	v_mfma_f32_16x16x32_bf16 v[82:85], v[162:165], v[200:203], v[82:85]
	v_mfma_f32_16x16x32_bf16 v[78:81], v[176:179], v[200:203], v[78:81]
	v_mfma_f32_16x16x32_bf16 v[70:73], v[162:165], v[208:211], v[70:73]
	v_mfma_f32_16x16x32_bf16 v[66:69], v[176:179], v[208:211], v[66:69]
	v_mfma_f32_16x16x32_bf16 v[122:125], v[166:169], v[188:191], v[122:125]
	v_mfma_f32_16x16x32_bf16 v[118:121], v[180:183], v[188:191], v[118:121]
	v_mfma_f32_16x16x32_bf16 v[98:101], v[166:169], v[196:199], v[98:101]
	v_mfma_f32_16x16x32_bf16 v[94:97], v[180:183], v[196:199], v[94:97]
	v_mfma_f32_16x16x32_bf16 v[82:85], v[166:169], v[204:207], v[82:85]
	v_mfma_f32_16x16x32_bf16 v[78:81], v[180:183], v[204:207], v[78:81]
	v_mfma_f32_16x16x32_bf16 v[70:73], v[166:169], v[212:215], v[70:73]
	v_mfma_f32_16x16x32_bf16 v[66:69], v[180:183], v[212:215], v[66:69]
	s_setprio 0
	s_barrier
	s_add_i32 s54, s62, s5
	v_lshl_add_u64 v[216:217], v[216:217], 0, s[28:29]
	s_mov_b32 m0, s54
	ds_read_b128 v[184:187], v174 offset:49152
	ds_read_b128 v[188:191], v174 offset:50176
	ds_read_b128 v[192:195], v174 offset:51200
	ds_read_b128 v[196:199], v174 offset:52224
	ds_read_b128 v[200:203], v174 offset:53248
	ds_read_b128 v[204:207], v174 offset:54272
	ds_read_b128 v[208:211], v174 offset:55296
	ds_read_b128 v[212:215], v174 offset:56320
	global_load_lds_dwordx4 v[216:217], off
	s_add_i32 m0, s54, 0x2000
	s_add_u32 s52, s52, 0x80080
	v_lshl_add_u64 v[216:217], v[218:219], 0, s[28:29]
	s_addc_u32 s53, s53, 0
	s_add_i32 s54, s63, s5
	global_load_lds_dwordx4 v[216:217], off
	v_lshl_add_u64 v[216:217], s[52:53], 0, v[150:151]
	s_mov_b32 m0, s54
	s_nop 0
	global_load_lds_dwordx4 v[216:217], off
	v_lshl_add_u64 v[216:217], s[52:53], 0, v[146:147]
	s_add_i32 m0, s54, 0x2000
	s_nop 0
	global_load_lds_dwordx4 v[216:217], off
	v_lshl_add_u64 v[240:241], v[220:221], 0, s[28:29]
	v_lshl_add_u64 v[242:243], v[222:223], 0, s[28:29]
	s_waitcnt vmcnt(6)
	s_waitcnt lgkmcnt(0)
	s_barrier
	s_setprio 1
	s_waitcnt lgkmcnt(0)
	v_mfma_f32_16x16x32_bf16 v[62:65], v[106:109], v[184:187], v[62:65]
	v_mfma_f32_16x16x32_bf16 v[58:61], v[130:133], v[184:187], v[58:61]
	v_mfma_f32_16x16x32_bf16 v[54:57], v[106:109], v[192:195], v[54:57]
	v_mfma_f32_16x16x32_bf16 v[42:45], v[130:133], v[192:195], v[42:45]
	v_mfma_f32_16x16x32_bf16 v[38:41], v[106:109], v[200:203], v[38:41]
	v_mfma_f32_16x16x32_bf16 v[26:29], v[130:133], v[200:203], v[26:29]
	v_mfma_f32_16x16x32_bf16 v[22:25], v[106:109], v[208:211], v[22:25]
	v_mfma_f32_16x16x32_bf16 v[10:13], v[130:133], v[208:211], v[10:13]
	v_mfma_f32_16x16x32_bf16 v[62:65], v[114:117], v[188:191], v[62:65]
	v_mfma_f32_16x16x32_bf16 v[58:61], v[134:137], v[188:191], v[58:61]
	v_mfma_f32_16x16x32_bf16 v[54:57], v[114:117], v[196:199], v[54:57]
	v_mfma_f32_16x16x32_bf16 v[42:45], v[134:137], v[196:199], v[42:45]
	v_mfma_f32_16x16x32_bf16 v[38:41], v[114:117], v[204:207], v[38:41]
	v_mfma_f32_16x16x32_bf16 v[26:29], v[134:137], v[204:207], v[26:29]
	v_mfma_f32_16x16x32_bf16 v[22:25], v[114:117], v[212:215], v[22:25]
	v_mfma_f32_16x16x32_bf16 v[10:13], v[134:137], v[212:215], v[10:13]
	s_setprio 0
	s_setprio 1
	v_mfma_f32_16x16x32_bf16 v[50:53], v[162:165], v[184:187], v[50:53]
	v_mfma_f32_16x16x32_bf16 v[46:49], v[176:179], v[184:187], v[46:49]
	v_mfma_f32_16x16x32_bf16 v[34:37], v[162:165], v[192:195], v[34:37]
	v_mfma_f32_16x16x32_bf16 v[30:33], v[176:179], v[192:195], v[30:33]
	v_mfma_f32_16x16x32_bf16 v[18:21], v[162:165], v[200:203], v[18:21]
	v_mfma_f32_16x16x32_bf16 v[14:17], v[176:179], v[200:203], v[14:17]
	v_mfma_f32_16x16x32_bf16 v[6:9], v[162:165], v[208:211], v[6:9]
	v_mfma_f32_16x16x32_bf16 v[2:5], v[176:179], v[208:211], v[2:5]
	v_mfma_f32_16x16x32_bf16 v[50:53], v[166:169], v[188:191], v[50:53]
	v_mfma_f32_16x16x32_bf16 v[46:49], v[180:183], v[188:191], v[46:49]
	v_mfma_f32_16x16x32_bf16 v[34:37], v[166:169], v[196:199], v[34:37]
	v_mfma_f32_16x16x32_bf16 v[30:33], v[180:183], v[196:199], v[30:33]
	v_mfma_f32_16x16x32_bf16 v[18:21], v[166:169], v[204:207], v[18:21]
	v_mfma_f32_16x16x32_bf16 v[14:17], v[180:183], v[204:207], v[14:17]
	v_mfma_f32_16x16x32_bf16 v[6:9], v[166:169], v[212:215], v[6:9]
	v_mfma_f32_16x16x32_bf16 v[2:5], v[180:183], v[212:215], v[2:5]
	s_setprio 0
	s_barrier
	s_mov_b32 s99, 1
	s_add_i32 s73, s73, 2
	s_add_u32 s50, s50, 0x100
	s_addc_u32 s51, s51, 0
	s_add_u32 s71, s71, 0x100
	s_addc_u32 s72, s72, 0
	s_cmp_gt_u32 s73, 29
	s_cbranch_scc0 .LBB0_1698
	s_and_b64 vcc, exec, s[30:31]
	s_cbranch_vccz .LBB0_1701
	s_barrier

.LBB0_2084:
	s_mov_b32 s99, 0
	v_readlane_b32 s0, v253, 11
	v_readlane_b32 s1, v253, 12
	s_mov_b32 s3, s1
	s_cmp_lt_i32 s0, 23
	s_cselect_b64 s[0:1], -1, 0
	s_cmp_gt_i32 s3, 22
	s_cselect_b64 s[4:5], -1, 0
	s_and_b64 s[0:1], s[0:1], s[4:5]
	s_andn2_b64 vcc, exec, s[0:1]
	s_cbranch_vccnz .LBB0_2156
	v_readlane_b32 s0, v253, 0
	v_readlane_b32 s1, v253, 1
	s_load_dwordx2 s[12:13], s[0:1], 0x80
	s_load_dwordx2 s[14:15], s[0:1], 0xa0
	s_load_dwordx4 s[8:11], s[0:1], 0xb0
	s_load_dwordx2 s[16:17], s[0:1], 0xc0
	s_load_dwordx2 s[18:19], s[0:1], 0xd0
	v_mov_b32_e32 v6, v0
	s_cmpk_lt_i32 s2, 0x580
	s_nop 0
	v_readfirstlane_b32 s34, v6
	s_cbranch_scc0 .LBB0_2103
	s_waitcnt lgkmcnt(0)
	s_add_u32 s20, s18, 0x25000000
	s_addc_u32 s21, s19, 0
	v_ashrrev_i32_e32 v1, 31, v6
	s_add_u32 s0, s18, 0xf000000
	v_lshrrev_b32_e32 v1, 26, v1
	s_addc_u32 s1, s19, 0
	v_add_u32_e32 v1, v6, v1
	s_add_u32 s22, s18, 0x940000
	v_ashrrev_i32_e32 v7, 6, v1
	v_bfe_i32 v1, v6, 27, 1
	s_addc_u32 s23, s19, 0
	s_and_b32 s3, s2, 7
	v_lshlrev_b32_e32 v2, 4, v6
	v_lshrrev_b32_e32 v1, 22, v1
	s_mulk_i32 s3, 0xb0
	s_ashr_i32 s4, s2, 3
	v_add_u32_e32 v1, v2, v1
	s_add_i32 s3, s3, s4
	v_and_b32_e32 v1, 0xfffffc00, v1
	s_mul_hi_i32 s4, s3, 0x2e8ba2e9
	v_sub_u32_e32 v1, v2, v1
	s_lshr_b32 s5, s4, 31
	s_ashr_i32 s4, s4, 4
	v_lshrrev_b32_e32 v3, 4, v1
	s_add_i32 s4, s4, s5
	v_bitop3_b32 v8, v3, v1, 32 bitop3:0x6c
	v_ashrrev_i32_e32 v1, 31, v1
	s_mul_i32 s5, s4, 0xffffffa8
	v_lshrrev_b32_e32 v1, 26, v1
	s_add_i32 s5, s5, s3
	v_lshlrev_b32_e32 v3, 3, v7
	v_add_u32_e32 v1, v8, v1
	s_mul_hi_i32 s3, s5, 0x2e8ba2e9
	v_and_b32_e32 v3, -16, v3
	v_ashrrev_i32_e32 v9, 6, v1
	v_add_u32_e32 v2, 0x2000, v2
	s_lshr_b32 s6, s3, 31
	s_ashr_i32 s3, s3, 1
	v_add_u32_e32 v1, v9, v3
	v_ashrrev_i32_e32 v3, 31, v2
	s_add_i32 s3, s3, s6
	s_mul_i32 s6, s4, 9
	v_lshrrev_b32_e32 v3, 22, v3
	s_add_i32 s64, s3, s6
	s_sub_i32 s3, s4, s3
	v_add_u32_e32 v3, v2, v3
	s_mul_i32 s3, s3, 11
	v_ashrrev_i32_e32 v10, 10, v3
	s_add_i32 s40, s3, s5
	v_mul_i32_i24_e32 v3, 0x400, v10
	s_ashr_i32 s41, s40, 31
	v_sub_u32_e32 v2, v2, v3
	s_lshl_b64 s[4:5], s[40:41], 20
	v_lshrrev_b32_e32 v3, 4, v2
	s_add_u32 s42, s0, s4
	v_bitop3_b32 v11, v3, v2, 32 bitop3:0x6c
	s_addc_u32 s43, s1, s5
	v_ashrrev_i32_e32 v3, 31, v11
	s_ashr_i32 s36, s34, 6
	s_ashr_i32 s35, s34, 8
	v_lshrrev_b32_e32 v3, 26, v3
	s_lshl_b32 s3, s36, 10
	v_lshlrev_b32_e32 v2, 3, v10
	v_add_u32_e32 v12, v11, v3
	s_add_u32 s6, s42, 0x80000
	v_and_b32_e32 v2, -16, v2
	v_ashrrev_i32_e32 v13, 6, v12
	s_addc_u32 s7, s43, 0
	s_lshl_b32 s4, s64, 8
	v_add_u32_e32 v146, v13, v2
	s_or_b32 s5, s4, 0x80
	v_add_u32_e32 v2, s4, v1
	v_ashrrev_i32_e32 v3, 31, v2
	v_add_u32_e32 v4, s5, v1
	v_lshl_add_u64 v[2:3], v[2:3], 2, s[22:23]
	v_ashrrev_i32_e32 v5, 31, v4
	v_lshl_add_u64 v[4:5], v[4:5], 2, s[22:23]
	global_load_dword v14, v[2:3], off
	global_load_dword v15, v[4:5], off
	v_add_u32_e32 v2, s4, v146
	v_ashrrev_i32_e32 v3, 31, v2
	v_add_u32_e32 v4, s5, v146
	v_lshl_add_u64 v[2:3], v[2:3], 2, s[22:23]
	v_ashrrev_i32_e32 v5, 31, v4
	v_lshl_add_u64 v[4:5], v[4:5], 2, s[22:23]
	global_load_dword v16, v[2:3], off
	global_load_dword v17, v[4:5], off
	v_mul_i32_i24_e32 v3, 64, v9
	v_sub_u32_e32 v3, v8, v3
	v_mov_b32_e32 v4, 1
	v_lshlrev_b32_e32 v2, 5, v7
	v_ashrrev_i16_sdwa v3, v4, sext(v3) dst_sel:DWORD dst_unused:UNUSED_PAD src0_sel:DWORD src1_sel:BYTE_0
	v_and_b32_e32 v2, 32, v2
	v_bfe_i32 v3, v3, 0, 16
	v_add_lshl_u32 v147, v2, v3, 1
	v_and_b32_e32 v3, 0xc0, v12
	v_sub_u32_e32 v3, v11, v3
	v_lshlrev_b32_e32 v2, 5, v10
	v_ashrrev_i16_sdwa v3, v4, sext(v3) dst_sel:DWORD dst_unused:UNUSED_PAD src0_sel:DWORD src1_sel:BYTE_0
	v_and_b32_e32 v2, 32, v2
	v_bfe_i32 v3, v3, 0, 16
	v_add_lshl_u32 v148, v2, v3, 1
	v_and_b32_e32 v2, 3, v13
	s_mov_b32 s4, 0xfffe0
	v_lshrrev_b32_e32 v3, 2, v146
	v_lshlrev_b32_e32 v4, 1, v146
	v_and_or_b32 v2, v146, s4, v2
	v_and_b32_e32 v3, 4, v3
	v_and_b32_e32 v4, 24, v4
	v_or3_b32 v2, v2, v3, v4
	v_lshl_add_u32 v130, v2, 12, v148
	v_and_b32_e32 v2, 3, v9
	v_lshrrev_b32_e32 v3, 2, v1
	v_lshlrev_b32_e32 v4, 1, v1
	v_and_or_b32 v2, v1, s4, v2
	v_and_b32_e32 v3, 4, v3
	v_and_b32_e32 v4, 24, v4
	v_or3_b32 v2, v2, v3, v4
	s_add_i32 s4, s3, 0
	v_lshl_add_u32 v132, v2, 12, v147
	s_add_i32 m0, s4, 0x10000
	s_add_i32 s5, s4, 0x2000
	global_load_lds_dwordx4 v132, s[42:43]
	s_add_i32 m0, s4, 0x12000
	s_add_i32 s33, s4, 0x4000
	global_load_lds_dwordx4 v130, s[42:43]
	s_add_i32 m0, s4, 0x14000
	s_add_i32 s41, s4, 0x6000
	global_load_lds_dwordx4 v132, s[6:7]
	s_add_i32 m0, s4, 0x16000
	v_mov_b32_e32 v135, 0
	global_load_lds_dwordx4 v130, s[6:7]
	s_mov_b32 m0, s4
	v_mov_b32_e32 v133, v135
	v_mov_b32_e32 v131, v135
	s_cmp_eq_u32 s35, 1
	s_mov_b32 s48, 0
	v_lshl_add_u64 v[4:5], s[42:43], 0, v[132:133]
	s_cselect_b64 s[24:25], -1, 0
	s_cmp_lg_u32 s35, 1
	v_mov_b32_e32 v141, v135
	s_waitcnt vmcnt(0)
	v_max_i32_e32 v2, 0, v14
	v_lshl_add_u32 v134, v2, 12, v147
	v_max_i32_e32 v3, 0, v15
	global_load_lds_dwordx4 v134, s[20:21]
	s_mov_b32 m0, s5
	v_lshl_add_u32 v136, v3, 12, v147
	v_max_i32_e32 v2, 0, v16
	v_lshl_add_u32 v140, v2, 12, v148
	v_max_i32_e32 v3, 0, v17
	global_load_lds_dwordx4 v140, s[20:21]
	s_mov_b32 m0, s33
	v_lshl_add_u32 v138, v3, 12, v148
	global_load_lds_dwordx4 v136, s[20:21]
	s_mov_b32 m0, s41
	v_lshl_add_u64 v[2:3], s[42:43], 0, v[130:131]
	global_load_lds_dwordx4 v138, s[20:21]
	s_cbranch_scc1 .LBB0_2088
	s_barrier

.Lbal_skip_2096:
	ds_read_b128 v[160:163], v150
	ds_read_b128 v[164:167], v150 offset:1024
	ds_read_b128 v[168:171], v150 offset:2048
	ds_read_b128 v[172:175], v150 offset:3072
	ds_read_b128 v[176:179], v151
	ds_read_b128 v[180:183], v151 offset:1024
	ds_read_b128 v[184:187], v151 offset:2048
	ds_read_b128 v[188:191], v151 offset:3072
	s_add_u32 s44, s18, s42
	s_addc_u32 s45, s19, s43
	s_add_u32 s46, s44, 0x25000100
	s_addc_u32 s47, s45, 0
	s_add_u32 s62, s66, s42
	s_addc_u32 s63, s67, s43
	s_cmpk_eq_i32 s42, 0xf00
	s_cselect_b64 vcc, -1, 0
	s_and_b64 s[44:45], vcc, exec
	v_cndmask_b32_e32 v134, v159, v155, vcc
	s_cselect_b32 s47, s21, s47
	s_cselect_b32 s46, s20, s46
	v_cndmask_b32_e32 v224, v140, v156, vcc
	v_cndmask_b32_e32 v137, v136, v158, vcc
	v_cndmask_b32_e32 v139, v138, v157, vcc
	s_cselect_b32 s45, s37, s63
	s_cselect_b32 s44, s65, s62
	s_mov_b32 m0, s52
	v_lshl_add_u64 v[226:227], v[144:145], 0, s[42:43]
	ds_read_b128 v[192:195], v152
	ds_read_b128 v[196:199], v152 offset:1024
	ds_read_b128 v[200:203], v152 offset:2048
	ds_read_b128 v[204:207], v152 offset:3072
	ds_read_b128 v[208:211], v152 offset:4096
	ds_read_b128 v[212:215], v152 offset:5120
	ds_read_b128 v[216:219], v152 offset:6144
	ds_read_b128 v[220:223], v152 offset:7168
	global_load_lds_dwordx4 v[226:227], off
	v_lshl_add_u64 v[226:227], v[142:143], 0, s[42:43]
	s_mov_b32 m0, s53
	s_nop 0
	global_load_lds_dwordx4 v[226:227], off
	s_waitcnt vmcnt(8)
	s_waitcnt lgkmcnt(0)
	s_barrier
	s_setprio 1
	s_waitcnt lgkmcnt(0)
	v_mfma_f32_16x16x32_bf16 v[126:129], v[160:163], v[192:195], v[126:129]
	v_mfma_f32_16x16x32_bf16 v[122:125], v[168:171], v[192:195], v[122:125]
	v_mfma_f32_16x16x32_bf16 v[110:113], v[160:163], v[200:203], v[110:113]
	v_mfma_f32_16x16x32_bf16 v[106:109], v[168:171], v[200:203], v[106:109]
	v_mfma_f32_16x16x32_bf16 v[94:97], v[160:163], v[208:211], v[94:97]
	v_mfma_f32_16x16x32_bf16 v[90:93], v[168:171], v[208:211], v[90:93]
	v_mfma_f32_16x16x32_bf16 v[78:81], v[160:163], v[216:219], v[78:81]
	v_mfma_f32_16x16x32_bf16 v[74:77], v[168:171], v[216:219], v[74:77]
	v_mfma_f32_16x16x32_bf16 v[126:129], v[164:167], v[196:199], v[126:129]
	v_mfma_f32_16x16x32_bf16 v[122:125], v[172:175], v[196:199], v[122:125]
	v_mfma_f32_16x16x32_bf16 v[110:113], v[164:167], v[204:207], v[110:113]
	v_mfma_f32_16x16x32_bf16 v[106:109], v[172:175], v[204:207], v[106:109]
	v_mfma_f32_16x16x32_bf16 v[94:97], v[164:167], v[212:215], v[94:97]
	v_mfma_f32_16x16x32_bf16 v[90:93], v[172:175], v[212:215], v[90:93]
	v_mfma_f32_16x16x32_bf16 v[78:81], v[164:167], v[220:223], v[78:81]
	v_mfma_f32_16x16x32_bf16 v[74:77], v[172:175], v[220:223], v[74:77]
	s_setprio 0
	s_setprio 1
	v_mfma_f32_16x16x32_bf16 v[118:121], v[176:179], v[192:195], v[118:121]
	v_mfma_f32_16x16x32_bf16 v[114:117], v[184:187], v[192:195], v[114:117]
	v_mfma_f32_16x16x32_bf16 v[102:105], v[176:179], v[200:203], v[102:105]
	v_mfma_f32_16x16x32_bf16 v[98:101], v[184:187], v[200:203], v[98:101]
	v_mfma_f32_16x16x32_bf16 v[86:89], v[176:179], v[208:211], v[86:89]
	v_mfma_f32_16x16x32_bf16 v[82:85], v[184:187], v[208:211], v[82:85]
	v_mfma_f32_16x16x32_bf16 v[70:73], v[176:179], v[216:219], v[70:73]
	v_mfma_f32_16x16x32_bf16 v[66:69], v[184:187], v[216:219], v[66:69]
	v_mfma_f32_16x16x32_bf16 v[118:121], v[180:183], v[196:199], v[118:121]
	v_mfma_f32_16x16x32_bf16 v[114:117], v[188:191], v[196:199], v[114:117]
	v_mfma_f32_16x16x32_bf16 v[102:105], v[180:183], v[204:207], v[102:105]
	v_mfma_f32_16x16x32_bf16 v[98:101], v[188:191], v[204:207], v[98:101]
	v_mfma_f32_16x16x32_bf16 v[86:89], v[180:183], v[212:215], v[86:89]
	v_mfma_f32_16x16x32_bf16 v[82:85], v[188:191], v[212:215], v[82:85]
	v_mfma_f32_16x16x32_bf16 v[70:73], v[180:183], v[220:223], v[70:73]
	v_mfma_f32_16x16x32_bf16 v[66:69], v[188:191], v[220:223], v[66:69]
	s_setprio 0
	s_barrier
	s_mov_b32 m0, s54
	v_lshl_add_u64 v[226:227], s[44:45], 0, v[132:133]
	s_add_u32 s70, s44, 0x80000
	ds_read_b128 v[192:195], v152 offset:16384
	ds_read_b128 v[196:199], v152 offset:17408
	ds_read_b128 v[200:203], v152 offset:18432
	ds_read_b128 v[204:207], v152 offset:19456
	ds_read_b128 v[208:211], v152 offset:20480
	ds_read_b128 v[212:215], v152 offset:21504
	ds_read_b128 v[216:219], v152 offset:22528
	ds_read_b128 v[220:223], v152 offset:23552
	global_load_lds_dwordx4 v[226:227], off
	v_lshl_add_u64 v[228:229], s[44:45], 0, v[130:131]
	s_mov_b32 m0, s55
	s_addc_u32 s71, s45, 0
	global_load_lds_dwordx4 v[228:229], off
	v_lshl_add_u64 v[230:231], s[70:71], 0, v[132:133]
	s_mov_b32 m0, s56
	v_mov_b32_e32 v225, v135
	global_load_lds_dwordx4 v[230:231], off
	v_lshl_add_u64 v[230:231], s[70:71], 0, v[130:131]
	s_mov_b32 m0, s57
	s_nop 0
	global_load_lds_dwordx4 v[230:231], off
	s_waitcnt vmcnt(6)
	s_waitcnt lgkmcnt(0)
	v_lshl_add_u64 v[224:225], s[46:47], 0, v[224:225]
	s_barrier
	s_setprio 1
	s_waitcnt lgkmcnt(0)
	v_mfma_f32_16x16x32_bf16 v[62:65], v[160:163], v[192:195], v[62:65]
	v_mfma_f32_16x16x32_bf16 v[58:61], v[168:171], v[192:195], v[58:61]
	v_mfma_f32_16x16x32_bf16 v[46:49], v[160:163], v[200:203], v[46:49]
	v_mfma_f32_16x16x32_bf16 v[42:45], v[168:171], v[200:203], v[42:45]
	v_mfma_f32_16x16x32_bf16 v[30:33], v[160:163], v[208:211], v[30:33]
	v_mfma_f32_16x16x32_bf16 v[26:29], v[168:171], v[208:211], v[26:29]
	v_mfma_f32_16x16x32_bf16 v[14:17], v[160:163], v[216:219], v[14:17]
	v_mfma_f32_16x16x32_bf16 v[10:13], v[168:171], v[216:219], v[10:13]
	v_mfma_f32_16x16x32_bf16 v[62:65], v[164:167], v[196:199], v[62:65]
	v_mfma_f32_16x16x32_bf16 v[58:61], v[172:175], v[196:199], v[58:61]
	v_mfma_f32_16x16x32_bf16 v[46:49], v[164:167], v[204:207], v[46:49]
	v_mfma_f32_16x16x32_bf16 v[42:45], v[172:175], v[204:207], v[42:45]
	v_mfma_f32_16x16x32_bf16 v[30:33], v[164:167], v[212:215], v[30:33]
	v_mfma_f32_16x16x32_bf16 v[26:29], v[172:175], v[212:215], v[26:29]
	v_mfma_f32_16x16x32_bf16 v[14:17], v[164:167], v[220:223], v[14:17]
	v_mfma_f32_16x16x32_bf16 v[10:13], v[172:175], v[220:223], v[10:13]
	s_setprio 0
	s_setprio 1
	v_mfma_f32_16x16x32_bf16 v[54:57], v[176:179], v[192:195], v[54:57]
	v_mfma_f32_16x16x32_bf16 v[50:53], v[184:187], v[192:195], v[50:53]
	v_mfma_f32_16x16x32_bf16 v[38:41], v[176:179], v[200:203], v[38:41]
	v_mfma_f32_16x16x32_bf16 v[34:37], v[184:187], v[200:203], v[34:37]
	v_mfma_f32_16x16x32_bf16 v[22:25], v[176:179], v[208:211], v[22:25]
	v_mfma_f32_16x16x32_bf16 v[18:21], v[184:187], v[208:211], v[18:21]
	v_mfma_f32_16x16x32_bf16 v[6:9], v[176:179], v[216:219], v[6:9]
	v_mfma_f32_16x16x32_bf16 v[2:5], v[184:187], v[216:219], v[2:5]
	v_mfma_f32_16x16x32_bf16 v[54:57], v[180:183], v[196:199], v[54:57]
	v_mfma_f32_16x16x32_bf16 v[50:53], v[188:191], v[196:199], v[50:53]
	v_mfma_f32_16x16x32_bf16 v[38:41], v[180:183], v[204:207], v[38:41]
	v_mfma_f32_16x16x32_bf16 v[34:37], v[188:191], v[204:207], v[34:37]
	v_mfma_f32_16x16x32_bf16 v[22:25], v[180:183], v[212:215], v[22:25]
	v_mfma_f32_16x16x32_bf16 v[18:21], v[188:191], v[212:215], v[18:21]
	v_mfma_f32_16x16x32_bf16 v[6:9], v[180:183], v[220:223], v[6:9]
	v_mfma_f32_16x16x32_bf16 v[2:5], v[188:191], v[220:223], v[2:5]
	s_setprio 0
	s_barrier
	s_mov_b32 m0, s4
	v_lshl_add_u64 v[230:231], s[46:47], 0, v[134:135]
	global_load_lds_dwordx4 v134, s[46:47]
	s_mov_b32 m0, s5
	s_nop 0
	global_load_lds_dwordx4 v[224:225], off
	ds_read_b128 v[160:163], v153
	ds_read_b128 v[164:167], v153 offset:1024
	ds_read_b128 v[168:171], v153 offset:2048
	ds_read_b128 v[172:175], v153 offset:3072
	ds_read_b128 v[176:179], v154
	ds_read_b128 v[180:183], v154 offset:1024
	ds_read_b128 v[184:187], v154 offset:2048
	ds_read_b128 v[188:191], v154 offset:3072
	s_mov_b32 m0, s33
	ds_read_b128 v[192:195], v152 offset:32768
	ds_read_b128 v[196:199], v152 offset:33792
	ds_read_b128 v[200:203], v152 offset:34816
	ds_read_b128 v[204:207], v152 offset:35840
	ds_read_b128 v[208:211], v152 offset:36864
	ds_read_b128 v[212:215], v152 offset:37888
	ds_read_b128 v[216:219], v152 offset:38912
	ds_read_b128 v[220:223], v152 offset:39936
	global_load_lds_dwordx4 v137, s[46:47]
	s_mov_b32 m0, s41
	s_nop 0
	global_load_lds_dwordx4 v139, s[46:47]
	s_waitcnt vmcnt(8)
	s_waitcnt lgkmcnt(0)
	s_barrier
	s_setprio 1
	s_waitcnt lgkmcnt(0)
	v_mfma_f32_16x16x32_bf16 v[126:129], v[160:163], v[192:195], v[126:129]
	v_mfma_f32_16x16x32_bf16 v[122:125], v[168:171], v[192:195], v[122:125]
	v_mfma_f32_16x16x32_bf16 v[110:113], v[160:163], v[200:203], v[110:113]
	v_mfma_f32_16x16x32_bf16 v[106:109], v[168:171], v[200:203], v[106:109]
	v_mfma_f32_16x16x32_bf16 v[94:97], v[160:163], v[208:211], v[94:97]
	v_mfma_f32_16x16x32_bf16 v[90:93], v[168:171], v[208:211], v[90:93]
	v_mfma_f32_16x16x32_bf16 v[78:81], v[160:163], v[216:219], v[78:81]
	v_mfma_f32_16x16x32_bf16 v[74:77], v[168:171], v[216:219], v[74:77]
	v_mfma_f32_16x16x32_bf16 v[126:129], v[164:167], v[196:199], v[126:129]
	v_mfma_f32_16x16x32_bf16 v[122:125], v[172:175], v[196:199], v[122:125]
	v_mfma_f32_16x16x32_bf16 v[110:113], v[164:167], v[204:207], v[110:113]
	v_mfma_f32_16x16x32_bf16 v[106:109], v[172:175], v[204:207], v[106:109]
	v_mfma_f32_16x16x32_bf16 v[94:97], v[164:167], v[212:215], v[94:97]
	v_mfma_f32_16x16x32_bf16 v[90:93], v[172:175], v[212:215], v[90:93]
	v_mfma_f32_16x16x32_bf16 v[78:81], v[164:167], v[220:223], v[78:81]
	v_mfma_f32_16x16x32_bf16 v[74:77], v[172:175], v[220:223], v[74:77]
	s_setprio 0
	s_setprio 1
	v_mfma_f32_16x16x32_bf16 v[118:121], v[176:179], v[192:195], v[118:121]
	v_mfma_f32_16x16x32_bf16 v[114:117], v[184:187], v[192:195], v[114:117]
	v_mfma_f32_16x16x32_bf16 v[102:105], v[176:179], v[200:203], v[102:105]
	v_mfma_f32_16x16x32_bf16 v[98:101], v[184:187], v[200:203], v[98:101]
	v_mfma_f32_16x16x32_bf16 v[86:89], v[176:179], v[208:211], v[86:89]
	v_mfma_f32_16x16x32_bf16 v[82:85], v[184:187], v[208:211], v[82:85]
	v_mfma_f32_16x16x32_bf16 v[70:73], v[176:179], v[216:219], v[70:73]
	v_mfma_f32_16x16x32_bf16 v[66:69], v[184:187], v[216:219], v[66:69]
	v_mfma_f32_16x16x32_bf16 v[118:121], v[180:183], v[196:199], v[118:121]
	v_mfma_f32_16x16x32_bf16 v[114:117], v[188:191], v[196:199], v[114:117]
	v_mfma_f32_16x16x32_bf16 v[102:105], v[180:183], v[204:207], v[102:105]
	v_mfma_f32_16x16x32_bf16 v[98:101], v[188:191], v[204:207], v[98:101]
	v_mfma_f32_16x16x32_bf16 v[86:89], v[180:183], v[212:215], v[86:89]
	v_mfma_f32_16x16x32_bf16 v[82:85], v[188:191], v[212:215], v[82:85]
	v_mfma_f32_16x16x32_bf16 v[70:73], v[180:183], v[220:223], v[70:73]
	v_mfma_f32_16x16x32_bf16 v[66:69], v[188:191], v[220:223], v[66:69]
	s_setprio 0
	s_barrier
	s_add_i32 s46, s58, s3
	v_lshl_add_u64 v[226:227], v[226:227], 0, s[30:31]
	s_mov_b32 m0, s46
	ds_read_b128 v[192:195], v152 offset:49152
	ds_read_b128 v[196:199], v152 offset:50176
	ds_read_b128 v[200:203], v152 offset:51200
	ds_read_b128 v[204:207], v152 offset:52224
	ds_read_b128 v[208:211], v152 offset:53248
	ds_read_b128 v[212:215], v152 offset:54272
	ds_read_b128 v[216:219], v152 offset:55296
	ds_read_b128 v[220:223], v152 offset:56320
	global_load_lds_dwordx4 v[226:227], off
	s_add_i32 m0, s46, 0x2000
	s_add_u32 s44, s44, 0x80080
	v_lshl_add_u64 v[226:227], v[228:229], 0, s[30:31]
	s_addc_u32 s45, s45, 0
	s_add_i32 s46, s59, s3
	global_load_lds_dwordx4 v[226:227], off
	v_lshl_add_u64 v[226:227], s[44:45], 0, v[132:133]
	s_mov_b32 m0, s46
	v_lshl_add_u64 v[224:225], v[224:225], 0, s[30:31]
	global_load_lds_dwordx4 v[226:227], off
	v_lshl_add_u64 v[226:227], s[44:45], 0, v[130:131]
	s_add_i32 m0, s46, 0x2000
	s_nop 0
	global_load_lds_dwordx4 v[226:227], off
	v_lshl_add_u64 v[240:241], v[230:231], 0, s[30:31]
	v_mov_b32_e32 v242, v224
	v_mov_b32_e32 v243, v225
	s_waitcnt vmcnt(6)
	s_waitcnt lgkmcnt(0)
	s_barrier
	s_setprio 1
	s_waitcnt lgkmcnt(0)
	v_mfma_f32_16x16x32_bf16 v[62:65], v[160:163], v[192:195], v[62:65]
	v_mfma_f32_16x16x32_bf16 v[58:61], v[168:171], v[192:195], v[58:61]
	v_mfma_f32_16x16x32_bf16 v[46:49], v[160:163], v[200:203], v[46:49]
	v_mfma_f32_16x16x32_bf16 v[42:45], v[168:171], v[200:203], v[42:45]
	v_mfma_f32_16x16x32_bf16 v[30:33], v[160:163], v[208:211], v[30:33]
	v_mfma_f32_16x16x32_bf16 v[26:29], v[168:171], v[208:211], v[26:29]
	v_mfma_f32_16x16x32_bf16 v[14:17], v[160:163], v[216:219], v[14:17]
	v_mfma_f32_16x16x32_bf16 v[10:13], v[168:171], v[216:219], v[10:13]
	v_mfma_f32_16x16x32_bf16 v[62:65], v[164:167], v[196:199], v[62:65]
	v_mfma_f32_16x16x32_bf16 v[58:61], v[172:175], v[196:199], v[58:61]
	v_mfma_f32_16x16x32_bf16 v[46:49], v[164:167], v[204:207], v[46:49]
	v_mfma_f32_16x16x32_bf16 v[42:45], v[172:175], v[204:207], v[42:45]
	v_mfma_f32_16x16x32_bf16 v[30:33], v[164:167], v[212:215], v[30:33]
	v_mfma_f32_16x16x32_bf16 v[26:29], v[172:175], v[212:215], v[26:29]
	v_mfma_f32_16x16x32_bf16 v[14:17], v[164:167], v[220:223], v[14:17]
	v_mfma_f32_16x16x32_bf16 v[10:13], v[172:175], v[220:223], v[10:13]
	s_setprio 0
	s_setprio 1
	v_mfma_f32_16x16x32_bf16 v[54:57], v[176:179], v[192:195], v[54:57]
	v_mfma_f32_16x16x32_bf16 v[50:53], v[184:187], v[192:195], v[50:53]
	v_mfma_f32_16x16x32_bf16 v[38:41], v[176:179], v[200:203], v[38:41]
	v_mfma_f32_16x16x32_bf16 v[34:37], v[184:187], v[200:203], v[34:37]
	v_mfma_f32_16x16x32_bf16 v[22:25], v[176:179], v[208:211], v[22:25]
	v_mfma_f32_16x16x32_bf16 v[18:21], v[184:187], v[208:211], v[18:21]
	v_mfma_f32_16x16x32_bf16 v[6:9], v[176:179], v[216:219], v[6:9]
	v_mfma_f32_16x16x32_bf16 v[2:5], v[184:187], v[216:219], v[2:5]
	v_mfma_f32_16x16x32_bf16 v[54:57], v[180:183], v[196:199], v[54:57]
	v_mfma_f32_16x16x32_bf16 v[50:53], v[188:191], v[196:199], v[50:53]
	v_mfma_f32_16x16x32_bf16 v[38:41], v[180:183], v[204:207], v[38:41]
	v_mfma_f32_16x16x32_bf16 v[34:37], v[188:191], v[204:207], v[34:37]
	v_mfma_f32_16x16x32_bf16 v[22:25], v[180:183], v[212:215], v[22:25]
	v_mfma_f32_16x16x32_bf16 v[18:21], v[188:191], v[212:215], v[18:21]
	v_mfma_f32_16x16x32_bf16 v[6:9], v[180:183], v[220:223], v[6:9]
	v_mfma_f32_16x16x32_bf16 v[2:5], v[188:191], v[220:223], v[2:5]
	s_setprio 0
	s_barrier
	s_mov_b32 s99, 1
	s_add_i32 s68, s68, 2
	s_add_u32 s42, s42, 0x100
	s_addc_u32 s43, s43, 0
	s_cmp_gt_u32 s68, 29
	s_cbranch_scc0 .LBB0_2096
	s_and_b64 vcc, exec, s[34:35]
	s_cbranch_vccz .LBB0_2099
	s_barrier

.LBB0_2214:
	s_mov_b32 s99, 0
	v_readlane_b32 s0, v253, 11
	v_readlane_b32 s1, v253, 12
	s_mov_b32 s3, s1
	s_cmp_lt_i32 s0, 24
	s_cselect_b64 s[0:1], -1, 0
	s_cmp_gt_i32 s3, 23
	s_cselect_b64 s[4:5], -1, 0
	s_and_b64 s[0:1], s[0:1], s[4:5]
	s_andn2_b64 vcc, exec, s[0:1]
	s_cbranch_vccnz .LBB0_2235
	v_readlane_b32 s6, v253, 0
	v_readlane_b32 s7, v253, 1
	v_mov_b32_e32 v10, v0
	s_cmpk_gt_i32 s2, 0x3ff
	s_nop 0
	v_readfirstlane_b32 s16, v10
	s_cbranch_scc1 .LBB0_2235
	v_lshlrev_b32_e32 v1, 4, v10
	v_add_u32_e32 v2, 0x2000, v1
	v_ashrrev_i32_e32 v3, 31, v2
	v_lshrrev_b32_e32 v3, 22, v3
	v_add_u32_e32 v3, v2, v3
	v_ashrrev_i32_e32 v11, 10, v3
	v_mul_i32_i24_e32 v3, 0x400, v11
	v_sub_u32_e32 v2, v2, v3
	v_lshrrev_b32_e32 v3, 4, v2
	v_bitop3_b32 v2, v3, v2, 32 bitop3:0x6c
	v_ashrrev_i32_e32 v3, 31, v2
	s_load_dwordx2 s[6:7], s[6:7], 0xd0
	v_lshrrev_b32_e32 v3, 26, v3
	v_add_u32_e32 v3, v2, v3
	v_lshlrev_b32_e32 v4, 3, v11
	v_ashrrev_i32_e32 v12, 6, v3
	v_and_b32_e32 v4, -16, v4
	v_add_u32_e32 v4, v12, v4
	v_and_b32_e32 v5, 3, v12
	s_mov_b32 s12, 0x1ffffe0
	v_lshrrev_b32_e32 v6, 2, v4
	v_lshlrev_b32_e32 v7, 1, v4
	v_and_b32_e32 v3, 0xc0, v3
	s_waitcnt lgkmcnt(0)
	s_add_u32 s0, s6, 0x3a300000
	v_and_or_b32 v5, v4, s12, v5
	v_and_b32_e32 v6, 4, v6
	v_and_b32_e32 v7, 24, v7
	v_sub_u32_e32 v2, v2, v3
	v_mov_b32_e32 v3, 1
	s_addc_u32 s1, s7, 0
	v_or3_b32 v5, v5, v6, v7
	v_lshlrev_b32_e32 v6, 5, v11
	v_ashrrev_i16_sdwa v2, v3, sext(v2) dst_sel:DWORD dst_unused:UNUSED_PAD src0_sel:DWORD src1_sel:BYTE_0
	s_add_u32 s3, s6, 0x1f800000
	s_movk_i32 s19, 0x580
	v_and_b32_e32 v13, 32, v6
	v_bfe_i32 v14, v2, 0, 16
	s_addc_u32 s4, s7, 0
	s_lshl_b32 s5, s2, 7
	v_mul_lo_u32 v5, v5, s19
	v_add_u32_e32 v2, v13, v14
	v_mul_lo_u32 v4, v4, s19
	s_ashr_i32 s8, s2, 3
	s_and_b32 s5, s5, 0x380
	v_add_lshl_u32 v130, v5, v2, 1
	v_add_lshl_u32 v132, v2, v4, 1
	v_bfe_i32 v2, v10, 27, 1
	s_add_i32 s5, s5, s8
	v_lshrrev_b32_e32 v2, 22, v2
	s_ashr_i32 s8, s5, 31
	v_add_u32_e32 v2, v1, v2
	s_lshr_b32 s8, s8, 26
	v_and_b32_e32 v2, 0xfffffc00, v2
	s_add_i32 s8, s5, s8
	v_sub_u32_e32 v1, v1, v2
	s_ashr_i32 s9, s8, 6
	s_andn2_b32 s8, s8, 63
	v_lshrrev_b32_e32 v2, 4, v1
	s_sub_i32 s5, s5, s8
	v_bitop3_b32 v2, v2, v1, 32 bitop3:0x6c
	v_ashrrev_i32_e32 v1, 31, v1
	s_ashr_i32 s10, s5, 31
	v_lshrrev_b32_e32 v1, 26, v1
	s_lshr_b32 s10, s10, 29
	v_add_u32_e32 v1, v2, v1
	s_add_i32 s10, s5, s10
	v_ashrrev_i32_e32 v15, 6, v1
	v_ashrrev_i32_e32 v1, 31, v10
	s_mul_i32 s8, s9, 9
	s_ashr_i32 s10, s10, 3
	v_lshrrev_b32_e32 v1, 26, v1
	s_add_i32 s54, s10, s8
	s_sub_i32 s8, s9, s10
	v_add_u32_e32 v1, v10, v1
	s_lshl_b32 s8, s8, 3
	v_ashrrev_i32_e32 v16, 6, v1
	s_add_i32 s55, s8, s5
	v_lshlrev_b32_e32 v1, 3, v16
	s_mul_i32 s10, s55, 0xb0000
	v_and_b32_e32 v1, -16, v1
	s_mul_hi_i32 s9, s55, 0xb0000
	s_add_u32 s34, s3, s10
	v_add_u32_e32 v1, v15, v1
	s_mul_i32 s8, s54, 0xb0000
	s_addc_u32 s35, s4, s9
	v_and_b32_e32 v4, 3, v15
	v_lshrrev_b32_e32 v5, 2, v1
	v_lshlrev_b32_e32 v6, 1, v1
	s_mul_hi_i32 s5, s54, 0xb0000
	s_add_u32 s30, s0, s8
	v_and_or_b32 v4, v1, s12, v4
	v_and_b32_e32 v5, 4, v5
	v_and_b32_e32 v6, 24, v6
	s_addc_u32 s31, s1, s5
	s_ashr_i32 s17, s16, 6
	v_or3_b32 v4, v4, v5, v6
	v_lshlrev_b32_e32 v5, 5, v16
	s_ashr_i32 s18, s16, 8
	s_lshl_b32 s5, s17, 10
	v_and_b32_e32 v17, 32, v5
	v_mul_i32_i24_e32 v5, 64, v15
	s_add_u32 s8, s30, 0x58000
	v_sub_u32_e32 v2, v2, v5
	s_addc_u32 s9, s31, 0
	v_ashrrev_i16_sdwa v2, v3, sext(v2) dst_sel:DWORD dst_unused:UNUSED_PAD src0_sel:DWORD src1_sel:BYTE_0
	s_add_u32 s10, s34, 0x58000
	v_bfe_i32 v18, v2, 0, 16
	s_addc_u32 s11, s35, 0
	v_mul_lo_u32 v4, v4, s19
	v_add_u32_e32 v2, v17, v18
	s_add_i32 s33, s5, 0
	v_add_lshl_u32 v134, v4, v2, 1
	s_add_i32 m0, s33, 0x10000
	v_mul_lo_u32 v1, v1, s19
	global_load_lds_dwordx4 v134, s[34:35]
	s_add_i32 m0, s33, 0x12000
	v_add_lshl_u32 v136, v2, v1, 1
	global_load_lds_dwordx4 v130, s[34:35]
	s_add_i32 m0, s33, 0x14000
	s_add_i32 s40, s33, 0x2000
	global_load_lds_dwordx4 v134, s[10:11]
	s_add_i32 m0, s33, 0x16000
	s_add_i32 s41, s33, 0x4000
	global_load_lds_dwordx4 v130, s[10:11]
	s_mov_b32 m0, s33
	s_add_i32 s42, s33, 0x6000
	global_load_lds_dwordx4 v136, s[30:31]
	s_mov_b32 m0, s40
	v_mov_b32_e32 v135, 0
	global_load_lds_dwordx4 v132, s[30:31]
	s_mov_b32 m0, s41
	v_mov_b32_e32 v131, v135
	global_load_lds_dwordx4 v136, s[8:9]
	s_mov_b32 m0, s42
	v_mov_b32_e32 v137, v135
	global_load_lds_dwordx4 v132, s[8:9]
	v_mov_b32_e32 v133, v135
	s_cmp_eq_u32 s18, 1
	s_mov_b32 s43, 0xb0000
	s_mov_b32 s44, 0
	v_lshl_add_u64 v[8:9], s[34:35], 0, v[134:135]
	v_lshl_add_u64 v[6:7], s[34:35], 0, v[130:131]
	v_lshl_add_u64 v[2:3], s[30:31], 0, v[136:137]
	s_cselect_b64 s[8:9], -1, 0
	s_cmp_lg_u32 s18, 1
	v_lshl_add_u64 v[4:5], s[30:31], 0, v[132:133]
	s_cbranch_scc1 .LBB0_2218
	s_barrier

.LBB0_2228:
	s_cmp_eq_u32 s99, 0
	s_cbranch_scc1 .Lbal_skip_2228
	s_mov_b32 m0, s45
	s_nop 0
	global_load_lds_dwordx4 v[240:241], off
	s_mov_b32 m0, s46
	s_nop 0
	global_load_lds_dwordx4 v[242:243], off
.Lbal_skip_2228:
	ds_read_b128 v[142:145], v148
	ds_read_b128 v[152:155], v148 offset:1024
	ds_read_b128 v[156:159], v148 offset:2048
	ds_read_b128 v[160:163], v148 offset:3072
	ds_read_b128 v[164:167], v149
	ds_read_b128 v[168:171], v149 offset:1024
	ds_read_b128 v[172:175], v149 offset:2048
	ds_read_b128 v[176:179], v149 offset:3072
	s_add_u32 s34, s30, 0x100
	s_addc_u32 s35, s31, 0
	s_cmp_eq_u32 s58, 18
	s_cselect_b32 s39, s27, s35
	s_cselect_b32 s38, s26, s34
	s_cselect_b32 s37, s29, s57
	s_cselect_b32 s36, s28, s56
	v_lshl_add_u64 v[212:213], s[30:31], 0, v[138:139]
	s_add_i32 m0, s33, 0xc000
	ds_read_b128 v[180:183], v150
	ds_read_b128 v[184:187], v150 offset:1024
	ds_read_b128 v[188:191], v150 offset:2048
	ds_read_b128 v[192:195], v150 offset:3072
	ds_read_b128 v[196:199], v150 offset:4096
	ds_read_b128 v[200:203], v150 offset:5120
	ds_read_b128 v[204:207], v150 offset:6144
	ds_read_b128 v[208:211], v150 offset:7168
	global_load_lds_dwordx4 v[212:213], off
	v_lshl_add_u64 v[212:213], s[30:31], 0, v[140:141]
	s_add_i32 m0, s33, 0xe000
	s_nop 0
	global_load_lds_dwordx4 v[212:213], off
	s_waitcnt vmcnt(8)
	s_waitcnt lgkmcnt(0)
	s_barrier
	s_setprio 1
	s_waitcnt lgkmcnt(0)
	v_mfma_f32_16x16x32_bf16 v[126:129], v[142:145], v[180:183], v[126:129]
	v_mfma_f32_16x16x32_bf16 v[122:125], v[156:159], v[180:183], v[122:125]
	v_mfma_f32_16x16x32_bf16 v[110:113], v[142:145], v[188:191], v[110:113]
	v_mfma_f32_16x16x32_bf16 v[106:109], v[156:159], v[188:191], v[106:109]
	v_mfma_f32_16x16x32_bf16 v[94:97], v[142:145], v[196:199], v[94:97]
	v_mfma_f32_16x16x32_bf16 v[90:93], v[156:159], v[196:199], v[90:93]
	v_mfma_f32_16x16x32_bf16 v[86:89], v[142:145], v[204:207], v[86:89]
	v_mfma_f32_16x16x32_bf16 v[78:81], v[156:159], v[204:207], v[78:81]
	v_mfma_f32_16x16x32_bf16 v[126:129], v[152:155], v[184:187], v[126:129]
	v_mfma_f32_16x16x32_bf16 v[122:125], v[160:163], v[184:187], v[122:125]
	v_mfma_f32_16x16x32_bf16 v[110:113], v[152:155], v[192:195], v[110:113]
	v_mfma_f32_16x16x32_bf16 v[106:109], v[160:163], v[192:195], v[106:109]
	v_mfma_f32_16x16x32_bf16 v[94:97], v[152:155], v[200:203], v[94:97]
	v_mfma_f32_16x16x32_bf16 v[90:93], v[160:163], v[200:203], v[90:93]
	v_mfma_f32_16x16x32_bf16 v[86:89], v[152:155], v[208:211], v[86:89]
	v_mfma_f32_16x16x32_bf16 v[78:81], v[160:163], v[208:211], v[78:81]
	s_setprio 0
	s_setprio 1
	v_mfma_f32_16x16x32_bf16 v[118:121], v[164:167], v[180:183], v[118:121]
	v_mfma_f32_16x16x32_bf16 v[114:117], v[172:175], v[180:183], v[114:117]
	v_mfma_f32_16x16x32_bf16 v[102:105], v[164:167], v[188:191], v[102:105]
	v_mfma_f32_16x16x32_bf16 v[98:101], v[172:175], v[188:191], v[98:101]
	v_mfma_f32_16x16x32_bf16 v[82:85], v[164:167], v[196:199], v[82:85]
	v_mfma_f32_16x16x32_bf16 v[74:77], v[172:175], v[196:199], v[74:77]
	v_mfma_f32_16x16x32_bf16 v[70:73], v[164:167], v[204:207], v[70:73]
	v_mfma_f32_16x16x32_bf16 v[66:69], v[172:175], v[204:207], v[66:69]
	v_mfma_f32_16x16x32_bf16 v[118:121], v[168:171], v[184:187], v[118:121]
	v_mfma_f32_16x16x32_bf16 v[114:117], v[176:179], v[184:187], v[114:117]
	v_mfma_f32_16x16x32_bf16 v[102:105], v[168:171], v[192:195], v[102:105]
	v_mfma_f32_16x16x32_bf16 v[98:101], v[176:179], v[192:195], v[98:101]
	v_mfma_f32_16x16x32_bf16 v[82:85], v[168:171], v[200:203], v[82:85]
	v_mfma_f32_16x16x32_bf16 v[74:77], v[176:179], v[200:203], v[74:77]
	v_mfma_f32_16x16x32_bf16 v[70:73], v[168:171], v[208:211], v[70:73]
	v_mfma_f32_16x16x32_bf16 v[66:69], v[176:179], v[208:211], v[66:69]
	s_setprio 0
	s_barrier
	s_add_i32 s30, s47, s5
	v_lshl_add_u64 v[212:213], s[36:37], 0, v[134:135]
	s_mov_b32 m0, s30
	ds_read_b128 v[180:183], v150 offset:16384
	ds_read_b128 v[184:187], v150 offset:17408
	ds_read_b128 v[188:191], v150 offset:18432
	ds_read_b128 v[192:195], v150 offset:19456
	ds_read_b128 v[196:199], v150 offset:20480
	ds_read_b128 v[200:203], v150 offset:21504
	ds_read_b128 v[204:207], v150 offset:22528
	ds_read_b128 v[208:211], v150 offset:23552
	global_load_lds_dwordx4 v[212:213], off
	s_add_i32 m0, s30, 0x2000
	s_add_u32 s30, s36, 0x58000
	v_lshl_add_u64 v[214:215], s[36:37], 0, v[130:131]
	s_addc_u32 s31, s37, 0
	s_add_i32 s59, s48, s5
	global_load_lds_dwordx4 v[214:215], off
	v_lshl_add_u64 v[216:217], s[30:31], 0, v[134:135]
	s_mov_b32 m0, s59
	v_lshl_add_u64 v[218:219], s[38:39], 0, v[132:133]
	global_load_lds_dwordx4 v[216:217], off
	v_lshl_add_u64 v[216:217], s[30:31], 0, v[130:131]
	s_add_i32 m0, s59, 0x2000
	s_nop 0
	global_load_lds_dwordx4 v[216:217], off
	s_waitcnt vmcnt(6)
	s_waitcnt lgkmcnt(0)
	s_barrier
	s_setprio 1
	s_waitcnt lgkmcnt(0)
	v_mfma_f32_16x16x32_bf16 v[62:65], v[142:145], v[180:183], v[62:65]
	v_mfma_f32_16x16x32_bf16 v[58:61], v[156:159], v[180:183], v[58:61]
	v_mfma_f32_16x16x32_bf16 v[46:49], v[142:145], v[188:191], v[46:49]
	v_mfma_f32_16x16x32_bf16 v[42:45], v[156:159], v[188:191], v[42:45]
	v_mfma_f32_16x16x32_bf16 v[30:33], v[142:145], v[196:199], v[30:33]
	v_mfma_f32_16x16x32_bf16 v[26:29], v[156:159], v[196:199], v[26:29]
	v_mfma_f32_16x16x32_bf16 v[14:17], v[142:145], v[204:207], v[14:17]
	v_mfma_f32_16x16x32_bf16 v[10:13], v[156:159], v[204:207], v[10:13]
	v_mfma_f32_16x16x32_bf16 v[62:65], v[152:155], v[184:187], v[62:65]
	v_mfma_f32_16x16x32_bf16 v[58:61], v[160:163], v[184:187], v[58:61]
	v_mfma_f32_16x16x32_bf16 v[46:49], v[152:155], v[192:195], v[46:49]
	v_mfma_f32_16x16x32_bf16 v[42:45], v[160:163], v[192:195], v[42:45]
	v_mfma_f32_16x16x32_bf16 v[30:33], v[152:155], v[200:203], v[30:33]
	v_mfma_f32_16x16x32_bf16 v[26:29], v[160:163], v[200:203], v[26:29]
	v_mfma_f32_16x16x32_bf16 v[14:17], v[152:155], v[208:211], v[14:17]
	v_mfma_f32_16x16x32_bf16 v[10:13], v[160:163], v[208:211], v[10:13]
	s_setprio 0
	s_setprio 1
	v_mfma_f32_16x16x32_bf16 v[54:57], v[164:167], v[180:183], v[54:57]
	v_mfma_f32_16x16x32_bf16 v[50:53], v[172:175], v[180:183], v[50:53]
	v_mfma_f32_16x16x32_bf16 v[38:41], v[164:167], v[188:191], v[38:41]
	v_mfma_f32_16x16x32_bf16 v[34:37], v[172:175], v[188:191], v[34:37]
	v_mfma_f32_16x16x32_bf16 v[22:25], v[164:167], v[196:199], v[22:25]
	v_mfma_f32_16x16x32_bf16 v[18:21], v[172:175], v[196:199], v[18:21]
	v_mfma_f32_16x16x32_bf16 v[6:9], v[164:167], v[204:207], v[6:9]
	v_mfma_f32_16x16x32_bf16 v[2:5], v[172:175], v[204:207], v[2:5]
	v_mfma_f32_16x16x32_bf16 v[54:57], v[168:171], v[184:187], v[54:57]
	v_mfma_f32_16x16x32_bf16 v[50:53], v[176:179], v[184:187], v[50:53]
	v_mfma_f32_16x16x32_bf16 v[38:41], v[168:171], v[192:195], v[38:41]
	v_mfma_f32_16x16x32_bf16 v[34:37], v[176:179], v[192:195], v[34:37]
	v_mfma_f32_16x16x32_bf16 v[22:25], v[168:171], v[200:203], v[22:25]
	v_mfma_f32_16x16x32_bf16 v[18:21], v[176:179], v[200:203], v[18:21]
	v_mfma_f32_16x16x32_bf16 v[6:9], v[168:171], v[208:211], v[6:9]
	v_mfma_f32_16x16x32_bf16 v[2:5], v[176:179], v[208:211], v[2:5]
	s_setprio 0
	s_barrier
	v_lshl_add_u64 v[216:217], s[38:39], 0, v[136:137]
	s_mov_b32 m0, s33
	s_nop 0
	global_load_lds_dwordx4 v[216:217], off
	s_mov_b32 m0, s40
	s_nop 0
	global_load_lds_dwordx4 v[218:219], off
	s_add_i32 s59, 0, 0x18000
	v_add_u32_e32 v151, s59, v146
	s_add_i32 s61, 0, 0x1c000
	ds_read_b128 v[142:145], v151
	ds_read_b128 v[152:155], v151 offset:1024
	ds_read_b128 v[156:159], v151 offset:2048
	ds_read_b128 v[160:163], v151 offset:3072
	v_add_u32_e32 v151, s61, v146
	ds_read_b128 v[164:167], v151
	ds_read_b128 v[168:171], v151 offset:1024
	ds_read_b128 v[172:175], v151 offset:2048
	ds_read_b128 v[176:179], v151 offset:3072
	s_add_u32 s30, s38, 0x58000
	s_addc_u32 s31, s39, 0
	s_mov_b32 m0, s41
	v_lshl_add_u64 v[220:221], s[30:31], 0, v[136:137]
	ds_read_b128 v[180:183], v150 offset:32768
	ds_read_b128 v[184:187], v150 offset:33792
	ds_read_b128 v[188:191], v150 offset:34816
	ds_read_b128 v[192:195], v150 offset:35840
	ds_read_b128 v[196:199], v150 offset:36864
	ds_read_b128 v[200:203], v150 offset:37888
	ds_read_b128 v[204:207], v150 offset:38912
	ds_read_b128 v[208:211], v150 offset:39936
	global_load_lds_dwordx4 v[220:221], off
	v_lshl_add_u64 v[220:221], s[30:31], 0, v[132:133]
	s_mov_b32 m0, s42
	s_nop 0
	global_load_lds_dwordx4 v[220:221], off
	s_waitcnt vmcnt(8)
	s_waitcnt lgkmcnt(0)
	s_barrier
	s_setprio 1
	s_waitcnt lgkmcnt(0)
	v_mfma_f32_16x16x32_bf16 v[126:129], v[142:145], v[180:183], v[126:129]
	v_mfma_f32_16x16x32_bf16 v[122:125], v[156:159], v[180:183], v[122:125]
	v_mfma_f32_16x16x32_bf16 v[110:113], v[142:145], v[188:191], v[110:113]
	v_mfma_f32_16x16x32_bf16 v[106:109], v[156:159], v[188:191], v[106:109]
	v_mfma_f32_16x16x32_bf16 v[94:97], v[142:145], v[196:199], v[94:97]
	v_mfma_f32_16x16x32_bf16 v[90:93], v[156:159], v[196:199], v[90:93]
	v_mfma_f32_16x16x32_bf16 v[86:89], v[142:145], v[204:207], v[86:89]
	v_mfma_f32_16x16x32_bf16 v[78:81], v[156:159], v[204:207], v[78:81]
	v_mfma_f32_16x16x32_bf16 v[126:129], v[152:155], v[184:187], v[126:129]
	v_mfma_f32_16x16x32_bf16 v[122:125], v[160:163], v[184:187], v[122:125]
	v_mfma_f32_16x16x32_bf16 v[110:113], v[152:155], v[192:195], v[110:113]
	v_mfma_f32_16x16x32_bf16 v[106:109], v[160:163], v[192:195], v[106:109]
	v_mfma_f32_16x16x32_bf16 v[94:97], v[152:155], v[200:203], v[94:97]
	v_mfma_f32_16x16x32_bf16 v[90:93], v[160:163], v[200:203], v[90:93]
	v_mfma_f32_16x16x32_bf16 v[86:89], v[152:155], v[208:211], v[86:89]
	v_mfma_f32_16x16x32_bf16 v[78:81], v[160:163], v[208:211], v[78:81]
	s_setprio 0
	s_setprio 1
	v_mfma_f32_16x16x32_bf16 v[118:121], v[164:167], v[180:183], v[118:121]
	v_mfma_f32_16x16x32_bf16 v[114:117], v[172:175], v[180:183], v[114:117]
	v_mfma_f32_16x16x32_bf16 v[102:105], v[164:167], v[188:191], v[102:105]
	v_mfma_f32_16x16x32_bf16 v[98:101], v[172:175], v[188:191], v[98:101]
	v_mfma_f32_16x16x32_bf16 v[82:85], v[164:167], v[196:199], v[82:85]
	v_mfma_f32_16x16x32_bf16 v[74:77], v[172:175], v[196:199], v[74:77]
	v_mfma_f32_16x16x32_bf16 v[70:73], v[164:167], v[204:207], v[70:73]
	v_mfma_f32_16x16x32_bf16 v[66:69], v[172:175], v[204:207], v[66:69]
	v_mfma_f32_16x16x32_bf16 v[118:121], v[168:171], v[184:187], v[118:121]
	v_mfma_f32_16x16x32_bf16 v[114:117], v[176:179], v[184:187], v[114:117]
	v_mfma_f32_16x16x32_bf16 v[102:105], v[168:171], v[192:195], v[102:105]
	v_mfma_f32_16x16x32_bf16 v[98:101], v[176:179], v[192:195], v[98:101]
	v_mfma_f32_16x16x32_bf16 v[82:85], v[168:171], v[200:203], v[82:85]
	v_mfma_f32_16x16x32_bf16 v[74:77], v[176:179], v[200:203], v[74:77]
	v_mfma_f32_16x16x32_bf16 v[70:73], v[168:171], v[208:211], v[70:73]
	v_mfma_f32_16x16x32_bf16 v[66:69], v[176:179], v[208:211], v[66:69]
	s_setprio 0
	s_barrier
	s_add_i32 s30, s59, s5
	v_lshl_add_u64 v[212:213], v[212:213], 0, s[14:15]
	s_mov_b32 m0, s30
	ds_read_b128 v[180:183], v150 offset:49152
	ds_read_b128 v[184:187], v150 offset:50176
	ds_read_b128 v[188:191], v150 offset:51200
	ds_read_b128 v[192:195], v150 offset:52224
	ds_read_b128 v[196:199], v150 offset:53248
	ds_read_b128 v[200:203], v150 offset:54272
	ds_read_b128 v[204:207], v150 offset:55296
	ds_read_b128 v[208:211], v150 offset:56320
	global_load_lds_dwordx4 v[212:213], off
	s_add_i32 m0, s30, 0x2000
	s_add_u32 s30, s36, 0x58080
	v_lshl_add_u64 v[212:213], v[214:215], 0, s[14:15]
	s_addc_u32 s31, s37, 0
	s_add_i32 s36, s61, s5
	global_load_lds_dwordx4 v[212:213], off
	v_lshl_add_u64 v[212:213], s[30:31], 0, v[134:135]
	s_mov_b32 m0, s36
	s_nop 0
	global_load_lds_dwordx4 v[212:213], off
	v_lshl_add_u64 v[212:213], s[30:31], 0, v[130:131]
	s_add_i32 m0, s36, 0x2000
	s_nop 0
	global_load_lds_dwordx4 v[212:213], off
	v_lshl_add_u64 v[240:241], v[216:217], 0, s[14:15]
	v_lshl_add_u64 v[242:243], v[218:219], 0, s[14:15]
	s_waitcnt vmcnt(6)
	s_waitcnt lgkmcnt(0)
	s_barrier
	s_setprio 1
	s_waitcnt lgkmcnt(0)
	v_mfma_f32_16x16x32_bf16 v[62:65], v[142:145], v[180:183], v[62:65]
	v_mfma_f32_16x16x32_bf16 v[58:61], v[156:159], v[180:183], v[58:61]
	v_mfma_f32_16x16x32_bf16 v[46:49], v[142:145], v[188:191], v[46:49]
	v_mfma_f32_16x16x32_bf16 v[42:45], v[156:159], v[188:191], v[42:45]
	v_mfma_f32_16x16x32_bf16 v[30:33], v[142:145], v[196:199], v[30:33]
	v_mfma_f32_16x16x32_bf16 v[26:29], v[156:159], v[196:199], v[26:29]
	v_mfma_f32_16x16x32_bf16 v[14:17], v[142:145], v[204:207], v[14:17]
	v_mfma_f32_16x16x32_bf16 v[10:13], v[156:159], v[204:207], v[10:13]
	v_mfma_f32_16x16x32_bf16 v[62:65], v[152:155], v[184:187], v[62:65]
	v_mfma_f32_16x16x32_bf16 v[58:61], v[160:163], v[184:187], v[58:61]
	v_mfma_f32_16x16x32_bf16 v[46:49], v[152:155], v[192:195], v[46:49]
	v_mfma_f32_16x16x32_bf16 v[42:45], v[160:163], v[192:195], v[42:45]
	v_mfma_f32_16x16x32_bf16 v[30:33], v[152:155], v[200:203], v[30:33]
	v_mfma_f32_16x16x32_bf16 v[26:29], v[160:163], v[200:203], v[26:29]
	v_mfma_f32_16x16x32_bf16 v[14:17], v[152:155], v[208:211], v[14:17]
	v_mfma_f32_16x16x32_bf16 v[10:13], v[160:163], v[208:211], v[10:13]
	s_setprio 0
	s_setprio 1
	v_mfma_f32_16x16x32_bf16 v[54:57], v[164:167], v[180:183], v[54:57]
	v_mfma_f32_16x16x32_bf16 v[50:53], v[172:175], v[180:183], v[50:53]
	v_mfma_f32_16x16x32_bf16 v[38:41], v[164:167], v[188:191], v[38:41]
	v_mfma_f32_16x16x32_bf16 v[34:37], v[172:175], v[188:191], v[34:37]
	v_mfma_f32_16x16x32_bf16 v[22:25], v[164:167], v[196:199], v[22:25]
	v_mfma_f32_16x16x32_bf16 v[18:21], v[172:175], v[196:199], v[18:21]
	v_mfma_f32_16x16x32_bf16 v[6:9], v[164:167], v[204:207], v[6:9]
	v_mfma_f32_16x16x32_bf16 v[2:5], v[172:175], v[204:207], v[2:5]
	v_mfma_f32_16x16x32_bf16 v[54:57], v[168:171], v[184:187], v[54:57]
	v_mfma_f32_16x16x32_bf16 v[50:53], v[176:179], v[184:187], v[50:53]
	v_mfma_f32_16x16x32_bf16 v[38:41], v[168:171], v[192:195], v[38:41]
	v_mfma_f32_16x16x32_bf16 v[34:37], v[176:179], v[192:195], v[34:37]
	v_mfma_f32_16x16x32_bf16 v[22:25], v[168:171], v[200:203], v[22:25]
	v_mfma_f32_16x16x32_bf16 v[18:21], v[176:179], v[200:203], v[18:21]
	v_mfma_f32_16x16x32_bf16 v[6:9], v[168:171], v[208:211], v[6:9]
	v_mfma_f32_16x16x32_bf16 v[2:5], v[176:179], v[208:211], v[2:5]
	s_setprio 0
	s_barrier
	s_mov_b32 s99, 1
	s_add_i32 s58, s58, 2
	s_add_u32 s56, s56, 0x100
	s_addc_u32 s57, s57, 0
	s_cmp_gt_u32 s58, 19
	s_mov_b64 s[30:31], s[34:35]
	s_cbranch_scc0 .LBB0_2228
	s_and_b64 vcc, exec, s[16:17]
	s_cbranch_vccz .LBB0_2231
	s_barrier

	.amdhsa_kernel _Z10fwd_kernel4Args
		.amdhsa_group_segment_fixed_size 0
		.amdhsa_private_segment_fixed_size 0
		.amdhsa_kernarg_size 480
		.amdhsa_user_sgpr_count 2
		.amdhsa_user_sgpr_dispatch_ptr 0
		.amdhsa_user_sgpr_queue_ptr 0
		.amdhsa_user_sgpr_kernarg_segment_ptr 1
		.amdhsa_user_sgpr_dispatch_id 0
		.amdhsa_user_sgpr_kernarg_preload_length 0
		.amdhsa_user_sgpr_kernarg_preload_offset 0
		.amdhsa_user_sgpr_private_segment_size 0
		.amdhsa_uses_dynamic_stack 0
		.amdhsa_enable_private_segment 0
		.amdhsa_system_sgpr_workgroup_id_x 1
		.amdhsa_system_sgpr_workgroup_id_y 0
		.amdhsa_system_sgpr_workgroup_id_z 0
		.amdhsa_system_sgpr_workgroup_info 0
		.amdhsa_system_vgpr_workitem_id 0
		.amdhsa_next_free_vgpr 254
		.amdhsa_next_free_sgpr 102
		.amdhsa_accum_offset 256
		.amdhsa_reserve_vcc 1
		.amdhsa_float_round_mode_32 0
		.amdhsa_float_round_mode_16_64 0
		.amdhsa_float_denorm_mode_32 3
		.amdhsa_float_denorm_mode_16_64 3
		.amdhsa_dx10_clamp 1
		.amdhsa_ieee_mode 1
		.amdhsa_fp16_overflow 0
		.amdhsa_tg_split 0
		.amdhsa_exception_fp_ieee_invalid_op 0
		.amdhsa_exception_fp_denorm_src 0
		.amdhsa_exception_fp_ieee_div_zero 0
		.amdhsa_exception_fp_ieee_overflow 0
		.amdhsa_exception_fp_ieee_underflow 0
		.amdhsa_exception_fp_ieee_inexact 0
		.amdhsa_exception_int_div_zero 0
	.end_amdhsa_kernel

amdhsa.kernels:
  - .agpr_count:     0
    .args:
      - .offset:         0
        .size:           224
        .value_kind:     by_value
      - .offset:         224
        .size:           4
        .value_kind:     hidden_block_count_x
      - .offset:         228
        .size:           4
        .value_kind:     hidden_block_count_y
      - .offset:         232
        .size:           4
        .value_kind:     hidden_block_count_z
      - .offset:         236
        .size:           2
        .value_kind:     hidden_group_size_x
      - .offset:         238
        .size:           2
        .value_kind:     hidden_group_size_y
      - .offset:         240
        .size:           2
        .value_kind:     hidden_group_size_z
      - .offset:         242
        .size:           2
        .value_kind:     hidden_remainder_x
      - .offset:         244
        .size:           2
        .value_kind:     hidden_remainder_y
      - .offset:         246
        .size:           2
        .value_kind:     hidden_remainder_z
      - .offset:         264
        .size:           8
        .value_kind:     hidden_global_offset_x
      - .offset:         272
        .size:           8
        .value_kind:     hidden_global_offset_y
      - .offset:         280
        .size:           8
        .value_kind:     hidden_global_offset_z
      - .offset:         288
        .size:           2
        .value_kind:     hidden_grid_dims
      - .offset:         344
        .size:           4
        .value_kind:     hidden_dynamic_lds_size
    .group_segment_fixed_size: 0
    .kernarg_segment_align: 8
    .kernarg_segment_size: 480
    .language:       OpenCL C
    .language_version:
      - 2
      - 0
    .max_flat_workgroup_size: 512
    .name:           _Z10fwd_kernel4Args
    .private_segment_fixed_size: 0
    .sgpr_count:     108
    .sgpr_spill_count: 23
    .symbol:         _Z10fwd_kernel4Args.kd
    .uniform_work_group_size: 1
    .uses_dynamic_stack: false
    .vgpr_count:     254
    .vgpr_spill_count: 0
    .wavefront_size: 64
